# P2 EpiProj epilogue specialised per class-flag combination (straight-line traces, dead flag bookkeeping removed, trans wait states filled by neighbouring elements) on top of p7b_epi ga168 p8_atom acc0
# baseline (speedup 1.0000x reference)
; #define LAS __attribute__((address_space(3)))
;     DI void operator()(const f32x4 (&acc)[2][2][4][2], const Unit& u, int wr, int wc, int fr, int fq, const LAS unsigned char* slot) const {
;     ...
;         const int row0 = u.pm * BM + wr * 64 + fr + zz, cin0 = u.pn * BM + wc * 32 + 8 * fq - cbase;
;         bf16* base = P + po;
;         float rsv[2][4];
; #pragma unroll
;         for (int ai = 0; ai < 2; ++ai)
; #pragma unroll
;             for (int m = 0; m < 4; ++m) rsv[ai][m] = *(const LAS float*)(slot + 4 * (ai * HALF + wr * 64 + m * 16 + fr));
; #pragma unroll
;         for (int bj = 0; bj < 2; ++bj) {
;             float lbv[8];
;             const int cin = cin0 + bj * HALF;
;             { const int lc = bj * HALF + wc * 32 + 8 * fq; const f32x4 a = *(const LAS f32x4*)(slot + 2048 + 4 * lc), b = *(const LAS f32x4*)(slot + 2048 + 4 * lc + 16);
; #pragma unroll
;               for (int j = 0; j < 4; ++j) { lbv[j] = (cls == 2) ? a[j] : 0.f; lbv[4 + j] = (cls == 2) ? b[j] : 0.f; } }
;             bf16* colp = base + (size_t)(cin >> hs) * MROWS * pitch + (cin & ((1 << hs) - 1));
;             float csv[8];
;             { const int lc = bj * HALF + wc * 32 + 8 * fq; const f32x4 a = *(const LAS f32x4*)(slot + 1024 + 4 * lc), b = *(const LAS f32x4*)(slot + 1024 + 4 * lc + 16);
; #pragma unroll
;               for (int j = 0; j < 4; ++j) { csv[j] = a[j]; csv[4 + j] = b[j]; }
;               if (cls >= 2) {
; #pragma unroll
;                   for (int j = 0; j < 8; ++j) csv[j] *= -1.4426950408889634f; } }
; #pragma unroll
;             for (int ai = 0; ai < 2; ++ai)
; #pragma unroll
;                 for (int m = 0; m < 4; ++m) { const int rr = row0 + ai * HALF + m * 16; const size_t ro = (size_t)rr * pitch; float v[8]; const float rs = rsv[ai][m];
; #pragma unroll
;                     for (int j = 0; j < 8; ++j) v[j] = (float)__builtin_bit_cast(i32x4, acc[ai][bj][m][j >> 2])[j & 3] * (rs * csv[j]);
;                     if (cls != 0) {
; #pragma unroll
;                         for (int j = 0; j < 8; ++j) { if (cls == 1) v[j] *= sigmoidf_(v[j]); else v[j] = __builtin_amdgcn_rcpf(1.0f + __builtin_amdgcn_exp2f(v[j])); }
;                         if (cls == 2) {
; #pragma unroll
;                             for (int j = 0; j < 8; ++j) { const float l = lbv[j]; v[j] = __builtin_amdgcn_logf(l + (1.0f - l) * v[j]); } }
;                     }
.LBB0_506:
	s_cmp_lg_u64 s[34:35], 0
	s_cbranch_scc1 .Lepj_A
	s_cmp_lg_u64 s[44:45], 0
	s_cbranch_scc1 .Lepj_B
	s_cmp_lg_u64 s[30:31], 0
	s_cbranch_scc1 .Lepj_C
	s_lshl_b32 s37, s90, 12
	s_and_b32 s37, s37, 0x1000
	s_add_i32 s37, s37, 0
	s_add_i32 s37, s37, 0x21000
	v_mov_b32_e32 v150, v151
	v_add_u32_e32 v14, s37, v182
	v_add_u32_e32 v195, s37, v185
	ds_read2_b32 v[168:169], v14 offset1:16
	ds_read2_b32 v[160:161], v14 offset0:32 offset1:48
	ds_read2_b32 v[158:159], v14 offset0:128 offset1:144
	ds_read_b128 v[10:13], v195 offset:1024
	ds_read2_b32 v[156:157], v14 offset0:160 offset1:176
	ds_read_b128 v[14:17], v195 offset:1040
	ds_read_b128 v[106:109], v195 offset:2048
	ds_read_b128 v[98:101], v195 offset:2064
	v_cvt_f32_i32_e32 v3, v3
	v_cvt_f32_i32_e32 v2, v2
	s_waitcnt lgkmcnt(0)
	v_pk_mul_f32 v[170:171], v[10:11], s[26:27] op_sel_hi:[1,0]
	v_cvt_f32_i32_e32 v5, v5
	v_cvt_f32_i32_e32 v4, v4
	v_pk_mul_f32 v[176:177], v[12:13], s[26:27] op_sel_hi:[1,0]
	v_cndmask_b32_e64 v179, v11, v171, s[38:39]
	v_cndmask_b32_e64 v178, v10, v170, s[38:39]
	v_cvt_f32_i32_e32 v7, v7
	v_cvt_f32_i32_e32 v6, v6
	v_pk_mul_f32 v[174:175], v[14:15], s[26:27] op_sel_hi:[1,0]
	v_cndmask_b32_e64 v177, v13, v177, s[38:39]
	v_cndmask_b32_e64 v176, v12, v176, s[38:39]
	v_pk_mul_f32 v[10:11], v[168:169], v[178:179] op_sel_hi:[0,1]
	v_cvt_f32_i32_e32 v9, v9
	v_cvt_f32_i32_e32 v8, v8
	v_pk_mul_f32 v[172:173], v[16:17], s[26:27] op_sel_hi:[1,0]
	v_cndmask_b32_e64 v175, v15, v175, s[38:39]
	v_cndmask_b32_e64 v174, v14, v174, s[38:39]
	v_pk_mul_f32 v[2:3], v[10:11], v[2:3]
	v_pk_mul_f32 v[10:11], v[168:169], v[176:177] op_sel_hi:[0,1]
	v_cndmask_b32_e64 v173, v17, v173, s[38:39]
	v_cndmask_b32_e64 v172, v16, v172, s[38:39]
	v_pk_mul_f32 v[4:5], v[10:11], v[4:5]
	v_pk_mul_f32 v[10:11], v[168:169], v[174:175] op_sel_hi:[0,1]
	v_pk_mul_f32 v[6:7], v[10:11], v[6:7]
	v_pk_mul_f32 v[10:11], v[168:169], v[172:173] op_sel_hi:[0,1]
	v_pk_mul_f32 v[8:9], v[10:11], v[8:9]
	v_exp_f32_e32 v10, v2
	v_exp_f32_e32 v11, v3
	v_add_f32_e32 v10, 1.0, v10
	v_rcp_f32_e32 v10, v10
	v_add_f32_e32 v11, 1.0, v11
	v_rcp_f32_e32 v11, v11
	v_exp_f32_e32 v12, v4
	v_exp_f32_e32 v13, v5
	v_add_f32_e32 v12, 1.0, v12
	v_rcp_f32_e32 v12, v12
	v_add_f32_e32 v13, 1.0, v13
	v_rcp_f32_e32 v13, v13
	v_exp_f32_e32 v14, v6
	v_exp_f32_e32 v15, v7
	v_add_f32_e32 v14, 1.0, v14
	v_rcp_f32_e32 v14, v14
	v_add_f32_e32 v15, 1.0, v15
	v_rcp_f32_e32 v15, v15
	v_exp_f32_e32 v16, v8
	v_exp_f32_e32 v17, v9
	v_add_f32_e32 v16, 1.0, v16
	v_rcp_f32_e32 v16, v16
	v_add_f32_e32 v17, 1.0, v17
	v_rcp_f32_e32 v17, v17
	v_lshl_or_b32 v2, s95, 8, v184
	s_lshl_b32 s6, s94, 8
	v_add_u32_e32 v196, s3, v2
	s_lshl_b32 s3, s42, 1
	s_add_u32 s42, s76, s3
	s_addc_u32 s43, s77, 0
	s_mul_i32 s94, s36, 0x4100
	s_lshl_b32 s95, -1, s93
	v_ashrrev_i32_e32 v2, s93, v196
	v_add3_u32 v197, s6, v167, v150
	v_mad_i64_i32 v[2:3], s[6:7], s94, v2, 0
	v_bitop3_b32 v4, v196, s95, v196 bitop3:0x30
	v_lshl_add_u64 v[2:3], v[2:3], 1, s[42:43]
	v_lshlrev_b32_e32 v150, 1, v4
	v_lshl_add_u64 v[180:181], v[2:3], 0, v[150:151]
	v_mad_i64_i32 v[170:171], s[6:7], s36, v197, 0
	v_cvt_pk_bf16_f32 v2, v10, v11
	v_cvt_pk_bf16_f32 v3, v12, v13
	v_cvt_pk_bf16_f32 v4, v14, v15
	v_cvt_pk_bf16_f32 v5, v16, v17
	v_lshl_add_u64 v[6:7], v[170:171], 1, v[180:181]
	global_store_dwordx4 v[6:7], v[2:5], off
	v_mov_b32_e32 v8, v169
	v_pk_mul_f32 v[6:7], v[8:9], v[178:179] op_sel_hi:[0,1]
	v_cvt_f32_i32_e32 v3, v143
	v_cvt_f32_i32_e32 v2, v142
	v_cvt_f32_i32_e32 v5, v145
	v_cvt_f32_i32_e32 v4, v144
	v_cvt_f32_i32_e32 v11, v141
	v_pk_mul_f32 v[2:3], v[6:7], v[2:3]
	v_pk_mul_f32 v[6:7], v[8:9], v[176:177] op_sel_hi:[0,1]
	v_cvt_f32_i32_e32 v10, v140
	v_pk_mul_f32 v[4:5], v[6:7], v[4:5]
	v_cvt_f32_i32_e32 v7, v139
	v_cvt_f32_i32_e32 v6, v138
	v_pk_mul_f32 v[12:13], v[8:9], v[174:175] op_sel_hi:[0,1]
	v_pk_mul_f32 v[8:9], v[8:9], v[172:173] op_sel_hi:[0,1]
	v_pk_mul_f32 v[8:9], v[8:9], v[10:11]
	v_pk_mul_f32 v[6:7], v[12:13], v[6:7]
	v_exp_f32_e32 v10, v2
	v_exp_f32_e32 v11, v3
	v_add_f32_e32 v10, 1.0, v10
	v_rcp_f32_e32 v10, v10
	v_add_f32_e32 v11, 1.0, v11
	v_rcp_f32_e32 v11, v11
	v_exp_f32_e32 v12, v4
	v_exp_f32_e32 v13, v5
	v_add_f32_e32 v12, 1.0, v12
	v_rcp_f32_e32 v12, v12
	v_add_f32_e32 v13, 1.0, v13
	v_rcp_f32_e32 v13, v13
	v_exp_f32_e32 v14, v6
	v_exp_f32_e32 v15, v7
	v_add_f32_e32 v14, 1.0, v14
	v_rcp_f32_e32 v14, v14
	v_add_f32_e32 v15, 1.0, v15
	v_rcp_f32_e32 v15, v15
	v_exp_f32_e32 v16, v8
	v_exp_f32_e32 v17, v9
	v_add_f32_e32 v16, 1.0, v16
	v_rcp_f32_e32 v16, v16
	v_add_f32_e32 v17, 1.0, v17
	v_rcp_f32_e32 v17, v17
	s_mov_b64 s[62:63], 0
	v_add_u32_e32 v2, 16, v197
	v_mad_i64_i32 v[138:139], s[44:45], s36, v2, 0
	v_cvt_pk_bf16_f32 v2, v10, v11
	v_cvt_pk_bf16_f32 v3, v12, v13
	v_cvt_pk_bf16_f32 v4, v14, v15
	v_cvt_pk_bf16_f32 v5, v16, v17
	v_lshl_add_u64 v[6:7], v[138:139], 1, v[180:181]
	global_store_dwordx4 v[6:7], v[2:5], off
	v_pk_mul_f32 v[6:7], v[160:161], v[178:179] op_sel_hi:[0,1]
	v_cvt_f32_i32_e32 v9, v133
	v_cvt_f32_i32_e32 v3, v135
	v_cvt_f32_i32_e32 v2, v134
	v_cvt_f32_i32_e32 v5, v137
	v_cvt_f32_i32_e32 v4, v136
	v_cvt_f32_i32_e32 v8, v132
	v_pk_mul_f32 v[2:3], v[6:7], v[2:3]
	v_pk_mul_f32 v[6:7], v[160:161], v[176:177] op_sel_hi:[0,1]
	v_pk_mul_f32 v[4:5], v[6:7], v[4:5]
	v_cvt_f32_i32_e32 v7, v131
	v_cvt_f32_i32_e32 v6, v130
	v_pk_mul_f32 v[10:11], v[160:161], v[174:175] op_sel_hi:[0,1]
	v_pk_mul_f32 v[6:7], v[10:11], v[6:7]
	v_pk_mul_f32 v[10:11], v[160:161], v[172:173] op_sel_hi:[0,1]
	v_pk_mul_f32 v[8:9], v[10:11], v[8:9]
	v_exp_f32_e32 v10, v2
	v_exp_f32_e32 v11, v3
	v_add_f32_e32 v10, 1.0, v10
	v_rcp_f32_e32 v10, v10
	v_add_f32_e32 v11, 1.0, v11
; DI unsigned pk2(float lo, float hi) { f32x2 v = {lo, hi}; bf16x2_t b = __builtin_convertvector(v, bf16x2_t); return __builtin_bit_cast(unsigned, b); }
; DI float sigmoidf_(float x) { return __builtin_amdgcn_rcpf(1.0f + __expf(-x)); }
;     DI void operator()(const f32x4 (&acc)[2][2][4][2], const Unit& u, int wr, int wc, int fr, int fq, const LAS unsigned char* slot) const {
;     ...
;             for (int ai = 0; ai < 2; ++ai)
; #pragma unroll
;                 for (int m = 0; m < 4; ++m) { const int rr = row0 + ai * HALF + m * 16; const size_t ro = (size_t)rr * pitch; float v[8]; const float rs = rsv[ai][m];
; #pragma unroll
;                     for (int j = 0; j < 8; ++j) v[j] = (float)__builtin_bit_cast(i32x4, acc[ai][bj][m][j >> 2])[j & 3] * (rs * csv[j]);
;                     if (cls != 0) {
; #pragma unroll
;                         for (int j = 0; j < 8; ++j) { if (cls == 1) v[j] *= sigmoidf_(v[j]); else v[j] = __builtin_amdgcn_rcpf(1.0f + __builtin_amdgcn_exp2f(v[j])); }
;                         if (cls == 2) {
; #pragma unroll
;                             for (int j = 0; j < 8; ++j) { const float l = lbv[j]; v[j] = __builtin_amdgcn_logf(l + (1.0f - l) * v[j]); } }
;                     }
;                     u32x4 w; w.x = pk2(v[0], v[1]); w.y = pk2(v[2], v[3]); w.z = pk2(v[4], v[5]); w.w = pk2(v[6], v[7]);
;                     *(u32x4*)(colp + ro) = w; }
	v_rcp_f32_e32 v11, v11
	v_exp_f32_e32 v12, v4
	v_exp_f32_e32 v13, v5
	v_add_f32_e32 v12, 1.0, v12
	v_rcp_f32_e32 v12, v12
	v_add_f32_e32 v13, 1.0, v13
	v_rcp_f32_e32 v13, v13
	v_exp_f32_e32 v14, v6
	v_exp_f32_e32 v15, v7
	v_add_f32_e32 v14, 1.0, v14
	v_rcp_f32_e32 v14, v14
	v_add_f32_e32 v15, 1.0, v15
	v_rcp_f32_e32 v15, v15
	v_exp_f32_e32 v16, v8
	v_exp_f32_e32 v17, v9
	v_add_f32_e32 v16, 1.0, v16
	v_rcp_f32_e32 v16, v16
	v_add_f32_e32 v17, 1.0, v17
	v_rcp_f32_e32 v17, v17
	v_add_u32_e32 v2, 32, v197
	v_mad_i64_i32 v[130:131], s[44:45], s36, v2, 0
	v_cvt_pk_bf16_f32 v2, v10, v11
	v_cvt_pk_bf16_f32 v3, v12, v13
	v_cvt_pk_bf16_f32 v4, v14, v15
	v_cvt_pk_bf16_f32 v5, v16, v17
	v_lshl_add_u64 v[6:7], v[130:131], 1, v[180:181]
	global_store_dwordx4 v[6:7], v[2:5], off
	v_mov_b32_e32 v8, v161
	v_pk_mul_f32 v[6:7], v[8:9], v[178:179] op_sel_hi:[0,1]
	v_cvt_f32_i32_e32 v3, v127
	v_cvt_f32_i32_e32 v2, v126
	v_cvt_f32_i32_e32 v5, v129
	v_cvt_f32_i32_e32 v4, v128
	v_cvt_f32_i32_e32 v11, v125
	v_pk_mul_f32 v[2:3], v[6:7], v[2:3]
	v_pk_mul_f32 v[6:7], v[8:9], v[176:177] op_sel_hi:[0,1]
	v_pk_mul_f32 v[4:5], v[6:7], v[4:5]
	v_cvt_f32_i32_e32 v7, v123
	v_cvt_f32_i32_e32 v6, v122
	v_cvt_f32_i32_e32 v10, v124
	v_pk_mul_f32 v[12:13], v[8:9], v[174:175] op_sel_hi:[0,1]
	v_pk_mul_f32 v[8:9], v[8:9], v[172:173] op_sel_hi:[0,1]
	v_pk_mul_f32 v[6:7], v[12:13], v[6:7]
	v_pk_mul_f32 v[8:9], v[8:9], v[10:11]
	v_exp_f32_e32 v10, v2
	v_exp_f32_e32 v11, v3
	v_add_f32_e32 v10, 1.0, v10
	v_rcp_f32_e32 v10, v10
	v_add_f32_e32 v11, 1.0, v11
	v_rcp_f32_e32 v11, v11
	v_exp_f32_e32 v12, v4
	v_exp_f32_e32 v13, v5
	v_add_f32_e32 v12, 1.0, v12
	v_rcp_f32_e32 v12, v12
	v_add_f32_e32 v13, 1.0, v13
	v_rcp_f32_e32 v13, v13
	v_exp_f32_e32 v14, v6
	v_exp_f32_e32 v15, v7
	v_add_f32_e32 v14, 1.0, v14
	v_rcp_f32_e32 v14, v14
	v_add_f32_e32 v15, 1.0, v15
	v_rcp_f32_e32 v15, v15
	v_exp_f32_e32 v16, v8
	v_exp_f32_e32 v17, v9
	v_add_f32_e32 v16, 1.0, v16
	v_rcp_f32_e32 v16, v16
	v_add_f32_e32 v17, 1.0, v17
	v_rcp_f32_e32 v17, v17
	v_add_u32_e32 v2, 48, v197
	v_mad_i64_i32 v[122:123], s[44:45], s36, v2, 0
	v_cvt_pk_bf16_f32 v2, v10, v11
	v_cvt_pk_bf16_f32 v3, v12, v13
	v_cvt_pk_bf16_f32 v4, v14, v15
	v_cvt_pk_bf16_f32 v5, v16, v17
	v_lshl_add_u64 v[6:7], v[122:123], 1, v[180:181]
	global_store_dwordx4 v[6:7], v[2:5], off
	v_pk_mul_f32 v[6:7], v[158:159], v[178:179] op_sel_hi:[0,1]
	v_cvt_f32_i32_e32 v9, v117
	v_cvt_f32_i32_e32 v3, v119
	v_cvt_f32_i32_e32 v2, v118
	v_cvt_f32_i32_e32 v5, v121
	v_cvt_f32_i32_e32 v4, v120
	v_cvt_f32_i32_e32 v8, v116
	v_pk_mul_f32 v[2:3], v[6:7], v[2:3]
	v_pk_mul_f32 v[6:7], v[158:159], v[176:177] op_sel_hi:[0,1]
	v_pk_mul_f32 v[4:5], v[6:7], v[4:5]
	v_cvt_f32_i32_e32 v7, v115
	v_cvt_f32_i32_e32 v6, v114
	v_pk_mul_f32 v[10:11], v[158:159], v[174:175] op_sel_hi:[0,1]
	v_pk_mul_f32 v[6:7], v[10:11], v[6:7]
	v_pk_mul_f32 v[10:11], v[158:159], v[172:173] op_sel_hi:[0,1]
	v_pk_mul_f32 v[8:9], v[10:11], v[8:9]
	v_exp_f32_e32 v10, v2
	v_exp_f32_e32 v11, v3
	v_add_f32_e32 v10, 1.0, v10
	v_rcp_f32_e32 v10, v10
	v_add_f32_e32 v11, 1.0, v11
	v_rcp_f32_e32 v11, v11
	v_exp_f32_e32 v12, v4
	v_exp_f32_e32 v13, v5
	v_add_f32_e32 v12, 1.0, v12
	v_rcp_f32_e32 v12, v12
	v_add_f32_e32 v13, 1.0, v13
	v_rcp_f32_e32 v13, v13
	v_exp_f32_e32 v14, v6
	v_exp_f32_e32 v15, v7
	v_add_f32_e32 v14, 1.0, v14
	v_rcp_f32_e32 v14, v14
	v_add_f32_e32 v15, 1.0, v15
	v_rcp_f32_e32 v15, v15
	v_exp_f32_e32 v16, v8
	v_exp_f32_e32 v17, v9
	v_add_f32_e32 v16, 1.0, v16
	v_rcp_f32_e32 v16, v16
	v_add_f32_e32 v17, 1.0, v17
	v_rcp_f32_e32 v17, v17
	v_add_u32_e32 v2, 0x80, v197
	v_mad_i64_i32 v[114:115], s[44:45], s36, v2, 0
	v_cvt_pk_bf16_f32 v2, v10, v11
	v_cvt_pk_bf16_f32 v3, v12, v13
	v_cvt_pk_bf16_f32 v4, v14, v15
	v_cvt_pk_bf16_f32 v5, v16, v17
	v_lshl_add_u64 v[6:7], v[114:115], 1, v[180:181]
	global_store_dwordx4 v[6:7], v[2:5], off
	v_mov_b32_e32 v8, v159
	v_pk_mul_f32 v[6:7], v[8:9], v[178:179] op_sel_hi:[0,1]
	v_cvt_f32_i32_e32 v3, v111
	v_cvt_f32_i32_e32 v2, v110
	v_cvt_f32_i32_e32 v5, v113
	v_cvt_f32_i32_e32 v4, v112
	v_cvt_f32_i32_e32 v11, v105
	v_pk_mul_f32 v[2:3], v[6:7], v[2:3]
	v_pk_mul_f32 v[6:7], v[8:9], v[176:177] op_sel_hi:[0,1]
	v_pk_mul_f32 v[4:5], v[6:7], v[4:5]
	v_cvt_f32_i32_e32 v7, v103
	v_cvt_f32_i32_e32 v6, v102
	v_cvt_f32_i32_e32 v10, v104
	v_pk_mul_f32 v[12:13], v[8:9], v[174:175] op_sel_hi:[0,1]
	v_pk_mul_f32 v[8:9], v[8:9], v[172:173] op_sel_hi:[0,1]
	v_pk_mul_f32 v[6:7], v[12:13], v[6:7]
	v_pk_mul_f32 v[8:9], v[8:9], v[10:11]
	v_exp_f32_e32 v10, v2
	v_exp_f32_e32 v11, v3
	v_add_f32_e32 v10, 1.0, v10
	v_rcp_f32_e32 v10, v10
	v_add_f32_e32 v11, 1.0, v11
	v_rcp_f32_e32 v11, v11
	v_exp_f32_e32 v12, v4
	v_exp_f32_e32 v13, v5
	v_add_f32_e32 v12, 1.0, v12
	v_rcp_f32_e32 v12, v12
	v_add_f32_e32 v13, 1.0, v13
	v_rcp_f32_e32 v13, v13
	v_exp_f32_e32 v14, v6
	v_exp_f32_e32 v15, v7
	v_add_f32_e32 v14, 1.0, v14
	v_rcp_f32_e32 v14, v14
	v_add_f32_e32 v15, 1.0, v15
	v_rcp_f32_e32 v15, v15
	v_exp_f32_e32 v16, v8
	v_exp_f32_e32 v17, v9
	v_add_f32_e32 v16, 1.0, v16
	v_rcp_f32_e32 v16, v16
	v_add_f32_e32 v17, 1.0, v17
	v_rcp_f32_e32 v17, v17
	v_add_u32_e32 v2, 0x90, v197
	v_mad_i64_i32 v[102:103], s[44:45], s36, v2, 0
	v_cvt_pk_bf16_f32 v2, v10, v11
	v_cvt_pk_bf16_f32 v3, v12, v13
	v_cvt_pk_bf16_f32 v4, v14, v15
	v_cvt_pk_bf16_f32 v5, v16, v17
	v_lshl_add_u64 v[6:7], v[102:103], 1, v[180:181]
	global_store_dwordx4 v[6:7], v[2:5], off
	v_pk_mul_f32 v[6:7], v[156:157], v[178:179] op_sel_hi:[0,1]
	v_cvt_f32_i32_e32 v9, v93
	v_cvt_f32_i32_e32 v3, v95
	v_cvt_f32_i32_e32 v2, v94
	v_cvt_f32_i32_e32 v5, v97
	v_cvt_f32_i32_e32 v4, v96
	v_cvt_f32_i32_e32 v8, v92
	v_pk_mul_f32 v[2:3], v[6:7], v[2:3]
; #define LAS __attribute__((address_space(3)))
; DI unsigned pk2(float lo, float hi) { f32x2 v = {lo, hi}; bf16x2_t b = __builtin_convertvector(v, bf16x2_t); return __builtin_bit_cast(unsigned, b); }
;     DI void operator()(const f32x4 (&acc)[2][2][4][2], const Unit& u, int wr, int wc, int fr, int fq, const LAS unsigned char* slot) const {
;     ...
;         for (int bj = 0; bj < 2; ++bj) {
;             float lbv[8];
;             const int cin = cin0 + bj * HALF;
;             { const int lc = bj * HALF + wc * 32 + 8 * fq; const f32x4 a = *(const LAS f32x4*)(slot + 2048 + 4 * lc), b = *(const LAS f32x4*)(slot + 2048 + 4 * lc + 16);
; #pragma unroll
;               for (int j = 0; j < 4; ++j) { lbv[j] = (cls == 2) ? a[j] : 0.f; lbv[4 + j] = (cls == 2) ? b[j] : 0.f; } }
;             bf16* colp = base + (size_t)(cin >> hs) * MROWS * pitch + (cin & ((1 << hs) - 1));
;             float csv[8];
;             { const int lc = bj * HALF + wc * 32 + 8 * fq; const f32x4 a = *(const LAS f32x4*)(slot + 1024 + 4 * lc), b = *(const LAS f32x4*)(slot + 1024 + 4 * lc + 16);
; #pragma unroll
;               for (int j = 0; j < 4; ++j) { csv[j] = a[j]; csv[4 + j] = b[j]; }
;               if (cls >= 2) {
; #pragma unroll
;                   for (int j = 0; j < 8; ++j) csv[j] *= -1.4426950408889634f; } }
; #pragma unroll
;             for (int ai = 0; ai < 2; ++ai)
; #pragma unroll
;                 for (int m = 0; m < 4; ++m) { const int rr = row0 + ai * HALF + m * 16; const size_t ro = (size_t)rr * pitch; float v[8]; const float rs = rsv[ai][m];
; #pragma unroll
;                     for (int j = 0; j < 8; ++j) v[j] = (float)__builtin_bit_cast(i32x4, acc[ai][bj][m][j >> 2])[j & 3] * (rs * csv[j]);
;                     if (cls != 0) {
; #pragma unroll
;                         for (int j = 0; j < 8; ++j) { if (cls == 1) v[j] *= sigmoidf_(v[j]); else v[j] = __builtin_amdgcn_rcpf(1.0f + __builtin_amdgcn_exp2f(v[j])); }
;                         if (cls == 2) {
; #pragma unroll
;                             for (int j = 0; j < 8; ++j) { const float l = lbv[j]; v[j] = __builtin_amdgcn_logf(l + (1.0f - l) * v[j]); } }
;                     }
;                     u32x4 w; w.x = pk2(v[0], v[1]); w.y = pk2(v[2], v[3]); w.z = pk2(v[4], v[5]); w.w = pk2(v[6], v[7]);
;                     *(u32x4*)(colp + ro) = w; }
	v_pk_mul_f32 v[6:7], v[156:157], v[176:177] op_sel_hi:[0,1]
	v_pk_mul_f32 v[4:5], v[6:7], v[4:5]
	v_cvt_f32_i32_e32 v7, v91
	v_cvt_f32_i32_e32 v6, v90
	v_pk_mul_f32 v[10:11], v[156:157], v[174:175] op_sel_hi:[0,1]
	v_pk_mul_f32 v[6:7], v[10:11], v[6:7]
	v_pk_mul_f32 v[10:11], v[156:157], v[172:173] op_sel_hi:[0,1]
	v_pk_mul_f32 v[8:9], v[10:11], v[8:9]
	v_exp_f32_e32 v10, v2
	v_exp_f32_e32 v11, v3
	v_add_f32_e32 v10, 1.0, v10
	v_rcp_f32_e32 v10, v10
	v_add_f32_e32 v11, 1.0, v11
	v_rcp_f32_e32 v11, v11
	v_exp_f32_e32 v12, v4
	v_exp_f32_e32 v13, v5
	v_add_f32_e32 v12, 1.0, v12
	v_rcp_f32_e32 v12, v12
	v_add_f32_e32 v13, 1.0, v13
	v_rcp_f32_e32 v13, v13
	v_exp_f32_e32 v14, v6
	v_exp_f32_e32 v15, v7
	v_add_f32_e32 v14, 1.0, v14
	v_rcp_f32_e32 v14, v14
	v_add_f32_e32 v15, 1.0, v15
	v_rcp_f32_e32 v15, v15
	v_exp_f32_e32 v16, v8
	v_exp_f32_e32 v17, v9
	v_add_f32_e32 v16, 1.0, v16
	v_rcp_f32_e32 v16, v16
	v_add_f32_e32 v17, 1.0, v17
	v_rcp_f32_e32 v17, v17
	v_add_u32_e32 v2, 0xa0, v197
	v_mad_i64_i32 v[90:91], s[44:45], s36, v2, 0
	v_cvt_pk_bf16_f32 v2, v10, v11
	v_cvt_pk_bf16_f32 v3, v12, v13
	v_cvt_pk_bf16_f32 v4, v14, v15
	v_cvt_pk_bf16_f32 v5, v16, v17
	v_lshl_add_u64 v[6:7], v[90:91], 1, v[180:181]
	global_store_dwordx4 v[6:7], v[2:5], off
	v_mov_b32_e32 v8, v157
	v_pk_mul_f32 v[6:7], v[8:9], v[178:179] op_sel_hi:[0,1]
	v_cvt_f32_i32_e32 v3, v87
	v_cvt_f32_i32_e32 v2, v86
	v_cvt_f32_i32_e32 v5, v89
	v_cvt_f32_i32_e32 v4, v88
	v_cvt_f32_i32_e32 v11, v85
	v_pk_mul_f32 v[2:3], v[6:7], v[2:3]
	v_pk_mul_f32 v[6:7], v[8:9], v[176:177] op_sel_hi:[0,1]
	v_pk_mul_f32 v[4:5], v[6:7], v[4:5]
	v_cvt_f32_i32_e32 v7, v83
	v_cvt_f32_i32_e32 v6, v82
	v_cvt_f32_i32_e32 v10, v84
	v_pk_mul_f32 v[12:13], v[8:9], v[174:175] op_sel_hi:[0,1]
	v_pk_mul_f32 v[8:9], v[8:9], v[172:173] op_sel_hi:[0,1]
	v_pk_mul_f32 v[6:7], v[12:13], v[6:7]
	v_pk_mul_f32 v[8:9], v[8:9], v[10:11]
	v_exp_f32_e32 v10, v2
	v_exp_f32_e32 v11, v3
	v_add_f32_e32 v10, 1.0, v10
	v_rcp_f32_e32 v10, v10
	v_add_f32_e32 v11, 1.0, v11
	v_rcp_f32_e32 v11, v11
	v_exp_f32_e32 v12, v4
	v_exp_f32_e32 v13, v5
	v_add_f32_e32 v12, 1.0, v12
	v_rcp_f32_e32 v12, v12
	v_add_f32_e32 v13, 1.0, v13
	v_rcp_f32_e32 v13, v13
	v_exp_f32_e32 v14, v6
	v_exp_f32_e32 v15, v7
	v_add_f32_e32 v14, 1.0, v14
	v_rcp_f32_e32 v14, v14
	v_add_f32_e32 v15, 1.0, v15
	v_rcp_f32_e32 v15, v15
	v_exp_f32_e32 v16, v8
	v_exp_f32_e32 v17, v9
	v_add_f32_e32 v16, 1.0, v16
	v_rcp_f32_e32 v16, v16
	v_add_f32_e32 v17, 1.0, v17
	v_rcp_f32_e32 v17, v17
	s_mov_b64 s[44:45], 0
	v_add_u32_e32 v2, 0xb0, v197
	v_mad_i64_i32 v[92:93], s[36:37], s36, v2, 0
	v_cvt_pk_bf16_f32 v2, v10, v11
	v_cvt_pk_bf16_f32 v3, v12, v13
	v_cvt_pk_bf16_f32 v4, v14, v15
	v_cvt_pk_bf16_f32 v5, v16, v17
	v_lshl_add_u64 v[10:11], v[92:93], 1, v[180:181]
	global_store_dwordx4 v[10:11], v[2:5], off
	ds_read_b128 v[6:9], v195 offset:1536
	ds_read_b128 v[2:5], v195 offset:1552
	ds_read_b128 v[86:89], v195 offset:2560
	ds_read_b128 v[82:85], v195 offset:2576
	v_mov_b32_e32 v104, v168
	v_mov_b32_e32 v105, v168
	s_waitcnt lgkmcnt(0)
	v_pk_mul_f32 v[14:15], v[2:3], s[26:27] op_sel_hi:[1,0]
	v_pk_mul_f32 v[16:17], v[4:5], s[26:27] op_sel_hi:[1,0]
	v_cndmask_b32_e64 v97, v3, v15, s[38:39]
	v_cndmask_b32_e64 v96, v2, v14, s[38:39]
	v_cvt_f32_i32_e32 v3, v79
	v_cvt_f32_i32_e32 v2, v78
	v_pk_mul_f32 v[10:11], v[6:7], s[26:27] op_sel_hi:[1,0]
	v_cndmask_b32_e64 v95, v5, v17, s[38:39]
	v_cndmask_b32_e64 v94, v4, v16, s[38:39]
	v_cvt_f32_i32_e32 v5, v81
	v_cvt_f32_i32_e32 v4, v80
	v_pk_mul_f32 v[12:13], v[8:9], s[26:27] op_sel_hi:[1,0]
	v_cndmask_b32_e64 v101, v7, v11, s[38:39]
	v_cndmask_b32_e64 v100, v6, v10, s[38:39]
	v_cndmask_b32_e64 v99, v9, v13, s[38:39]
	v_cndmask_b32_e64 v98, v8, v12, s[38:39]
	v_pk_mul_f32 v[6:7], v[104:105], v[100:101]
	v_cvt_f32_i32_e32 v9, v77
	v_pk_mul_f32 v[2:3], v[6:7], v[2:3]
	v_pk_mul_f32 v[6:7], v[104:105], v[98:99]
	v_cvt_f32_i32_e32 v8, v76
	v_pk_mul_f32 v[4:5], v[6:7], v[4:5]
	v_cvt_f32_i32_e32 v7, v75
	v_cvt_f32_i32_e32 v6, v74
	v_pk_mul_f32 v[10:11], v[104:105], v[96:97]
	v_pk_mul_f32 v[6:7], v[10:11], v[6:7]
	v_pk_mul_f32 v[10:11], v[104:105], v[94:95]
	v_pk_mul_f32 v[8:9], v[10:11], v[8:9]
	v_exp_f32_e32 v10, v2
	v_exp_f32_e32 v11, v3
	v_add_f32_e32 v10, 1.0, v10
	v_rcp_f32_e32 v10, v10
	v_add_f32_e32 v11, 1.0, v11
	v_rcp_f32_e32 v11, v11
	v_exp_f32_e32 v12, v4
	v_exp_f32_e32 v13, v5
	v_add_f32_e32 v12, 1.0, v12
	v_rcp_f32_e32 v12, v12
	v_add_f32_e32 v13, 1.0, v13
	v_rcp_f32_e32 v13, v13
	v_exp_f32_e32 v14, v6
	v_exp_f32_e32 v15, v7
	v_add_f32_e32 v14, 1.0, v14
	v_rcp_f32_e32 v14, v14
	v_add_f32_e32 v15, 1.0, v15
	v_rcp_f32_e32 v15, v15
	v_exp_f32_e32 v16, v8
	v_exp_f32_e32 v17, v9
	v_add_f32_e32 v16, 1.0, v16
	v_rcp_f32_e32 v16, v16
	v_add_f32_e32 v17, 1.0, v17
	v_rcp_f32_e32 v17, v17
	v_or_b32_e32 v2, 0x80, v196
	s_not_b32 s3, s95
	v_ashrrev_i32_e32 v2, s93, v2
	v_mad_i64_i32 v[2:3], s[36:37], s94, v2, 0
	v_bitop3_b32 v4, v196, s3, v190 bitop3:0xc8
	v_lshl_add_u64 v[2:3], v[2:3], 1, s[42:43]
	v_lshlrev_b32_e32 v150, 1, v4
	v_lshl_add_u64 v[74:75], v[2:3], 0, v[150:151]
	v_cvt_pk_bf16_f32 v2, v10, v11
	v_cvt_pk_bf16_f32 v3, v12, v13
	v_cvt_pk_bf16_f32 v4, v14, v15
	v_cvt_pk_bf16_f32 v5, v16, v17
	v_lshl_add_u64 v[6:7], v[170:171], 1, v[74:75]
	global_store_dwordx4 v[6:7], v[2:5], off
	v_mov_b32_e32 v168, v169
	v_pk_mul_f32 v[6:7], v[168:169], v[100:101]
	v_cvt_f32_i32_e32 v3, v71
	v_cvt_f32_i32_e32 v2, v70
	v_cvt_f32_i32_e32 v5, v73
	v_cvt_f32_i32_e32 v4, v72
	v_cvt_f32_i32_e32 v9, v69
	v_pk_mul_f32 v[2:3], v[6:7], v[2:3]
	v_pk_mul_f32 v[6:7], v[168:169], v[98:99]
	v_cvt_f32_i32_e32 v8, v68
	v_pk_mul_f32 v[4:5], v[6:7], v[4:5]
	v_cvt_f32_i32_e32 v7, v67
; DI unsigned pk2(float lo, float hi) { f32x2 v = {lo, hi}; bf16x2_t b = __builtin_convertvector(v, bf16x2_t); return __builtin_bit_cast(unsigned, b); }
; DI float sigmoidf_(float x) { return __builtin_amdgcn_rcpf(1.0f + __expf(-x)); }
;     DI void operator()(const f32x4 (&acc)[2][2][4][2], const Unit& u, int wr, int wc, int fr, int fq, const LAS unsigned char* slot) const {
;     ...
;             for (int ai = 0; ai < 2; ++ai)
; #pragma unroll
;                 for (int m = 0; m < 4; ++m) { const int rr = row0 + ai * HALF + m * 16; const size_t ro = (size_t)rr * pitch; float v[8]; const float rs = rsv[ai][m];
; #pragma unroll
;                     for (int j = 0; j < 8; ++j) v[j] = (float)__builtin_bit_cast(i32x4, acc[ai][bj][m][j >> 2])[j & 3] * (rs * csv[j]);
;                     if (cls != 0) {
; #pragma unroll
;                         for (int j = 0; j < 8; ++j) { if (cls == 1) v[j] *= sigmoidf_(v[j]); else v[j] = __builtin_amdgcn_rcpf(1.0f + __builtin_amdgcn_exp2f(v[j])); }
;                         if (cls == 2) {
; #pragma unroll
;                             for (int j = 0; j < 8; ++j) { const float l = lbv[j]; v[j] = __builtin_amdgcn_logf(l + (1.0f - l) * v[j]); } }
;                     }
;                     u32x4 w; w.x = pk2(v[0], v[1]); w.y = pk2(v[2], v[3]); w.z = pk2(v[4], v[5]); w.w = pk2(v[6], v[7]);
;                     *(u32x4*)(colp + ro) = w; }
	v_cvt_f32_i32_e32 v6, v66
	v_pk_mul_f32 v[10:11], v[168:169], v[96:97]
	v_pk_mul_f32 v[6:7], v[10:11], v[6:7]
	v_pk_mul_f32 v[10:11], v[168:169], v[94:95]
	v_pk_mul_f32 v[8:9], v[10:11], v[8:9]
	v_exp_f32_e32 v10, v2
	v_exp_f32_e32 v11, v3
	v_add_f32_e32 v10, 1.0, v10
	v_rcp_f32_e32 v10, v10
	v_add_f32_e32 v11, 1.0, v11
	v_rcp_f32_e32 v11, v11
	v_exp_f32_e32 v12, v4
	v_exp_f32_e32 v13, v5
	v_add_f32_e32 v12, 1.0, v12
	v_rcp_f32_e32 v12, v12
	v_add_f32_e32 v13, 1.0, v13
	v_rcp_f32_e32 v13, v13
	v_exp_f32_e32 v14, v6
	v_exp_f32_e32 v15, v7
	v_add_f32_e32 v14, 1.0, v14
	v_rcp_f32_e32 v14, v14
	v_add_f32_e32 v15, 1.0, v15
	v_rcp_f32_e32 v15, v15
	v_exp_f32_e32 v16, v8
	v_exp_f32_e32 v17, v9
	v_add_f32_e32 v16, 1.0, v16
	v_rcp_f32_e32 v16, v16
	v_add_f32_e32 v17, 1.0, v17
	v_rcp_f32_e32 v17, v17
	v_cvt_pk_bf16_f32 v2, v10, v11
	v_cvt_pk_bf16_f32 v3, v12, v13
	v_cvt_pk_bf16_f32 v4, v14, v15
	v_cvt_pk_bf16_f32 v5, v16, v17
	v_lshl_add_u64 v[6:7], v[138:139], 1, v[74:75]
	global_store_dwordx4 v[6:7], v[2:5], off
	v_mov_b32_e32 v8, v160
	v_mov_b32_e32 v9, v160
	v_cvt_f32_i32_e32 v3, v63
	v_cvt_f32_i32_e32 v2, v62
	v_cvt_f32_i32_e32 v5, v65
	v_cvt_f32_i32_e32 v4, v64
	v_pk_mul_f32 v[6:7], v[8:9], v[100:101]
	v_cvt_f32_i32_e32 v11, v61
	v_pk_mul_f32 v[2:3], v[6:7], v[2:3]
	v_pk_mul_f32 v[6:7], v[8:9], v[98:99]
	v_cvt_f32_i32_e32 v10, v60
	v_pk_mul_f32 v[4:5], v[6:7], v[4:5]
	v_cvt_f32_i32_e32 v7, v59
	v_cvt_f32_i32_e32 v6, v58
	v_pk_mul_f32 v[12:13], v[8:9], v[96:97]
	v_pk_mul_f32 v[8:9], v[8:9], v[94:95]
	v_pk_mul_f32 v[6:7], v[12:13], v[6:7]
	v_pk_mul_f32 v[8:9], v[8:9], v[10:11]
	v_exp_f32_e32 v10, v2
	v_exp_f32_e32 v11, v3
	v_add_f32_e32 v10, 1.0, v10
	v_rcp_f32_e32 v10, v10
	v_add_f32_e32 v11, 1.0, v11
	v_rcp_f32_e32 v11, v11
	v_exp_f32_e32 v12, v4
	v_exp_f32_e32 v13, v5
	v_add_f32_e32 v12, 1.0, v12
	v_rcp_f32_e32 v12, v12
	v_add_f32_e32 v13, 1.0, v13
	v_rcp_f32_e32 v13, v13
	v_exp_f32_e32 v14, v6
	v_exp_f32_e32 v15, v7
	v_add_f32_e32 v14, 1.0, v14
	v_rcp_f32_e32 v14, v14
	v_add_f32_e32 v15, 1.0, v15
	v_rcp_f32_e32 v15, v15
	v_exp_f32_e32 v16, v8
	v_exp_f32_e32 v17, v9
	v_add_f32_e32 v16, 1.0, v16
	v_rcp_f32_e32 v16, v16
	v_add_f32_e32 v17, 1.0, v17
	v_rcp_f32_e32 v17, v17
	v_cvt_pk_bf16_f32 v2, v10, v11
	v_cvt_pk_bf16_f32 v3, v12, v13
	v_cvt_pk_bf16_f32 v4, v14, v15
	v_cvt_pk_bf16_f32 v5, v16, v17
	v_lshl_add_u64 v[6:7], v[130:131], 1, v[74:75]
	global_store_dwordx4 v[6:7], v[2:5], off
	v_mov_b32_e32 v160, v161
	v_pk_mul_f32 v[6:7], v[160:161], v[100:101]
	v_cvt_f32_i32_e32 v3, v55
	v_cvt_f32_i32_e32 v2, v54
	v_cvt_f32_i32_e32 v5, v57
	v_cvt_f32_i32_e32 v4, v56
	v_cvt_f32_i32_e32 v9, v53
	v_pk_mul_f32 v[2:3], v[6:7], v[2:3]
	v_pk_mul_f32 v[6:7], v[160:161], v[98:99]
	v_cvt_f32_i32_e32 v8, v52
	v_pk_mul_f32 v[4:5], v[6:7], v[4:5]
	v_cvt_f32_i32_e32 v7, v51
	v_cvt_f32_i32_e32 v6, v50
	v_pk_mul_f32 v[10:11], v[160:161], v[96:97]
	v_pk_mul_f32 v[6:7], v[10:11], v[6:7]
	v_pk_mul_f32 v[10:11], v[160:161], v[94:95]
	v_pk_mul_f32 v[8:9], v[10:11], v[8:9]
	v_exp_f32_e32 v10, v2
	v_exp_f32_e32 v11, v3
	v_add_f32_e32 v10, 1.0, v10
	v_rcp_f32_e32 v10, v10
	v_add_f32_e32 v11, 1.0, v11
	v_rcp_f32_e32 v11, v11
	v_exp_f32_e32 v12, v4
	v_exp_f32_e32 v13, v5
	v_add_f32_e32 v12, 1.0, v12
	v_rcp_f32_e32 v12, v12
	v_add_f32_e32 v13, 1.0, v13
	v_rcp_f32_e32 v13, v13
	v_exp_f32_e32 v14, v6
	v_exp_f32_e32 v15, v7
	v_add_f32_e32 v14, 1.0, v14
	v_rcp_f32_e32 v14, v14
	v_add_f32_e32 v15, 1.0, v15
	v_rcp_f32_e32 v15, v15
	v_exp_f32_e32 v16, v8
	v_exp_f32_e32 v17, v9
	v_add_f32_e32 v16, 1.0, v16
	v_rcp_f32_e32 v16, v16
	v_add_f32_e32 v17, 1.0, v17
	v_rcp_f32_e32 v17, v17
	v_cvt_pk_bf16_f32 v2, v10, v11
	v_cvt_pk_bf16_f32 v3, v12, v13
	v_cvt_pk_bf16_f32 v4, v14, v15
	v_cvt_pk_bf16_f32 v5, v16, v17
	v_lshl_add_u64 v[6:7], v[122:123], 1, v[74:75]
	global_store_dwordx4 v[6:7], v[2:5], off
	v_mov_b32_e32 v8, v158
	v_mov_b32_e32 v9, v158
	v_cvt_f32_i32_e32 v3, v47
	v_cvt_f32_i32_e32 v2, v46
	v_cvt_f32_i32_e32 v5, v49
	v_cvt_f32_i32_e32 v4, v48
	v_pk_mul_f32 v[6:7], v[8:9], v[100:101]
	v_cvt_f32_i32_e32 v11, v45
	v_pk_mul_f32 v[2:3], v[6:7], v[2:3]
	v_pk_mul_f32 v[6:7], v[8:9], v[98:99]
	v_cvt_f32_i32_e32 v10, v44
	v_pk_mul_f32 v[4:5], v[6:7], v[4:5]
	v_cvt_f32_i32_e32 v7, v43
	v_cvt_f32_i32_e32 v6, v42
	v_pk_mul_f32 v[12:13], v[8:9], v[96:97]
	v_pk_mul_f32 v[8:9], v[8:9], v[94:95]
	v_pk_mul_f32 v[6:7], v[12:13], v[6:7]
	v_pk_mul_f32 v[8:9], v[8:9], v[10:11]
	v_exp_f32_e32 v10, v2
	v_exp_f32_e32 v11, v3
	v_add_f32_e32 v10, 1.0, v10
	v_rcp_f32_e32 v10, v10
	v_add_f32_e32 v11, 1.0, v11
	v_rcp_f32_e32 v11, v11
	v_exp_f32_e32 v12, v4
	v_exp_f32_e32 v13, v5
	v_add_f32_e32 v12, 1.0, v12
	v_rcp_f32_e32 v12, v12
	v_add_f32_e32 v13, 1.0, v13
	v_rcp_f32_e32 v13, v13
	v_exp_f32_e32 v14, v6
	v_exp_f32_e32 v15, v7
	v_add_f32_e32 v14, 1.0, v14
	v_rcp_f32_e32 v14, v14
	v_add_f32_e32 v15, 1.0, v15
	v_rcp_f32_e32 v15, v15
	v_exp_f32_e32 v16, v8
	v_exp_f32_e32 v17, v9
	v_add_f32_e32 v16, 1.0, v16
	v_rcp_f32_e32 v16, v16
	v_add_f32_e32 v17, 1.0, v17
	v_rcp_f32_e32 v17, v17
	v_cvt_pk_bf16_f32 v2, v10, v11
	v_cvt_pk_bf16_f32 v3, v12, v13
	v_cvt_pk_bf16_f32 v4, v14, v15
	v_cvt_pk_bf16_f32 v5, v16, v17
	v_lshl_add_u64 v[6:7], v[114:115], 1, v[74:75]
	global_store_dwordx4 v[6:7], v[2:5], off
	v_mov_b32_e32 v158, v159
	v_pk_mul_f32 v[6:7], v[158:159], v[100:101]
	v_cvt_f32_i32_e32 v3, v39
	v_cvt_f32_i32_e32 v2, v38
	v_cvt_f32_i32_e32 v5, v41
	v_cvt_f32_i32_e32 v4, v40
	v_cvt_f32_i32_e32 v9, v37
	v_pk_mul_f32 v[2:3], v[6:7], v[2:3]
	v_pk_mul_f32 v[6:7], v[158:159], v[98:99]
	v_cvt_f32_i32_e32 v8, v36
	v_pk_mul_f32 v[4:5], v[6:7], v[4:5]
	v_cvt_f32_i32_e32 v7, v35
	v_cvt_f32_i32_e32 v6, v34
; DI unsigned pk2(float lo, float hi) { f32x2 v = {lo, hi}; bf16x2_t b = __builtin_convertvector(v, bf16x2_t); return __builtin_bit_cast(unsigned, b); }
; DI float sigmoidf_(float x) { return __builtin_amdgcn_rcpf(1.0f + __expf(-x)); }
;     DI void operator()(const f32x4 (&acc)[2][2][4][2], const Unit& u, int wr, int wc, int fr, int fq, const LAS unsigned char* slot) const {
;     ...
;         if (pn < 4)       { cls = 0; cbase = C_AQ; po = PO_AQ;  hs = 6;  pitch = 64; }
;         else if (pn < 5)  { cls = 0; cbase = C_AK; po = PO_AKV; hs = 30; pitch = 256; }
;         else if (pn < 9)  { cls = 1; cbase = C_BQ; po = PO_BQ;  hs = 7;  pitch = 128; }
;         else if (pn < 13) { cls = 2; cbase = C_ZF; po = PO_ZF;  hs = 7;  pitch = 128; }
;         else if (pn < 17) { cls = 2; cbase = C_ZB; po = PO_ZB;  hs = 7;  pitch = 128; lb = lbb; }
;         else if (pn < 21) { cls = 0; cbase = C_BV; po = PO_BV;  hs = 7;  pitch = 128; }
;         else if (pn < 25) { cls = 1; cbase = C_BG; po = PO_BG;  hs = 7;  pitch = 128; }
;         else if (pn < 33) { cls = 3; cbase = C_GA; po = PO_GA;  hs = 30; pitch = 2048; }
;         else              { cls = 3; cbase = C_GB; po = PO_GB;  hs = 30; pitch = 2048; }
;     ...
;             for (int ai = 0; ai < 2; ++ai)
; #pragma unroll
;                 for (int m = 0; m < 4; ++m) { const int rr = row0 + ai * HALF + m * 16; const size_t ro = (size_t)rr * pitch; float v[8]; const float rs = rsv[ai][m];
; #pragma unroll
;                     for (int j = 0; j < 8; ++j) v[j] = (float)__builtin_bit_cast(i32x4, acc[ai][bj][m][j >> 2])[j & 3] * (rs * csv[j]);
;                     if (cls != 0) {
; #pragma unroll
;                         for (int j = 0; j < 8; ++j) { if (cls == 1) v[j] *= sigmoidf_(v[j]); else v[j] = __builtin_amdgcn_rcpf(1.0f + __builtin_amdgcn_exp2f(v[j])); }
;                         if (cls == 2) {
; #pragma unroll
;                             for (int j = 0; j < 8; ++j) { const float l = lbv[j]; v[j] = __builtin_amdgcn_logf(l + (1.0f - l) * v[j]); } }
;                     }
;                     u32x4 w; w.x = pk2(v[0], v[1]); w.y = pk2(v[2], v[3]); w.z = pk2(v[4], v[5]); w.w = pk2(v[6], v[7]);
;                     *(u32x4*)(colp + ro) = w; }
	v_pk_mul_f32 v[10:11], v[158:159], v[96:97]
	v_pk_mul_f32 v[6:7], v[10:11], v[6:7]
	v_pk_mul_f32 v[10:11], v[158:159], v[94:95]
	v_pk_mul_f32 v[8:9], v[10:11], v[8:9]
	v_exp_f32_e32 v10, v2
	v_exp_f32_e32 v11, v3
	v_add_f32_e32 v10, 1.0, v10
	v_rcp_f32_e32 v10, v10
	v_add_f32_e32 v11, 1.0, v11
	v_rcp_f32_e32 v11, v11
	v_exp_f32_e32 v12, v4
	v_exp_f32_e32 v13, v5
	v_add_f32_e32 v12, 1.0, v12
	v_rcp_f32_e32 v12, v12
	v_add_f32_e32 v13, 1.0, v13
	v_rcp_f32_e32 v13, v13
	v_exp_f32_e32 v14, v6
	v_exp_f32_e32 v15, v7
	v_add_f32_e32 v14, 1.0, v14
	v_rcp_f32_e32 v14, v14
	v_add_f32_e32 v15, 1.0, v15
	v_rcp_f32_e32 v15, v15
	v_exp_f32_e32 v16, v8
	v_exp_f32_e32 v17, v9
	v_add_f32_e32 v16, 1.0, v16
	v_rcp_f32_e32 v16, v16
	v_add_f32_e32 v17, 1.0, v17
	v_rcp_f32_e32 v17, v17
	v_cvt_pk_bf16_f32 v2, v10, v11
	v_cvt_pk_bf16_f32 v3, v12, v13
	v_cvt_pk_bf16_f32 v4, v14, v15
	v_cvt_pk_bf16_f32 v5, v16, v17
	v_lshl_add_u64 v[6:7], v[102:103], 1, v[74:75]
	global_store_dwordx4 v[6:7], v[2:5], off
	v_mov_b32_e32 v8, v156
	v_mov_b32_e32 v9, v156
	v_cvt_f32_i32_e32 v3, v31
	v_cvt_f32_i32_e32 v2, v30
	v_cvt_f32_i32_e32 v5, v33
	v_cvt_f32_i32_e32 v4, v32
	v_pk_mul_f32 v[6:7], v[8:9], v[100:101]
	v_cvt_f32_i32_e32 v11, v29
	v_pk_mul_f32 v[2:3], v[6:7], v[2:3]
	v_pk_mul_f32 v[6:7], v[8:9], v[98:99]
	v_cvt_f32_i32_e32 v10, v28
	v_pk_mul_f32 v[4:5], v[6:7], v[4:5]
	v_cvt_f32_i32_e32 v7, v27
	v_cvt_f32_i32_e32 v6, v26
	v_pk_mul_f32 v[12:13], v[8:9], v[96:97]
	v_pk_mul_f32 v[8:9], v[8:9], v[94:95]
	v_pk_mul_f32 v[6:7], v[12:13], v[6:7]
	v_pk_mul_f32 v[8:9], v[8:9], v[10:11]
	v_exp_f32_e32 v10, v2
	v_exp_f32_e32 v11, v3
	v_add_f32_e32 v10, 1.0, v10
	v_rcp_f32_e32 v10, v10
	v_add_f32_e32 v11, 1.0, v11
	v_rcp_f32_e32 v11, v11
	v_exp_f32_e32 v12, v4
	v_exp_f32_e32 v13, v5
	v_add_f32_e32 v12, 1.0, v12
	v_rcp_f32_e32 v12, v12
	v_add_f32_e32 v13, 1.0, v13
	v_rcp_f32_e32 v13, v13
	v_exp_f32_e32 v14, v6
	v_exp_f32_e32 v15, v7
	v_add_f32_e32 v14, 1.0, v14
	v_rcp_f32_e32 v14, v14
	v_add_f32_e32 v15, 1.0, v15
	v_rcp_f32_e32 v15, v15
	v_exp_f32_e32 v16, v8
	v_exp_f32_e32 v17, v9
	v_add_f32_e32 v16, 1.0, v16
	v_rcp_f32_e32 v16, v16
	v_add_f32_e32 v17, 1.0, v17
	v_rcp_f32_e32 v17, v17
	v_cvt_pk_bf16_f32 v2, v10, v11
	v_cvt_pk_bf16_f32 v3, v12, v13
	v_cvt_pk_bf16_f32 v4, v14, v15
	v_cvt_pk_bf16_f32 v5, v16, v17
	v_lshl_add_u64 v[6:7], v[90:91], 1, v[74:75]
	global_store_dwordx4 v[6:7], v[2:5], off
	v_mov_b32_e32 v156, v157
	v_pk_mul_f32 v[6:7], v[156:157], v[100:101]
	v_cvt_f32_i32_e32 v3, v23
	v_cvt_f32_i32_e32 v2, v22
	v_cvt_f32_i32_e32 v5, v25
	v_cvt_f32_i32_e32 v4, v24
	v_cvt_f32_i32_e32 v9, v21
	v_pk_mul_f32 v[2:3], v[6:7], v[2:3]
	v_pk_mul_f32 v[6:7], v[156:157], v[98:99]
	v_cvt_f32_i32_e32 v8, v20
	v_pk_mul_f32 v[4:5], v[6:7], v[4:5]
	v_cvt_f32_i32_e32 v7, v19
	v_cvt_f32_i32_e32 v6, v18
	v_pk_mul_f32 v[10:11], v[156:157], v[96:97]
	v_pk_mul_f32 v[6:7], v[10:11], v[6:7]
	v_pk_mul_f32 v[10:11], v[156:157], v[94:95]
	v_pk_mul_f32 v[8:9], v[10:11], v[8:9]
	v_exp_f32_e32 v10, v2
	v_exp_f32_e32 v11, v3
	v_add_f32_e32 v10, 1.0, v10
	v_rcp_f32_e32 v10, v10
	v_add_f32_e32 v11, 1.0, v11
	v_rcp_f32_e32 v11, v11
	v_exp_f32_e32 v12, v4
	v_exp_f32_e32 v13, v5
	v_add_f32_e32 v12, 1.0, v12
	v_rcp_f32_e32 v12, v12
	v_add_f32_e32 v13, 1.0, v13
	v_rcp_f32_e32 v13, v13
	v_exp_f32_e32 v14, v6
	v_exp_f32_e32 v15, v7
	v_add_f32_e32 v14, 1.0, v14
	v_rcp_f32_e32 v14, v14
	v_add_f32_e32 v15, 1.0, v15
	v_rcp_f32_e32 v15, v15
	s_mov_b64 s[34:35], -1
	v_exp_f32_e32 v16, v8
	s_mov_b64 s[6:7], -1
	v_add_f32_e32 v16, 1.0, v16
	v_rcp_f32_e32 v16, v16
	v_exp_f32_e32 v17, v9
	s_mov_b64 s[36:37], 0
	v_add_f32_e32 v17, 1.0, v17
	v_rcp_f32_e32 v17, v17
	v_cvt_pk_bf16_f32 v2, v10, v11
	v_cvt_pk_bf16_f32 v3, v12, v13
	v_cvt_pk_bf16_f32 v4, v14, v15
	v_cvt_pk_bf16_f32 v5, v16, v17
	v_lshl_add_u64 v[6:7], v[92:93], 1, v[74:75]
	s_and_b64 vcc, exec, s[4:5]
	s_mov_b64 s[4:5], -1
	global_store_dwordx4 v[6:7], v[2:5], off
	s_branch .Lepj_join
.Lepj_A:
	s_lshl_b32 s37, s90, 12
	s_and_b32 s37, s37, 0x1000
	s_add_i32 s37, s37, 0
	s_add_i32 s37, s37, 0x21000
	v_mov_b32_e32 v150, v151
	v_add_u32_e32 v14, s37, v182
	v_add_u32_e32 v195, s37, v185
	ds_read2_b32 v[168:169], v14 offset1:16
	ds_read2_b32 v[160:161], v14 offset0:32 offset1:48
	ds_read2_b32 v[158:159], v14 offset0:128 offset1:144
	ds_read_b128 v[10:13], v195 offset:1024
	ds_read2_b32 v[156:157], v14 offset0:160 offset1:176
	ds_read_b128 v[14:17], v195 offset:1040
	ds_read_b128 v[106:109], v195 offset:2048
	ds_read_b128 v[98:101], v195 offset:2064
	v_cvt_f32_i32_e32 v3, v3
	v_cvt_f32_i32_e32 v2, v2
	s_waitcnt lgkmcnt(0)
; DI unsigned pk2(float lo, float hi) { f32x2 v = {lo, hi}; bf16x2_t b = __builtin_convertvector(v, bf16x2_t); return __builtin_bit_cast(unsigned, b); }
; DI float sigmoidf_(float x) { return __builtin_amdgcn_rcpf(1.0f + __expf(-x)); }
;     DI void operator()(const f32x4 (&acc)[2][2][4][2], const Unit& u, int wr, int wc, int fr, int fq, const LAS unsigned char* slot) const {
;     ...
;             for (int ai = 0; ai < 2; ++ai)
; #pragma unroll
;                 for (int m = 0; m < 4; ++m) { const int rr = row0 + ai * HALF + m * 16; const size_t ro = (size_t)rr * pitch; float v[8]; const float rs = rsv[ai][m];
; #pragma unroll
;                     for (int j = 0; j < 8; ++j) v[j] = (float)__builtin_bit_cast(i32x4, acc[ai][bj][m][j >> 2])[j & 3] * (rs * csv[j]);
;                     if (cls != 0) {
; #pragma unroll
;                         for (int j = 0; j < 8; ++j) { if (cls == 1) v[j] *= sigmoidf_(v[j]); else v[j] = __builtin_amdgcn_rcpf(1.0f + __builtin_amdgcn_exp2f(v[j])); }
;                         if (cls == 2) {
; #pragma unroll
;                             for (int j = 0; j < 8; ++j) { const float l = lbv[j]; v[j] = __builtin_amdgcn_logf(l + (1.0f - l) * v[j]); } }
;                     }
;                     u32x4 w; w.x = pk2(v[0], v[1]); w.y = pk2(v[2], v[3]); w.z = pk2(v[4], v[5]); w.w = pk2(v[6], v[7]);
;                     *(u32x4*)(colp + ro) = w; }
	v_pk_mul_f32 v[170:171], v[10:11], s[26:27] op_sel_hi:[1,0]
	v_cvt_f32_i32_e32 v5, v5
	v_cvt_f32_i32_e32 v4, v4
	v_pk_mul_f32 v[176:177], v[12:13], s[26:27] op_sel_hi:[1,0]
	v_cndmask_b32_e64 v179, v11, v171, s[38:39]
	v_cndmask_b32_e64 v178, v10, v170, s[38:39]
	v_cvt_f32_i32_e32 v7, v7
	v_cvt_f32_i32_e32 v6, v6
	v_pk_mul_f32 v[174:175], v[14:15], s[26:27] op_sel_hi:[1,0]
	v_cndmask_b32_e64 v177, v13, v177, s[38:39]
	v_cndmask_b32_e64 v176, v12, v176, s[38:39]
	v_pk_mul_f32 v[10:11], v[168:169], v[178:179] op_sel_hi:[0,1]
	v_cvt_f32_i32_e32 v9, v9
	v_cvt_f32_i32_e32 v8, v8
	v_pk_mul_f32 v[172:173], v[16:17], s[26:27] op_sel_hi:[1,0]
	v_cndmask_b32_e64 v175, v15, v175, s[38:39]
	v_cndmask_b32_e64 v174, v14, v174, s[38:39]
	v_pk_mul_f32 v[2:3], v[10:11], v[2:3]
	v_pk_mul_f32 v[10:11], v[168:169], v[176:177] op_sel_hi:[0,1]
	v_cndmask_b32_e64 v173, v17, v173, s[38:39]
	v_cndmask_b32_e64 v172, v16, v172, s[38:39]
	v_pk_mul_f32 v[4:5], v[10:11], v[4:5]
	v_pk_mul_f32 v[10:11], v[168:169], v[174:175] op_sel_hi:[0,1]
	s_xor_b64 s[34:35], s[34:35], -1
	v_pk_mul_f32 v[6:7], v[10:11], v[6:7]
	v_pk_mul_f32 v[10:11], v[168:169], v[172:173] op_sel_hi:[0,1]
	s_xor_b64 s[44:45], s[44:45], -1
	v_pk_mul_f32 v[8:9], v[10:11], v[8:9]
	v_mov_b64_e32 v[16:17], v[8:9]
	v_mov_b64_e32 v[14:15], v[6:7]
	v_mov_b64_e32 v[12:13], v[4:5]
	v_mov_b64_e32 v[10:11], v[2:3]
	v_lshl_or_b32 v2, s95, 8, v184
	s_lshl_b32 s6, s94, 8
	v_add_u32_e32 v196, s3, v2
	s_lshl_b32 s3, s42, 1
	s_add_u32 s42, s76, s3
	s_addc_u32 s43, s77, 0
	s_mul_i32 s94, s36, 0x4100
	s_lshl_b32 s95, -1, s93
	v_ashrrev_i32_e32 v2, s93, v196
	v_add3_u32 v197, s6, v167, v150
	v_mad_i64_i32 v[2:3], s[6:7], s94, v2, 0
	v_bitop3_b32 v4, v196, s95, v196 bitop3:0x30
	v_lshl_add_u64 v[2:3], v[2:3], 1, s[42:43]
	v_lshlrev_b32_e32 v150, 1, v4
	v_lshl_add_u64 v[180:181], v[2:3], 0, v[150:151]
	v_mad_i64_i32 v[170:171], s[6:7], s36, v197, 0
	v_cvt_pk_bf16_f32 v2, v10, v11
	v_cvt_pk_bf16_f32 v3, v12, v13
	v_cvt_pk_bf16_f32 v4, v14, v15
	v_cvt_pk_bf16_f32 v5, v16, v17
	v_lshl_add_u64 v[6:7], v[170:171], 1, v[180:181]
	global_store_dwordx4 v[6:7], v[2:5], off
	v_mov_b32_e32 v8, v169
	v_pk_mul_f32 v[6:7], v[8:9], v[178:179] op_sel_hi:[0,1]
	v_cvt_f32_i32_e32 v3, v143
	v_cvt_f32_i32_e32 v2, v142
	v_cvt_f32_i32_e32 v5, v145
	v_cvt_f32_i32_e32 v4, v144
	v_cvt_f32_i32_e32 v11, v141
	v_pk_mul_f32 v[2:3], v[6:7], v[2:3]
	v_pk_mul_f32 v[6:7], v[8:9], v[176:177] op_sel_hi:[0,1]
	v_cvt_f32_i32_e32 v10, v140
	v_pk_mul_f32 v[4:5], v[6:7], v[4:5]
	v_cvt_f32_i32_e32 v7, v139
	v_cvt_f32_i32_e32 v6, v138
	v_pk_mul_f32 v[12:13], v[8:9], v[174:175] op_sel_hi:[0,1]
	v_pk_mul_f32 v[8:9], v[8:9], v[172:173] op_sel_hi:[0,1]
	v_pk_mul_f32 v[8:9], v[8:9], v[10:11]
	v_cndmask_b32_e64 v10, 0, 1, s[44:45]
	v_pk_mul_f32 v[6:7], v[12:13], v[6:7]
	s_mov_b64 s[62:63], -1
	v_cmp_ne_u32_e64 s[6:7], 1, v10
	v_mov_b64_e32 v[16:17], v[8:9]
	v_mov_b64_e32 v[14:15], v[6:7]
	v_mov_b64_e32 v[12:13], v[4:5]
	v_mov_b64_e32 v[10:11], v[2:3]
	v_add_u32_e32 v2, 16, v197
	v_mad_i64_i32 v[138:139], s[44:45], s36, v2, 0
	v_cvt_pk_bf16_f32 v2, v10, v11
	v_cvt_pk_bf16_f32 v3, v12, v13
	v_cvt_pk_bf16_f32 v4, v14, v15
	v_cvt_pk_bf16_f32 v5, v16, v17
	v_lshl_add_u64 v[6:7], v[138:139], 1, v[180:181]
	global_store_dwordx4 v[6:7], v[2:5], off
	v_pk_mul_f32 v[6:7], v[160:161], v[178:179] op_sel_hi:[0,1]
	v_cvt_f32_i32_e32 v9, v133
	v_cvt_f32_i32_e32 v3, v135
	v_cvt_f32_i32_e32 v2, v134
	v_cvt_f32_i32_e32 v5, v137
	v_cvt_f32_i32_e32 v4, v136
	v_cvt_f32_i32_e32 v8, v132
	v_pk_mul_f32 v[2:3], v[6:7], v[2:3]
	v_pk_mul_f32 v[6:7], v[160:161], v[176:177] op_sel_hi:[0,1]
	v_pk_mul_f32 v[4:5], v[6:7], v[4:5]
	v_cvt_f32_i32_e32 v7, v131
	v_cvt_f32_i32_e32 v6, v130
	v_pk_mul_f32 v[10:11], v[160:161], v[174:175] op_sel_hi:[0,1]
	v_pk_mul_f32 v[6:7], v[10:11], v[6:7]
	v_pk_mul_f32 v[10:11], v[160:161], v[172:173] op_sel_hi:[0,1]
	v_pk_mul_f32 v[8:9], v[10:11], v[8:9]
	v_mov_b64_e32 v[16:17], v[8:9]
	v_mov_b64_e32 v[14:15], v[6:7]
	v_mov_b64_e32 v[12:13], v[4:5]
	v_mov_b64_e32 v[10:11], v[2:3]
	v_add_u32_e32 v2, 32, v197
	v_mad_i64_i32 v[130:131], s[44:45], s36, v2, 0
	v_cvt_pk_bf16_f32 v2, v10, v11
	v_cvt_pk_bf16_f32 v3, v12, v13
	v_cvt_pk_bf16_f32 v4, v14, v15
	v_cvt_pk_bf16_f32 v5, v16, v17
	v_lshl_add_u64 v[6:7], v[130:131], 1, v[180:181]
	global_store_dwordx4 v[6:7], v[2:5], off
	v_mov_b32_e32 v8, v161
	v_pk_mul_f32 v[6:7], v[8:9], v[178:179] op_sel_hi:[0,1]
	v_cvt_f32_i32_e32 v3, v127
	v_cvt_f32_i32_e32 v2, v126
	v_cvt_f32_i32_e32 v5, v129
	v_cvt_f32_i32_e32 v4, v128
	v_cvt_f32_i32_e32 v11, v125
	v_pk_mul_f32 v[2:3], v[6:7], v[2:3]
	v_pk_mul_f32 v[6:7], v[8:9], v[176:177] op_sel_hi:[0,1]
	v_pk_mul_f32 v[4:5], v[6:7], v[4:5]
	v_cvt_f32_i32_e32 v7, v123
	v_cvt_f32_i32_e32 v6, v122
	v_cvt_f32_i32_e32 v10, v124
	v_pk_mul_f32 v[12:13], v[8:9], v[174:175] op_sel_hi:[0,1]
	v_pk_mul_f32 v[8:9], v[8:9], v[172:173] op_sel_hi:[0,1]
	v_pk_mul_f32 v[6:7], v[12:13], v[6:7]
	v_pk_mul_f32 v[8:9], v[8:9], v[10:11]
	v_mov_b64_e32 v[16:17], v[8:9]
	v_mov_b64_e32 v[14:15], v[6:7]
	v_mov_b64_e32 v[12:13], v[4:5]
	v_mov_b64_e32 v[10:11], v[2:3]
	v_add_u32_e32 v2, 48, v197
	v_mad_i64_i32 v[122:123], s[44:45], s36, v2, 0
	v_cvt_pk_bf16_f32 v2, v10, v11
	v_cvt_pk_bf16_f32 v3, v12, v13
	v_cvt_pk_bf16_f32 v4, v14, v15
	v_cvt_pk_bf16_f32 v5, v16, v17
	v_lshl_add_u64 v[6:7], v[122:123], 1, v[180:181]
	global_store_dwordx4 v[6:7], v[2:5], off
	v_pk_mul_f32 v[6:7], v[158:159], v[178:179] op_sel_hi:[0,1]
	v_cvt_f32_i32_e32 v9, v117
	v_cvt_f32_i32_e32 v3, v119
	v_cvt_f32_i32_e32 v2, v118
	v_cvt_f32_i32_e32 v5, v121
	v_cvt_f32_i32_e32 v4, v120
	v_cvt_f32_i32_e32 v8, v116
	v_pk_mul_f32 v[2:3], v[6:7], v[2:3]
; DI unsigned pk2(float lo, float hi) { f32x2 v = {lo, hi}; bf16x2_t b = __builtin_convertvector(v, bf16x2_t); return __builtin_bit_cast(unsigned, b); }
; DI float sigmoidf_(float x) { return __builtin_amdgcn_rcpf(1.0f + __expf(-x)); }
;     DI void operator()(const f32x4 (&acc)[2][2][4][2], const Unit& u, int wr, int wc, int fr, int fq, const LAS unsigned char* slot) const {
;     ...
;             for (int ai = 0; ai < 2; ++ai)
; #pragma unroll
;                 for (int m = 0; m < 4; ++m) { const int rr = row0 + ai * HALF + m * 16; const size_t ro = (size_t)rr * pitch; float v[8]; const float rs = rsv[ai][m];
; #pragma unroll
;                     for (int j = 0; j < 8; ++j) v[j] = (float)__builtin_bit_cast(i32x4, acc[ai][bj][m][j >> 2])[j & 3] * (rs * csv[j]);
;                     if (cls != 0) {
; #pragma unroll
;                         for (int j = 0; j < 8; ++j) { if (cls == 1) v[j] *= sigmoidf_(v[j]); else v[j] = __builtin_amdgcn_rcpf(1.0f + __builtin_amdgcn_exp2f(v[j])); }
;                         if (cls == 2) {
; #pragma unroll
;                             for (int j = 0; j < 8; ++j) { const float l = lbv[j]; v[j] = __builtin_amdgcn_logf(l + (1.0f - l) * v[j]); } }
;                     }
;                     u32x4 w; w.x = pk2(v[0], v[1]); w.y = pk2(v[2], v[3]); w.z = pk2(v[4], v[5]); w.w = pk2(v[6], v[7]);
;                     *(u32x4*)(colp + ro) = w; }
	v_pk_mul_f32 v[6:7], v[158:159], v[176:177] op_sel_hi:[0,1]
	v_pk_mul_f32 v[4:5], v[6:7], v[4:5]
	v_cvt_f32_i32_e32 v7, v115
	v_cvt_f32_i32_e32 v6, v114
	v_pk_mul_f32 v[10:11], v[158:159], v[174:175] op_sel_hi:[0,1]
	v_pk_mul_f32 v[6:7], v[10:11], v[6:7]
	v_pk_mul_f32 v[10:11], v[158:159], v[172:173] op_sel_hi:[0,1]
	v_pk_mul_f32 v[8:9], v[10:11], v[8:9]
	v_mov_b64_e32 v[16:17], v[8:9]
	v_mov_b64_e32 v[14:15], v[6:7]
	v_mov_b64_e32 v[12:13], v[4:5]
	v_mov_b64_e32 v[10:11], v[2:3]
	v_add_u32_e32 v2, 0x80, v197
	v_mad_i64_i32 v[114:115], s[44:45], s36, v2, 0
	v_cvt_pk_bf16_f32 v2, v10, v11
	v_cvt_pk_bf16_f32 v3, v12, v13
	v_cvt_pk_bf16_f32 v4, v14, v15
	v_cvt_pk_bf16_f32 v5, v16, v17
	v_lshl_add_u64 v[6:7], v[114:115], 1, v[180:181]
	global_store_dwordx4 v[6:7], v[2:5], off
	v_mov_b32_e32 v8, v159
	v_pk_mul_f32 v[6:7], v[8:9], v[178:179] op_sel_hi:[0,1]
	v_cvt_f32_i32_e32 v3, v111
	v_cvt_f32_i32_e32 v2, v110
	v_cvt_f32_i32_e32 v5, v113
	v_cvt_f32_i32_e32 v4, v112
	v_cvt_f32_i32_e32 v11, v105
	v_pk_mul_f32 v[2:3], v[6:7], v[2:3]
	v_pk_mul_f32 v[6:7], v[8:9], v[176:177] op_sel_hi:[0,1]
	v_pk_mul_f32 v[4:5], v[6:7], v[4:5]
	v_cvt_f32_i32_e32 v7, v103
	v_cvt_f32_i32_e32 v6, v102
	v_cvt_f32_i32_e32 v10, v104
	v_pk_mul_f32 v[12:13], v[8:9], v[174:175] op_sel_hi:[0,1]
	v_pk_mul_f32 v[8:9], v[8:9], v[172:173] op_sel_hi:[0,1]
	v_pk_mul_f32 v[6:7], v[12:13], v[6:7]
	v_pk_mul_f32 v[8:9], v[8:9], v[10:11]
	v_mov_b64_e32 v[16:17], v[8:9]
	v_mov_b64_e32 v[14:15], v[6:7]
	v_mov_b64_e32 v[12:13], v[4:5]
	v_mov_b64_e32 v[10:11], v[2:3]
	v_add_u32_e32 v2, 0x90, v197
	v_mad_i64_i32 v[102:103], s[44:45], s36, v2, 0
	v_cvt_pk_bf16_f32 v2, v10, v11
	v_cvt_pk_bf16_f32 v3, v12, v13
	v_cvt_pk_bf16_f32 v4, v14, v15
	v_cvt_pk_bf16_f32 v5, v16, v17
	v_lshl_add_u64 v[6:7], v[102:103], 1, v[180:181]
	global_store_dwordx4 v[6:7], v[2:5], off
	v_pk_mul_f32 v[6:7], v[156:157], v[178:179] op_sel_hi:[0,1]
	v_cvt_f32_i32_e32 v9, v93
	v_cvt_f32_i32_e32 v3, v95
	v_cvt_f32_i32_e32 v2, v94
	v_cvt_f32_i32_e32 v5, v97
	v_cvt_f32_i32_e32 v4, v96
	v_cvt_f32_i32_e32 v8, v92
	v_pk_mul_f32 v[2:3], v[6:7], v[2:3]
	v_pk_mul_f32 v[6:7], v[156:157], v[176:177] op_sel_hi:[0,1]
	v_pk_mul_f32 v[4:5], v[6:7], v[4:5]
	v_cvt_f32_i32_e32 v7, v91
	v_cvt_f32_i32_e32 v6, v90
	v_pk_mul_f32 v[10:11], v[156:157], v[174:175] op_sel_hi:[0,1]
	v_pk_mul_f32 v[6:7], v[10:11], v[6:7]
	v_pk_mul_f32 v[10:11], v[156:157], v[172:173] op_sel_hi:[0,1]
	v_pk_mul_f32 v[8:9], v[10:11], v[8:9]
	v_mov_b64_e32 v[16:17], v[8:9]
	v_mov_b64_e32 v[14:15], v[6:7]
	v_mov_b64_e32 v[12:13], v[4:5]
	v_mov_b64_e32 v[10:11], v[2:3]
	v_add_u32_e32 v2, 0xa0, v197
	v_mad_i64_i32 v[90:91], s[44:45], s36, v2, 0
	v_cvt_pk_bf16_f32 v2, v10, v11
	v_cvt_pk_bf16_f32 v3, v12, v13
	v_cvt_pk_bf16_f32 v4, v14, v15
	v_cvt_pk_bf16_f32 v5, v16, v17
	v_lshl_add_u64 v[6:7], v[90:91], 1, v[180:181]
	global_store_dwordx4 v[6:7], v[2:5], off
	v_mov_b32_e32 v8, v157
	v_pk_mul_f32 v[6:7], v[8:9], v[178:179] op_sel_hi:[0,1]
	v_cvt_f32_i32_e32 v3, v87
	v_cvt_f32_i32_e32 v2, v86
	v_cvt_f32_i32_e32 v5, v89
	v_cvt_f32_i32_e32 v4, v88
	v_cvt_f32_i32_e32 v11, v85
	v_pk_mul_f32 v[2:3], v[6:7], v[2:3]
	v_pk_mul_f32 v[6:7], v[8:9], v[176:177] op_sel_hi:[0,1]
	v_pk_mul_f32 v[4:5], v[6:7], v[4:5]
	v_cvt_f32_i32_e32 v7, v83
	v_cvt_f32_i32_e32 v6, v82
	v_cvt_f32_i32_e32 v10, v84
	v_pk_mul_f32 v[12:13], v[8:9], v[174:175] op_sel_hi:[0,1]
	v_pk_mul_f32 v[8:9], v[8:9], v[172:173] op_sel_hi:[0,1]
	v_pk_mul_f32 v[6:7], v[12:13], v[6:7]
	v_pk_mul_f32 v[8:9], v[8:9], v[10:11]
	s_mov_b64 s[44:45], -1
	v_mov_b64_e32 v[16:17], v[8:9]
	v_mov_b64_e32 v[14:15], v[6:7]
	v_mov_b64_e32 v[12:13], v[4:5]
	v_mov_b64_e32 v[10:11], v[2:3]
	v_add_u32_e32 v2, 0xb0, v197
	v_mad_i64_i32 v[92:93], s[36:37], s36, v2, 0
	v_cvt_pk_bf16_f32 v2, v10, v11
	v_cvt_pk_bf16_f32 v3, v12, v13
	v_cvt_pk_bf16_f32 v4, v14, v15
	v_cvt_pk_bf16_f32 v5, v16, v17
	v_lshl_add_u64 v[10:11], v[92:93], 1, v[180:181]
	global_store_dwordx4 v[10:11], v[2:5], off
	ds_read_b128 v[6:9], v195 offset:1536
	ds_read_b128 v[2:5], v195 offset:1552
	ds_read_b128 v[86:89], v195 offset:2560
	ds_read_b128 v[82:85], v195 offset:2576
	v_mov_b32_e32 v104, v168
	v_mov_b32_e32 v105, v168
	s_waitcnt lgkmcnt(0)
	v_pk_mul_f32 v[14:15], v[2:3], s[26:27] op_sel_hi:[1,0]
	v_pk_mul_f32 v[16:17], v[4:5], s[26:27] op_sel_hi:[1,0]
	v_cndmask_b32_e64 v97, v3, v15, s[38:39]
	v_cndmask_b32_e64 v96, v2, v14, s[38:39]
	v_cvt_f32_i32_e32 v3, v79
	v_cvt_f32_i32_e32 v2, v78
	v_pk_mul_f32 v[10:11], v[6:7], s[26:27] op_sel_hi:[1,0]
	v_cndmask_b32_e64 v95, v5, v17, s[38:39]
	v_cndmask_b32_e64 v94, v4, v16, s[38:39]
	v_cvt_f32_i32_e32 v5, v81
	v_cvt_f32_i32_e32 v4, v80
	v_pk_mul_f32 v[12:13], v[8:9], s[26:27] op_sel_hi:[1,0]
	v_cndmask_b32_e64 v101, v7, v11, s[38:39]
	v_cndmask_b32_e64 v100, v6, v10, s[38:39]
	v_cndmask_b32_e64 v99, v9, v13, s[38:39]
	v_cndmask_b32_e64 v98, v8, v12, s[38:39]
	v_pk_mul_f32 v[6:7], v[104:105], v[100:101]
	v_cvt_f32_i32_e32 v9, v77
	v_pk_mul_f32 v[2:3], v[6:7], v[2:3]
	v_pk_mul_f32 v[6:7], v[104:105], v[98:99]
	v_cvt_f32_i32_e32 v8, v76
	v_pk_mul_f32 v[4:5], v[6:7], v[4:5]
	v_cvt_f32_i32_e32 v7, v75
	v_cvt_f32_i32_e32 v6, v74
	v_pk_mul_f32 v[10:11], v[104:105], v[96:97]
	v_pk_mul_f32 v[6:7], v[10:11], v[6:7]
	v_pk_mul_f32 v[10:11], v[104:105], v[94:95]
	v_pk_mul_f32 v[8:9], v[10:11], v[8:9]
	v_mov_b64_e32 v[16:17], v[8:9]
	v_mov_b64_e32 v[14:15], v[6:7]
	v_mov_b64_e32 v[12:13], v[4:5]
	v_mov_b64_e32 v[10:11], v[2:3]
	v_or_b32_e32 v2, 0x80, v196
	s_not_b32 s3, s95
	v_ashrrev_i32_e32 v2, s93, v2
	v_mad_i64_i32 v[2:3], s[36:37], s94, v2, 0
	v_bitop3_b32 v4, v196, s3, v190 bitop3:0xc8
	v_lshl_add_u64 v[2:3], v[2:3], 1, s[42:43]
; DI unsigned pk2(float lo, float hi) { f32x2 v = {lo, hi}; bf16x2_t b = __builtin_convertvector(v, bf16x2_t); return __builtin_bit_cast(unsigned, b); }
; DI float sigmoidf_(float x) { return __builtin_amdgcn_rcpf(1.0f + __expf(-x)); }
;     DI void operator()(const f32x4 (&acc)[2][2][4][2], const Unit& u, int wr, int wc, int fr, int fq, const LAS unsigned char* slot) const {
;     ...
;             for (int ai = 0; ai < 2; ++ai)
; #pragma unroll
;                 for (int m = 0; m < 4; ++m) { const int rr = row0 + ai * HALF + m * 16; const size_t ro = (size_t)rr * pitch; float v[8]; const float rs = rsv[ai][m];
; #pragma unroll
;                     for (int j = 0; j < 8; ++j) v[j] = (float)__builtin_bit_cast(i32x4, acc[ai][bj][m][j >> 2])[j & 3] * (rs * csv[j]);
;                     if (cls != 0) {
; #pragma unroll
;                         for (int j = 0; j < 8; ++j) { if (cls == 1) v[j] *= sigmoidf_(v[j]); else v[j] = __builtin_amdgcn_rcpf(1.0f + __builtin_amdgcn_exp2f(v[j])); }
;                         if (cls == 2) {
; #pragma unroll
;                             for (int j = 0; j < 8; ++j) { const float l = lbv[j]; v[j] = __builtin_amdgcn_logf(l + (1.0f - l) * v[j]); } }
;                     }
;                     u32x4 w; w.x = pk2(v[0], v[1]); w.y = pk2(v[2], v[3]); w.z = pk2(v[4], v[5]); w.w = pk2(v[6], v[7]);
;                     *(u32x4*)(colp + ro) = w; }
	v_lshlrev_b32_e32 v150, 1, v4
	v_lshl_add_u64 v[74:75], v[2:3], 0, v[150:151]
	v_cvt_pk_bf16_f32 v2, v10, v11
	v_cvt_pk_bf16_f32 v3, v12, v13
	v_cvt_pk_bf16_f32 v4, v14, v15
	v_cvt_pk_bf16_f32 v5, v16, v17
	v_lshl_add_u64 v[6:7], v[170:171], 1, v[74:75]
	global_store_dwordx4 v[6:7], v[2:5], off
	v_mov_b32_e32 v168, v169
	v_pk_mul_f32 v[6:7], v[168:169], v[100:101]
	v_cvt_f32_i32_e32 v3, v71
	v_cvt_f32_i32_e32 v2, v70
	v_cvt_f32_i32_e32 v5, v73
	v_cvt_f32_i32_e32 v4, v72
	v_cvt_f32_i32_e32 v9, v69
	v_pk_mul_f32 v[2:3], v[6:7], v[2:3]
	v_pk_mul_f32 v[6:7], v[168:169], v[98:99]
	v_cvt_f32_i32_e32 v8, v68
	v_pk_mul_f32 v[4:5], v[6:7], v[4:5]
	v_cvt_f32_i32_e32 v7, v67
	v_cvt_f32_i32_e32 v6, v66
	v_pk_mul_f32 v[10:11], v[168:169], v[96:97]
	v_pk_mul_f32 v[6:7], v[10:11], v[6:7]
	v_pk_mul_f32 v[10:11], v[168:169], v[94:95]
	v_pk_mul_f32 v[8:9], v[10:11], v[8:9]
	v_mov_b64_e32 v[16:17], v[8:9]
	v_mov_b64_e32 v[14:15], v[6:7]
	v_mov_b64_e32 v[12:13], v[4:5]
	v_mov_b64_e32 v[10:11], v[2:3]
	v_cvt_pk_bf16_f32 v2, v10, v11
	v_cvt_pk_bf16_f32 v3, v12, v13
	v_cvt_pk_bf16_f32 v4, v14, v15
	v_cvt_pk_bf16_f32 v5, v16, v17
	v_lshl_add_u64 v[6:7], v[138:139], 1, v[74:75]
	global_store_dwordx4 v[6:7], v[2:5], off
	v_mov_b32_e32 v8, v160
	v_mov_b32_e32 v9, v160
	v_cvt_f32_i32_e32 v3, v63
	v_cvt_f32_i32_e32 v2, v62
	v_cvt_f32_i32_e32 v5, v65
	v_cvt_f32_i32_e32 v4, v64
	v_pk_mul_f32 v[6:7], v[8:9], v[100:101]
	v_cvt_f32_i32_e32 v11, v61
	v_pk_mul_f32 v[2:3], v[6:7], v[2:3]
	v_pk_mul_f32 v[6:7], v[8:9], v[98:99]
	v_cvt_f32_i32_e32 v10, v60
	v_pk_mul_f32 v[4:5], v[6:7], v[4:5]
	v_cvt_f32_i32_e32 v7, v59
	v_cvt_f32_i32_e32 v6, v58
	v_pk_mul_f32 v[12:13], v[8:9], v[96:97]
	v_pk_mul_f32 v[8:9], v[8:9], v[94:95]
	v_pk_mul_f32 v[6:7], v[12:13], v[6:7]
	v_pk_mul_f32 v[8:9], v[8:9], v[10:11]
	v_mov_b64_e32 v[16:17], v[8:9]
	v_mov_b64_e32 v[14:15], v[6:7]
	v_mov_b64_e32 v[12:13], v[4:5]
	v_mov_b64_e32 v[10:11], v[2:3]
	v_cvt_pk_bf16_f32 v2, v10, v11
	v_cvt_pk_bf16_f32 v3, v12, v13
	v_cvt_pk_bf16_f32 v4, v14, v15
	v_cvt_pk_bf16_f32 v5, v16, v17
	v_lshl_add_u64 v[6:7], v[130:131], 1, v[74:75]
	global_store_dwordx4 v[6:7], v[2:5], off
	v_mov_b32_e32 v160, v161
	v_pk_mul_f32 v[6:7], v[160:161], v[100:101]
	v_cvt_f32_i32_e32 v3, v55
	v_cvt_f32_i32_e32 v2, v54
	v_cvt_f32_i32_e32 v5, v57
	v_cvt_f32_i32_e32 v4, v56
	v_cvt_f32_i32_e32 v9, v53
	v_pk_mul_f32 v[2:3], v[6:7], v[2:3]
	v_pk_mul_f32 v[6:7], v[160:161], v[98:99]
	v_cvt_f32_i32_e32 v8, v52
	v_pk_mul_f32 v[4:5], v[6:7], v[4:5]
	v_cvt_f32_i32_e32 v7, v51
	v_cvt_f32_i32_e32 v6, v50
	v_pk_mul_f32 v[10:11], v[160:161], v[96:97]
	v_pk_mul_f32 v[6:7], v[10:11], v[6:7]
	v_pk_mul_f32 v[10:11], v[160:161], v[94:95]
	v_pk_mul_f32 v[8:9], v[10:11], v[8:9]
	v_mov_b64_e32 v[16:17], v[8:9]
	v_mov_b64_e32 v[14:15], v[6:7]
	v_mov_b64_e32 v[12:13], v[4:5]
	v_mov_b64_e32 v[10:11], v[2:3]
	v_cvt_pk_bf16_f32 v2, v10, v11
	v_cvt_pk_bf16_f32 v3, v12, v13
	v_cvt_pk_bf16_f32 v4, v14, v15
	v_cvt_pk_bf16_f32 v5, v16, v17
	v_lshl_add_u64 v[6:7], v[122:123], 1, v[74:75]
	global_store_dwordx4 v[6:7], v[2:5], off
	v_mov_b32_e32 v8, v158
	v_mov_b32_e32 v9, v158
	v_cvt_f32_i32_e32 v3, v47
	v_cvt_f32_i32_e32 v2, v46
	v_cvt_f32_i32_e32 v5, v49
	v_cvt_f32_i32_e32 v4, v48
	v_pk_mul_f32 v[6:7], v[8:9], v[100:101]
	v_cvt_f32_i32_e32 v11, v45
	v_pk_mul_f32 v[2:3], v[6:7], v[2:3]
	v_pk_mul_f32 v[6:7], v[8:9], v[98:99]
	v_cvt_f32_i32_e32 v10, v44
	v_pk_mul_f32 v[4:5], v[6:7], v[4:5]
	v_cvt_f32_i32_e32 v7, v43
	v_cvt_f32_i32_e32 v6, v42
	v_pk_mul_f32 v[12:13], v[8:9], v[96:97]
	v_pk_mul_f32 v[8:9], v[8:9], v[94:95]
	v_pk_mul_f32 v[6:7], v[12:13], v[6:7]
	v_pk_mul_f32 v[8:9], v[8:9], v[10:11]
	v_mov_b64_e32 v[16:17], v[8:9]
	v_mov_b64_e32 v[14:15], v[6:7]
	v_mov_b64_e32 v[12:13], v[4:5]
	v_mov_b64_e32 v[10:11], v[2:3]
	v_cvt_pk_bf16_f32 v2, v10, v11
	v_cvt_pk_bf16_f32 v3, v12, v13
	v_cvt_pk_bf16_f32 v4, v14, v15
	v_cvt_pk_bf16_f32 v5, v16, v17
	v_lshl_add_u64 v[6:7], v[114:115], 1, v[74:75]
	global_store_dwordx4 v[6:7], v[2:5], off
	v_mov_b32_e32 v158, v159
	v_pk_mul_f32 v[6:7], v[158:159], v[100:101]
	v_cvt_f32_i32_e32 v3, v39
	v_cvt_f32_i32_e32 v2, v38
	v_cvt_f32_i32_e32 v5, v41
	v_cvt_f32_i32_e32 v4, v40
	v_cvt_f32_i32_e32 v9, v37
	v_pk_mul_f32 v[2:3], v[6:7], v[2:3]
	v_pk_mul_f32 v[6:7], v[158:159], v[98:99]
	v_cvt_f32_i32_e32 v8, v36
	v_pk_mul_f32 v[4:5], v[6:7], v[4:5]
	v_cvt_f32_i32_e32 v7, v35
	v_cvt_f32_i32_e32 v6, v34
	v_pk_mul_f32 v[10:11], v[158:159], v[96:97]
	v_pk_mul_f32 v[6:7], v[10:11], v[6:7]
	v_pk_mul_f32 v[10:11], v[158:159], v[94:95]
	v_pk_mul_f32 v[8:9], v[10:11], v[8:9]
	v_mov_b64_e32 v[16:17], v[8:9]
	v_mov_b64_e32 v[14:15], v[6:7]
	v_mov_b64_e32 v[12:13], v[4:5]
	v_mov_b64_e32 v[10:11], v[2:3]
	v_cvt_pk_bf16_f32 v2, v10, v11
	v_cvt_pk_bf16_f32 v3, v12, v13
	v_cvt_pk_bf16_f32 v4, v14, v15
	v_cvt_pk_bf16_f32 v5, v16, v17
	v_lshl_add_u64 v[6:7], v[102:103], 1, v[74:75]
	global_store_dwordx4 v[6:7], v[2:5], off
	v_mov_b32_e32 v8, v156
	v_mov_b32_e32 v9, v156
	v_cvt_f32_i32_e32 v3, v31
	v_cvt_f32_i32_e32 v2, v30
	v_cvt_f32_i32_e32 v5, v33
	v_cvt_f32_i32_e32 v4, v32
	v_pk_mul_f32 v[6:7], v[8:9], v[100:101]
	v_cvt_f32_i32_e32 v11, v29
	v_pk_mul_f32 v[2:3], v[6:7], v[2:3]
	v_pk_mul_f32 v[6:7], v[8:9], v[98:99]
	v_cvt_f32_i32_e32 v10, v28
	v_pk_mul_f32 v[4:5], v[6:7], v[4:5]
	v_cvt_f32_i32_e32 v7, v27
	v_cvt_f32_i32_e32 v6, v26
	v_pk_mul_f32 v[12:13], v[8:9], v[96:97]
	v_pk_mul_f32 v[8:9], v[8:9], v[94:95]
	v_pk_mul_f32 v[6:7], v[12:13], v[6:7]
	v_pk_mul_f32 v[8:9], v[8:9], v[10:11]
	v_mov_b64_e32 v[16:17], v[8:9]
	v_mov_b64_e32 v[14:15], v[6:7]
	v_mov_b64_e32 v[12:13], v[4:5]
	v_mov_b64_e32 v[10:11], v[2:3]
	v_cvt_pk_bf16_f32 v2, v10, v11
	v_cvt_pk_bf16_f32 v3, v12, v13
	v_cvt_pk_bf16_f32 v4, v14, v15
	v_cvt_pk_bf16_f32 v5, v16, v17
	v_lshl_add_u64 v[6:7], v[90:91], 1, v[74:75]
	global_store_dwordx4 v[6:7], v[2:5], off
	v_mov_b32_e32 v156, v157
	v_pk_mul_f32 v[6:7], v[156:157], v[100:101]
	v_cvt_f32_i32_e32 v3, v23
	v_cvt_f32_i32_e32 v2, v22
	v_cvt_f32_i32_e32 v5, v25
	v_cvt_f32_i32_e32 v4, v24
	v_cvt_f32_i32_e32 v9, v21
	v_pk_mul_f32 v[2:3], v[6:7], v[2:3]
	v_pk_mul_f32 v[6:7], v[156:157], v[98:99]
	v_cvt_f32_i32_e32 v8, v20
	v_pk_mul_f32 v[4:5], v[6:7], v[4:5]
	v_cvt_f32_i32_e32 v7, v19
	v_cvt_f32_i32_e32 v6, v18
	v_pk_mul_f32 v[10:11], v[156:157], v[96:97]
	s_mov_b64 s[36:37], -1
	v_pk_mul_f32 v[6:7], v[10:11], v[6:7]
	v_pk_mul_f32 v[10:11], v[156:157], v[94:95]
	v_pk_mul_f32 v[8:9], v[10:11], v[8:9]
	v_mov_b64_e32 v[16:17], v[8:9]
	v_mov_b64_e32 v[14:15], v[6:7]
	v_mov_b64_e32 v[12:13], v[4:5]
	v_mov_b64_e32 v[10:11], v[2:3]
	v_cvt_pk_bf16_f32 v2, v10, v11
	v_cvt_pk_bf16_f32 v3, v12, v13
	v_cvt_pk_bf16_f32 v4, v14, v15
	v_cvt_pk_bf16_f32 v5, v16, v17
	v_lshl_add_u64 v[6:7], v[92:93], 1, v[74:75]
	s_and_b64 vcc, exec, s[4:5]
	s_mov_b64 s[4:5], -1
	global_store_dwordx4 v[6:7], v[2:5], off
	s_branch .Lepj_join
; DI unsigned pk2(float lo, float hi) { f32x2 v = {lo, hi}; bf16x2_t b = __builtin_convertvector(v, bf16x2_t); return __builtin_bit_cast(unsigned, b); }
; DI float sigmoidf_(float x) { return __builtin_amdgcn_rcpf(1.0f + __expf(-x)); }
;     DI void operator()(const f32x4 (&acc)[2][2][4][2], const Unit& u, int wr, int wc, int fr, int fq, const LAS unsigned char* slot) const {
;     ...
;             for (int ai = 0; ai < 2; ++ai)
; #pragma unroll
;                 for (int m = 0; m < 4; ++m) { const int rr = row0 + ai * HALF + m * 16; const size_t ro = (size_t)rr * pitch; float v[8]; const float rs = rsv[ai][m];
; #pragma unroll
;                     for (int j = 0; j < 8; ++j) v[j] = (float)__builtin_bit_cast(i32x4, acc[ai][bj][m][j >> 2])[j & 3] * (rs * csv[j]);
;                     if (cls != 0) {
; #pragma unroll
;                         for (int j = 0; j < 8; ++j) { if (cls == 1) v[j] *= sigmoidf_(v[j]); else v[j] = __builtin_amdgcn_rcpf(1.0f + __builtin_amdgcn_exp2f(v[j])); }
;                         if (cls == 2) {
; #pragma unroll
;                             for (int j = 0; j < 8; ++j) { const float l = lbv[j]; v[j] = __builtin_amdgcn_logf(l + (1.0f - l) * v[j]); } }
;                     }
;                     u32x4 w; w.x = pk2(v[0], v[1]); w.y = pk2(v[2], v[3]); w.z = pk2(v[4], v[5]); w.w = pk2(v[6], v[7]);
;                     *(u32x4*)(colp + ro) = w; }
.Lepj_B:
	s_lshl_b32 s37, s90, 12
	s_and_b32 s37, s37, 0x1000
	s_add_i32 s37, s37, 0
	s_add_i32 s37, s37, 0x21000
	v_mov_b32_e32 v150, v151
	v_add_u32_e32 v14, s37, v182
	v_add_u32_e32 v195, s37, v185
	ds_read2_b32 v[168:169], v14 offset1:16
	ds_read2_b32 v[160:161], v14 offset0:32 offset1:48
	ds_read2_b32 v[158:159], v14 offset0:128 offset1:144
	ds_read_b128 v[10:13], v195 offset:1024
	ds_read2_b32 v[156:157], v14 offset0:160 offset1:176
	ds_read_b128 v[14:17], v195 offset:1040
	ds_read_b128 v[106:109], v195 offset:2048
	ds_read_b128 v[98:101], v195 offset:2064
	v_cvt_f32_i32_e32 v3, v3
	v_cvt_f32_i32_e32 v2, v2
	s_waitcnt lgkmcnt(0)
	v_pk_mul_f32 v[170:171], v[10:11], s[26:27] op_sel_hi:[1,0]
	v_cvt_f32_i32_e32 v5, v5
	v_cvt_f32_i32_e32 v4, v4
	v_pk_mul_f32 v[176:177], v[12:13], s[26:27] op_sel_hi:[1,0]
	v_cndmask_b32_e64 v179, v11, v171, s[38:39]
	v_cndmask_b32_e64 v178, v10, v170, s[38:39]
	v_cvt_f32_i32_e32 v7, v7
	v_cvt_f32_i32_e32 v6, v6
	v_pk_mul_f32 v[174:175], v[14:15], s[26:27] op_sel_hi:[1,0]
	v_cndmask_b32_e64 v177, v13, v177, s[38:39]
	v_cndmask_b32_e64 v176, v12, v176, s[38:39]
	v_pk_mul_f32 v[10:11], v[168:169], v[178:179] op_sel_hi:[0,1]
	v_cvt_f32_i32_e32 v9, v9
	v_cvt_f32_i32_e32 v8, v8
	v_pk_mul_f32 v[172:173], v[16:17], s[26:27] op_sel_hi:[1,0]
	v_cndmask_b32_e64 v175, v15, v175, s[38:39]
	v_cndmask_b32_e64 v174, v14, v174, s[38:39]
	v_pk_mul_f32 v[2:3], v[10:11], v[2:3]
	v_pk_mul_f32 v[10:11], v[168:169], v[176:177] op_sel_hi:[0,1]
	v_cndmask_b32_e64 v173, v17, v173, s[38:39]
	v_cndmask_b32_e64 v172, v16, v172, s[38:39]
	v_pk_mul_f32 v[4:5], v[10:11], v[4:5]
	v_pk_mul_f32 v[10:11], v[168:169], v[174:175] op_sel_hi:[0,1]
	v_pk_mul_f32 v[6:7], v[10:11], v[6:7]
	v_pk_mul_f32 v[10:11], v[168:169], v[172:173] op_sel_hi:[0,1]
	v_pk_mul_f32 v[8:9], v[10:11], v[8:9]
	v_mul_f32_e32 v10, 0xbfb8aa3b, v2
	v_exp_f32_e32 v10, v10
	v_mul_f32_e32 v11, 0xbfb8aa3b, v3
	v_add_f32_e32 v10, 1.0, v10
	v_rcp_f32_e32 v10, v10
	v_exp_f32_e32 v11, v11
	v_mul_f32_e32 v10, v2, v10
	v_add_f32_e32 v11, 1.0, v11
	v_rcp_f32_e32 v11, v11
	v_mul_f32_e32 v12, 0xbfb8aa3b, v4
	v_mul_f32_e32 v11, v3, v11
	v_exp_f32_e32 v12, v12
	v_mul_f32_e32 v13, 0xbfb8aa3b, v5
	v_add_f32_e32 v12, 1.0, v12
	v_rcp_f32_e32 v12, v12
	v_exp_f32_e32 v13, v13
	v_mul_f32_e32 v12, v4, v12
	v_add_f32_e32 v13, 1.0, v13
	v_rcp_f32_e32 v13, v13
	v_mul_f32_e32 v14, 0xbfb8aa3b, v6
	v_mul_f32_e32 v13, v5, v13
	v_exp_f32_e32 v14, v14
	v_mul_f32_e32 v15, 0xbfb8aa3b, v7
	v_add_f32_e32 v14, 1.0, v14
	v_rcp_f32_e32 v14, v14
	v_exp_f32_e32 v15, v15
	v_mul_f32_e32 v14, v6, v14
	v_add_f32_e32 v15, 1.0, v15
	v_rcp_f32_e32 v15, v15
	v_mul_f32_e32 v16, 0xbfb8aa3b, v8
	v_mul_f32_e32 v15, v7, v15
	v_exp_f32_e32 v16, v16
	v_mul_f32_e32 v17, 0xbfb8aa3b, v9
	v_add_f32_e32 v16, 1.0, v16
	v_rcp_f32_e32 v16, v16
	v_exp_f32_e32 v17, v17
	v_mul_f32_e32 v16, v8, v16
	v_add_f32_e32 v17, 1.0, v17
	v_rcp_f32_e32 v17, v17
	v_lshl_or_b32 v2, s95, 8, v184
	v_mul_f32_e32 v17, v9, v17
	s_lshl_b32 s6, s94, 8
	v_add_u32_e32 v196, s3, v2
	s_lshl_b32 s3, s42, 1
	s_add_u32 s42, s76, s3
	s_addc_u32 s43, s77, 0
	s_mul_i32 s94, s36, 0x4100
	s_lshl_b32 s95, -1, s93
	v_ashrrev_i32_e32 v2, s93, v196
	v_add3_u32 v197, s6, v167, v150
	v_mad_i64_i32 v[2:3], s[6:7], s94, v2, 0
	v_bitop3_b32 v4, v196, s95, v196 bitop3:0x30
	v_lshl_add_u64 v[2:3], v[2:3], 1, s[42:43]
	v_lshlrev_b32_e32 v150, 1, v4
	v_lshl_add_u64 v[180:181], v[2:3], 0, v[150:151]
	v_mad_i64_i32 v[170:171], s[6:7], s36, v197, 0
	v_cvt_pk_bf16_f32 v2, v10, v11
	v_cvt_pk_bf16_f32 v3, v12, v13
	v_cvt_pk_bf16_f32 v4, v14, v15
	v_cvt_pk_bf16_f32 v5, v16, v17
	v_lshl_add_u64 v[6:7], v[170:171], 1, v[180:181]
	global_store_dwordx4 v[6:7], v[2:5], off
	v_mov_b32_e32 v8, v169
	v_pk_mul_f32 v[6:7], v[8:9], v[178:179] op_sel_hi:[0,1]
	v_cvt_f32_i32_e32 v3, v143
	v_cvt_f32_i32_e32 v2, v142
	v_cvt_f32_i32_e32 v5, v145
	v_cvt_f32_i32_e32 v4, v144
	v_cvt_f32_i32_e32 v11, v141
	v_pk_mul_f32 v[2:3], v[6:7], v[2:3]
	v_pk_mul_f32 v[6:7], v[8:9], v[176:177] op_sel_hi:[0,1]
	v_cvt_f32_i32_e32 v10, v140
	v_pk_mul_f32 v[4:5], v[6:7], v[4:5]
	v_cvt_f32_i32_e32 v7, v139
	v_cvt_f32_i32_e32 v6, v138
	v_pk_mul_f32 v[12:13], v[8:9], v[174:175] op_sel_hi:[0,1]
	v_pk_mul_f32 v[8:9], v[8:9], v[172:173] op_sel_hi:[0,1]
	v_pk_mul_f32 v[8:9], v[8:9], v[10:11]
	v_pk_mul_f32 v[6:7], v[12:13], v[6:7]
	v_mul_f32_e32 v10, 0xbfb8aa3b, v2
	v_exp_f32_e32 v10, v10
	v_mul_f32_e32 v11, 0xbfb8aa3b, v3
	v_add_f32_e32 v10, 1.0, v10
	v_rcp_f32_e32 v10, v10
	v_exp_f32_e32 v11, v11
	v_mul_f32_e32 v10, v2, v10
	v_add_f32_e32 v11, 1.0, v11
	v_rcp_f32_e32 v11, v11
	v_mul_f32_e32 v12, 0xbfb8aa3b, v4
	v_mul_f32_e32 v11, v3, v11
	v_exp_f32_e32 v12, v12
	v_mul_f32_e32 v13, 0xbfb8aa3b, v5
	v_add_f32_e32 v12, 1.0, v12
	v_rcp_f32_e32 v12, v12
	v_exp_f32_e32 v13, v13
	v_mul_f32_e32 v12, v4, v12
	v_add_f32_e32 v13, 1.0, v13
	v_rcp_f32_e32 v13, v13
	v_mul_f32_e32 v14, 0xbfb8aa3b, v6
	v_mul_f32_e32 v13, v5, v13
	v_exp_f32_e32 v14, v14
	v_mul_f32_e32 v15, 0xbfb8aa3b, v7
	v_add_f32_e32 v14, 1.0, v14
	v_rcp_f32_e32 v14, v14
	v_exp_f32_e32 v15, v15
	v_mul_f32_e32 v14, v6, v14
	v_add_f32_e32 v15, 1.0, v15
	v_rcp_f32_e32 v15, v15
	v_mul_f32_e32 v16, 0xbfb8aa3b, v8
	v_mul_f32_e32 v15, v7, v15
	v_exp_f32_e32 v16, v16
	v_mul_f32_e32 v17, 0xbfb8aa3b, v9
	v_add_f32_e32 v16, 1.0, v16
	v_rcp_f32_e32 v16, v16
	v_exp_f32_e32 v17, v17
	v_mul_f32_e32 v16, v8, v16
	v_add_f32_e32 v17, 1.0, v17
	v_rcp_f32_e32 v17, v17
	s_mov_b64 s[62:63], 0
	v_mul_f32_e32 v17, v9, v17
	v_add_u32_e32 v2, 16, v197
	v_mad_i64_i32 v[138:139], s[44:45], s36, v2, 0
	v_cvt_pk_bf16_f32 v2, v10, v11
	v_cvt_pk_bf16_f32 v3, v12, v13
	v_cvt_pk_bf16_f32 v4, v14, v15
; DI unsigned pk2(float lo, float hi) { f32x2 v = {lo, hi}; bf16x2_t b = __builtin_convertvector(v, bf16x2_t); return __builtin_bit_cast(unsigned, b); }
; DI float sigmoidf_(float x) { return __builtin_amdgcn_rcpf(1.0f + __expf(-x)); }
;     DI void operator()(const f32x4 (&acc)[2][2][4][2], const Unit& u, int wr, int wc, int fr, int fq, const LAS unsigned char* slot) const {
;     ...
;             for (int ai = 0; ai < 2; ++ai)
; #pragma unroll
;                 for (int m = 0; m < 4; ++m) { const int rr = row0 + ai * HALF + m * 16; const size_t ro = (size_t)rr * pitch; float v[8]; const float rs = rsv[ai][m];
; #pragma unroll
;                     for (int j = 0; j < 8; ++j) v[j] = (float)__builtin_bit_cast(i32x4, acc[ai][bj][m][j >> 2])[j & 3] * (rs * csv[j]);
;                     if (cls != 0) {
; #pragma unroll
;                         for (int j = 0; j < 8; ++j) { if (cls == 1) v[j] *= sigmoidf_(v[j]); else v[j] = __builtin_amdgcn_rcpf(1.0f + __builtin_amdgcn_exp2f(v[j])); }
;                         if (cls == 2) {
; #pragma unroll
;                             for (int j = 0; j < 8; ++j) { const float l = lbv[j]; v[j] = __builtin_amdgcn_logf(l + (1.0f - l) * v[j]); } }
;                     }
;                     u32x4 w; w.x = pk2(v[0], v[1]); w.y = pk2(v[2], v[3]); w.z = pk2(v[4], v[5]); w.w = pk2(v[6], v[7]);
;                     *(u32x4*)(colp + ro) = w; }
	v_cvt_pk_bf16_f32 v5, v16, v17
	v_lshl_add_u64 v[6:7], v[138:139], 1, v[180:181]
	global_store_dwordx4 v[6:7], v[2:5], off
	v_pk_mul_f32 v[6:7], v[160:161], v[178:179] op_sel_hi:[0,1]
	v_cvt_f32_i32_e32 v9, v133
	v_cvt_f32_i32_e32 v3, v135
	v_cvt_f32_i32_e32 v2, v134
	v_cvt_f32_i32_e32 v5, v137
	v_cvt_f32_i32_e32 v4, v136
	v_cvt_f32_i32_e32 v8, v132
	v_pk_mul_f32 v[2:3], v[6:7], v[2:3]
	v_pk_mul_f32 v[6:7], v[160:161], v[176:177] op_sel_hi:[0,1]
	v_pk_mul_f32 v[4:5], v[6:7], v[4:5]
	v_cvt_f32_i32_e32 v7, v131
	v_cvt_f32_i32_e32 v6, v130
	v_pk_mul_f32 v[10:11], v[160:161], v[174:175] op_sel_hi:[0,1]
	v_pk_mul_f32 v[6:7], v[10:11], v[6:7]
	v_pk_mul_f32 v[10:11], v[160:161], v[172:173] op_sel_hi:[0,1]
	v_pk_mul_f32 v[8:9], v[10:11], v[8:9]
	v_mul_f32_e32 v10, 0xbfb8aa3b, v2
	v_exp_f32_e32 v10, v10
	v_mul_f32_e32 v11, 0xbfb8aa3b, v3
	v_add_f32_e32 v10, 1.0, v10
	v_rcp_f32_e32 v10, v10
	v_exp_f32_e32 v11, v11
	v_mul_f32_e32 v10, v2, v10
	v_add_f32_e32 v11, 1.0, v11
	v_rcp_f32_e32 v11, v11
	v_mul_f32_e32 v12, 0xbfb8aa3b, v4
	v_mul_f32_e32 v11, v3, v11
	v_exp_f32_e32 v12, v12
	v_mul_f32_e32 v13, 0xbfb8aa3b, v5
	v_add_f32_e32 v12, 1.0, v12
	v_rcp_f32_e32 v12, v12
	v_exp_f32_e32 v13, v13
	v_mul_f32_e32 v12, v4, v12
	v_add_f32_e32 v13, 1.0, v13
	v_rcp_f32_e32 v13, v13
	v_mul_f32_e32 v14, 0xbfb8aa3b, v6
	v_mul_f32_e32 v13, v5, v13
	v_exp_f32_e32 v14, v14
	v_mul_f32_e32 v15, 0xbfb8aa3b, v7
	v_add_f32_e32 v14, 1.0, v14
	v_rcp_f32_e32 v14, v14
	v_exp_f32_e32 v15, v15
	v_mul_f32_e32 v14, v6, v14
	v_add_f32_e32 v15, 1.0, v15
	v_rcp_f32_e32 v15, v15
	v_mul_f32_e32 v16, 0xbfb8aa3b, v8
	v_mul_f32_e32 v15, v7, v15
	v_exp_f32_e32 v16, v16
	v_mul_f32_e32 v17, 0xbfb8aa3b, v9
	v_add_f32_e32 v16, 1.0, v16
	v_rcp_f32_e32 v16, v16
	v_exp_f32_e32 v17, v17
	v_mul_f32_e32 v16, v8, v16
	v_add_f32_e32 v17, 1.0, v17
	v_rcp_f32_e32 v17, v17
	v_add_u32_e32 v2, 32, v197
	v_mul_f32_e32 v17, v9, v17
	v_mad_i64_i32 v[130:131], s[44:45], s36, v2, 0
	v_cvt_pk_bf16_f32 v2, v10, v11
	v_cvt_pk_bf16_f32 v3, v12, v13
	v_cvt_pk_bf16_f32 v4, v14, v15
	v_cvt_pk_bf16_f32 v5, v16, v17
	v_lshl_add_u64 v[6:7], v[130:131], 1, v[180:181]
	global_store_dwordx4 v[6:7], v[2:5], off
	v_mov_b32_e32 v8, v161
	v_pk_mul_f32 v[6:7], v[8:9], v[178:179] op_sel_hi:[0,1]
	v_cvt_f32_i32_e32 v3, v127
	v_cvt_f32_i32_e32 v2, v126
	v_cvt_f32_i32_e32 v5, v129
	v_cvt_f32_i32_e32 v4, v128
	v_cvt_f32_i32_e32 v11, v125
	v_pk_mul_f32 v[2:3], v[6:7], v[2:3]
	v_pk_mul_f32 v[6:7], v[8:9], v[176:177] op_sel_hi:[0,1]
	v_pk_mul_f32 v[4:5], v[6:7], v[4:5]
	v_cvt_f32_i32_e32 v7, v123
	v_cvt_f32_i32_e32 v6, v122
	v_cvt_f32_i32_e32 v10, v124
	v_pk_mul_f32 v[12:13], v[8:9], v[174:175] op_sel_hi:[0,1]
	v_pk_mul_f32 v[8:9], v[8:9], v[172:173] op_sel_hi:[0,1]
	v_pk_mul_f32 v[6:7], v[12:13], v[6:7]
	v_pk_mul_f32 v[8:9], v[8:9], v[10:11]
	v_mul_f32_e32 v10, 0xbfb8aa3b, v2
	v_exp_f32_e32 v10, v10
	v_mul_f32_e32 v11, 0xbfb8aa3b, v3
	v_add_f32_e32 v10, 1.0, v10
	v_rcp_f32_e32 v10, v10
	v_exp_f32_e32 v11, v11
	v_mul_f32_e32 v10, v2, v10
	v_add_f32_e32 v11, 1.0, v11
	v_rcp_f32_e32 v11, v11
	v_mul_f32_e32 v12, 0xbfb8aa3b, v4
	v_mul_f32_e32 v11, v3, v11
	v_exp_f32_e32 v12, v12
	v_mul_f32_e32 v13, 0xbfb8aa3b, v5
	v_add_f32_e32 v12, 1.0, v12
	v_rcp_f32_e32 v12, v12
	v_exp_f32_e32 v13, v13
	v_mul_f32_e32 v12, v4, v12
	v_add_f32_e32 v13, 1.0, v13
	v_rcp_f32_e32 v13, v13
	v_mul_f32_e32 v14, 0xbfb8aa3b, v6
	v_mul_f32_e32 v13, v5, v13
	v_exp_f32_e32 v14, v14
	v_mul_f32_e32 v15, 0xbfb8aa3b, v7
	v_add_f32_e32 v14, 1.0, v14
	v_rcp_f32_e32 v14, v14
	v_exp_f32_e32 v15, v15
	v_mul_f32_e32 v14, v6, v14
	v_add_f32_e32 v15, 1.0, v15
	v_rcp_f32_e32 v15, v15
	v_mul_f32_e32 v16, 0xbfb8aa3b, v8
	v_mul_f32_e32 v15, v7, v15
	v_exp_f32_e32 v16, v16
	v_mul_f32_e32 v17, 0xbfb8aa3b, v9
	v_add_f32_e32 v16, 1.0, v16
	v_rcp_f32_e32 v16, v16
	v_exp_f32_e32 v17, v17
	v_mul_f32_e32 v16, v8, v16
	v_add_f32_e32 v17, 1.0, v17
	v_rcp_f32_e32 v17, v17
	v_add_u32_e32 v2, 48, v197
	v_mul_f32_e32 v17, v9, v17
	v_mad_i64_i32 v[122:123], s[44:45], s36, v2, 0
	v_cvt_pk_bf16_f32 v2, v10, v11
	v_cvt_pk_bf16_f32 v3, v12, v13
	v_cvt_pk_bf16_f32 v4, v14, v15
	v_cvt_pk_bf16_f32 v5, v16, v17
	v_lshl_add_u64 v[6:7], v[122:123], 1, v[180:181]
	global_store_dwordx4 v[6:7], v[2:5], off
	v_pk_mul_f32 v[6:7], v[158:159], v[178:179] op_sel_hi:[0,1]
	v_cvt_f32_i32_e32 v9, v117
	v_cvt_f32_i32_e32 v3, v119
	v_cvt_f32_i32_e32 v2, v118
	v_cvt_f32_i32_e32 v5, v121
	v_cvt_f32_i32_e32 v4, v120
	v_cvt_f32_i32_e32 v8, v116
	v_pk_mul_f32 v[2:3], v[6:7], v[2:3]
	v_pk_mul_f32 v[6:7], v[158:159], v[176:177] op_sel_hi:[0,1]
	v_pk_mul_f32 v[4:5], v[6:7], v[4:5]
	v_cvt_f32_i32_e32 v7, v115
	v_cvt_f32_i32_e32 v6, v114
	v_pk_mul_f32 v[10:11], v[158:159], v[174:175] op_sel_hi:[0,1]
	v_pk_mul_f32 v[6:7], v[10:11], v[6:7]
	v_pk_mul_f32 v[10:11], v[158:159], v[172:173] op_sel_hi:[0,1]
	v_pk_mul_f32 v[8:9], v[10:11], v[8:9]
	v_mul_f32_e32 v10, 0xbfb8aa3b, v2
	v_exp_f32_e32 v10, v10
	v_mul_f32_e32 v11, 0xbfb8aa3b, v3
	v_add_f32_e32 v10, 1.0, v10
	v_rcp_f32_e32 v10, v10
	v_exp_f32_e32 v11, v11
	v_mul_f32_e32 v10, v2, v10
	v_add_f32_e32 v11, 1.0, v11
	v_rcp_f32_e32 v11, v11
	v_mul_f32_e32 v12, 0xbfb8aa3b, v4
	v_mul_f32_e32 v11, v3, v11
	v_exp_f32_e32 v12, v12
	v_mul_f32_e32 v13, 0xbfb8aa3b, v5
	v_add_f32_e32 v12, 1.0, v12
	v_rcp_f32_e32 v12, v12
	v_exp_f32_e32 v13, v13
	v_mul_f32_e32 v12, v4, v12
	v_add_f32_e32 v13, 1.0, v13
	v_rcp_f32_e32 v13, v13
	v_mul_f32_e32 v14, 0xbfb8aa3b, v6
	v_mul_f32_e32 v13, v5, v13
	v_exp_f32_e32 v14, v14
	v_mul_f32_e32 v15, 0xbfb8aa3b, v7
	v_add_f32_e32 v14, 1.0, v14
	v_rcp_f32_e32 v14, v14
	v_exp_f32_e32 v15, v15
	v_mul_f32_e32 v14, v6, v14
	v_add_f32_e32 v15, 1.0, v15
	v_rcp_f32_e32 v15, v15
; #define LAS __attribute__((address_space(3)))
; DI unsigned pk2(float lo, float hi) { f32x2 v = {lo, hi}; bf16x2_t b = __builtin_convertvector(v, bf16x2_t); return __builtin_bit_cast(unsigned, b); }
;     DI void operator()(const f32x4 (&acc)[2][2][4][2], const Unit& u, int wr, int wc, int fr, int fq, const LAS unsigned char* slot) const {
;     ...
;         for (int bj = 0; bj < 2; ++bj) {
;             float lbv[8];
;             const int cin = cin0 + bj * HALF;
;             { const int lc = bj * HALF + wc * 32 + 8 * fq; const f32x4 a = *(const LAS f32x4*)(slot + 2048 + 4 * lc), b = *(const LAS f32x4*)(slot + 2048 + 4 * lc + 16);
; #pragma unroll
;               for (int j = 0; j < 4; ++j) { lbv[j] = (cls == 2) ? a[j] : 0.f; lbv[4 + j] = (cls == 2) ? b[j] : 0.f; } }
;             bf16* colp = base + (size_t)(cin >> hs) * MROWS * pitch + (cin & ((1 << hs) - 1));
;             float csv[8];
;             { const int lc = bj * HALF + wc * 32 + 8 * fq; const f32x4 a = *(const LAS f32x4*)(slot + 1024 + 4 * lc), b = *(const LAS f32x4*)(slot + 1024 + 4 * lc + 16);
; #pragma unroll
;               for (int j = 0; j < 4; ++j) { csv[j] = a[j]; csv[4 + j] = b[j]; }
;               if (cls >= 2) {
; #pragma unroll
;                   for (int j = 0; j < 8; ++j) csv[j] *= -1.4426950408889634f; } }
; #pragma unroll
;             for (int ai = 0; ai < 2; ++ai)
; #pragma unroll
;                 for (int m = 0; m < 4; ++m) { const int rr = row0 + ai * HALF + m * 16; const size_t ro = (size_t)rr * pitch; float v[8]; const float rs = rsv[ai][m];
; #pragma unroll
;                     for (int j = 0; j < 8; ++j) v[j] = (float)__builtin_bit_cast(i32x4, acc[ai][bj][m][j >> 2])[j & 3] * (rs * csv[j]);
;                     if (cls != 0) {
; #pragma unroll
;                         for (int j = 0; j < 8; ++j) { if (cls == 1) v[j] *= sigmoidf_(v[j]); else v[j] = __builtin_amdgcn_rcpf(1.0f + __builtin_amdgcn_exp2f(v[j])); }
;                         if (cls == 2) {
; #pragma unroll
;                             for (int j = 0; j < 8; ++j) { const float l = lbv[j]; v[j] = __builtin_amdgcn_logf(l + (1.0f - l) * v[j]); } }
;                     }
;                     u32x4 w; w.x = pk2(v[0], v[1]); w.y = pk2(v[2], v[3]); w.z = pk2(v[4], v[5]); w.w = pk2(v[6], v[7]);
;                     *(u32x4*)(colp + ro) = w; }
	v_mul_f32_e32 v16, 0xbfb8aa3b, v8
	v_mul_f32_e32 v15, v7, v15
	v_exp_f32_e32 v16, v16
	v_mul_f32_e32 v17, 0xbfb8aa3b, v9
	v_add_f32_e32 v16, 1.0, v16
	v_rcp_f32_e32 v16, v16
	v_exp_f32_e32 v17, v17
	v_mul_f32_e32 v16, v8, v16
	v_add_f32_e32 v17, 1.0, v17
	v_rcp_f32_e32 v17, v17
	v_add_u32_e32 v2, 0x80, v197
	v_mul_f32_e32 v17, v9, v17
	v_mad_i64_i32 v[114:115], s[44:45], s36, v2, 0
	v_cvt_pk_bf16_f32 v2, v10, v11
	v_cvt_pk_bf16_f32 v3, v12, v13
	v_cvt_pk_bf16_f32 v4, v14, v15
	v_cvt_pk_bf16_f32 v5, v16, v17
	v_lshl_add_u64 v[6:7], v[114:115], 1, v[180:181]
	global_store_dwordx4 v[6:7], v[2:5], off
	v_mov_b32_e32 v8, v159
	v_pk_mul_f32 v[6:7], v[8:9], v[178:179] op_sel_hi:[0,1]
	v_cvt_f32_i32_e32 v3, v111
	v_cvt_f32_i32_e32 v2, v110
	v_cvt_f32_i32_e32 v5, v113
	v_cvt_f32_i32_e32 v4, v112
	v_cvt_f32_i32_e32 v11, v105
	v_pk_mul_f32 v[2:3], v[6:7], v[2:3]
	v_pk_mul_f32 v[6:7], v[8:9], v[176:177] op_sel_hi:[0,1]
	v_pk_mul_f32 v[4:5], v[6:7], v[4:5]
	v_cvt_f32_i32_e32 v7, v103
	v_cvt_f32_i32_e32 v6, v102
	v_cvt_f32_i32_e32 v10, v104
	v_pk_mul_f32 v[12:13], v[8:9], v[174:175] op_sel_hi:[0,1]
	v_pk_mul_f32 v[8:9], v[8:9], v[172:173] op_sel_hi:[0,1]
	v_pk_mul_f32 v[6:7], v[12:13], v[6:7]
	v_pk_mul_f32 v[8:9], v[8:9], v[10:11]
	v_mul_f32_e32 v10, 0xbfb8aa3b, v2
	v_exp_f32_e32 v10, v10
	v_mul_f32_e32 v11, 0xbfb8aa3b, v3
	v_add_f32_e32 v10, 1.0, v10
	v_rcp_f32_e32 v10, v10
	v_exp_f32_e32 v11, v11
	v_mul_f32_e32 v10, v2, v10
	v_add_f32_e32 v11, 1.0, v11
	v_rcp_f32_e32 v11, v11
	v_mul_f32_e32 v12, 0xbfb8aa3b, v4
	v_mul_f32_e32 v11, v3, v11
	v_exp_f32_e32 v12, v12
	v_mul_f32_e32 v13, 0xbfb8aa3b, v5
	v_add_f32_e32 v12, 1.0, v12
	v_rcp_f32_e32 v12, v12
	v_exp_f32_e32 v13, v13
	v_mul_f32_e32 v12, v4, v12
	v_add_f32_e32 v13, 1.0, v13
	v_rcp_f32_e32 v13, v13
	v_mul_f32_e32 v14, 0xbfb8aa3b, v6
	v_mul_f32_e32 v13, v5, v13
	v_exp_f32_e32 v14, v14
	v_mul_f32_e32 v15, 0xbfb8aa3b, v7
	v_add_f32_e32 v14, 1.0, v14
	v_rcp_f32_e32 v14, v14
	v_exp_f32_e32 v15, v15
	v_mul_f32_e32 v14, v6, v14
	v_add_f32_e32 v15, 1.0, v15
	v_rcp_f32_e32 v15, v15
	v_mul_f32_e32 v16, 0xbfb8aa3b, v8
	v_mul_f32_e32 v15, v7, v15
	v_exp_f32_e32 v16, v16
	v_mul_f32_e32 v17, 0xbfb8aa3b, v9
	v_add_f32_e32 v16, 1.0, v16
	v_rcp_f32_e32 v16, v16
	v_exp_f32_e32 v17, v17
	v_mul_f32_e32 v16, v8, v16
	v_add_f32_e32 v17, 1.0, v17
	v_rcp_f32_e32 v17, v17
	v_add_u32_e32 v2, 0x90, v197
	v_mul_f32_e32 v17, v9, v17
	v_mad_i64_i32 v[102:103], s[44:45], s36, v2, 0
	v_cvt_pk_bf16_f32 v2, v10, v11
	v_cvt_pk_bf16_f32 v3, v12, v13
	v_cvt_pk_bf16_f32 v4, v14, v15
	v_cvt_pk_bf16_f32 v5, v16, v17
	v_lshl_add_u64 v[6:7], v[102:103], 1, v[180:181]
	global_store_dwordx4 v[6:7], v[2:5], off
	v_pk_mul_f32 v[6:7], v[156:157], v[178:179] op_sel_hi:[0,1]
	v_cvt_f32_i32_e32 v9, v93
	v_cvt_f32_i32_e32 v3, v95
	v_cvt_f32_i32_e32 v2, v94
	v_cvt_f32_i32_e32 v5, v97
	v_cvt_f32_i32_e32 v4, v96
	v_cvt_f32_i32_e32 v8, v92
	v_pk_mul_f32 v[2:3], v[6:7], v[2:3]
	v_pk_mul_f32 v[6:7], v[156:157], v[176:177] op_sel_hi:[0,1]
	v_pk_mul_f32 v[4:5], v[6:7], v[4:5]
	v_cvt_f32_i32_e32 v7, v91
	v_cvt_f32_i32_e32 v6, v90
	v_pk_mul_f32 v[10:11], v[156:157], v[174:175] op_sel_hi:[0,1]
	v_pk_mul_f32 v[6:7], v[10:11], v[6:7]
	v_pk_mul_f32 v[10:11], v[156:157], v[172:173] op_sel_hi:[0,1]
	v_pk_mul_f32 v[8:9], v[10:11], v[8:9]
	v_mul_f32_e32 v10, 0xbfb8aa3b, v2
	v_exp_f32_e32 v10, v10
	v_mul_f32_e32 v11, 0xbfb8aa3b, v3
	v_add_f32_e32 v10, 1.0, v10
	v_rcp_f32_e32 v10, v10
	v_exp_f32_e32 v11, v11
	v_mul_f32_e32 v10, v2, v10
	v_add_f32_e32 v11, 1.0, v11
	v_rcp_f32_e32 v11, v11
	v_mul_f32_e32 v12, 0xbfb8aa3b, v4
	v_mul_f32_e32 v11, v3, v11
	v_exp_f32_e32 v12, v12
	v_mul_f32_e32 v13, 0xbfb8aa3b, v5
	v_add_f32_e32 v12, 1.0, v12
	v_rcp_f32_e32 v12, v12
	v_exp_f32_e32 v13, v13
	v_mul_f32_e32 v12, v4, v12
	v_add_f32_e32 v13, 1.0, v13
	v_rcp_f32_e32 v13, v13
	v_mul_f32_e32 v14, 0xbfb8aa3b, v6
	v_mul_f32_e32 v13, v5, v13
	v_exp_f32_e32 v14, v14
	v_mul_f32_e32 v15, 0xbfb8aa3b, v7
	v_add_f32_e32 v14, 1.0, v14
	v_rcp_f32_e32 v14, v14
	v_exp_f32_e32 v15, v15
	v_mul_f32_e32 v14, v6, v14
	v_add_f32_e32 v15, 1.0, v15
	v_rcp_f32_e32 v15, v15
	v_mul_f32_e32 v16, 0xbfb8aa3b, v8
	v_mul_f32_e32 v15, v7, v15
	v_exp_f32_e32 v16, v16
	v_mul_f32_e32 v17, 0xbfb8aa3b, v9
	v_add_f32_e32 v16, 1.0, v16
	v_rcp_f32_e32 v16, v16
	v_exp_f32_e32 v17, v17
	v_mul_f32_e32 v16, v8, v16
	v_add_f32_e32 v17, 1.0, v17
	v_rcp_f32_e32 v17, v17
	v_add_u32_e32 v2, 0xa0, v197
	v_mul_f32_e32 v17, v9, v17
	v_mad_i64_i32 v[90:91], s[44:45], s36, v2, 0
	v_cvt_pk_bf16_f32 v2, v10, v11
	v_cvt_pk_bf16_f32 v3, v12, v13
	v_cvt_pk_bf16_f32 v4, v14, v15
	v_cvt_pk_bf16_f32 v5, v16, v17
	v_lshl_add_u64 v[6:7], v[90:91], 1, v[180:181]
	global_store_dwordx4 v[6:7], v[2:5], off
	v_mov_b32_e32 v8, v157
	v_pk_mul_f32 v[6:7], v[8:9], v[178:179] op_sel_hi:[0,1]
	v_cvt_f32_i32_e32 v3, v87
	v_cvt_f32_i32_e32 v2, v86
	v_cvt_f32_i32_e32 v5, v89
	v_cvt_f32_i32_e32 v4, v88
	v_cvt_f32_i32_e32 v11, v85
	v_pk_mul_f32 v[2:3], v[6:7], v[2:3]
	v_pk_mul_f32 v[6:7], v[8:9], v[176:177] op_sel_hi:[0,1]
	v_pk_mul_f32 v[4:5], v[6:7], v[4:5]
	v_cvt_f32_i32_e32 v7, v83
	v_cvt_f32_i32_e32 v6, v82
	v_cvt_f32_i32_e32 v10, v84
	v_pk_mul_f32 v[12:13], v[8:9], v[174:175] op_sel_hi:[0,1]
	v_pk_mul_f32 v[8:9], v[8:9], v[172:173] op_sel_hi:[0,1]
	v_pk_mul_f32 v[6:7], v[12:13], v[6:7]
	v_pk_mul_f32 v[8:9], v[8:9], v[10:11]
	v_mul_f32_e32 v10, 0xbfb8aa3b, v2
	v_exp_f32_e32 v10, v10
	v_mul_f32_e32 v11, 0xbfb8aa3b, v3
	v_add_f32_e32 v10, 1.0, v10
	v_rcp_f32_e32 v10, v10
	v_exp_f32_e32 v11, v11
	v_mul_f32_e32 v10, v2, v10
	v_add_f32_e32 v11, 1.0, v11
	v_rcp_f32_e32 v11, v11
	v_mul_f32_e32 v12, 0xbfb8aa3b, v4
	v_mul_f32_e32 v11, v3, v11
	v_exp_f32_e32 v12, v12
	v_mul_f32_e32 v13, 0xbfb8aa3b, v5
	v_add_f32_e32 v12, 1.0, v12
	v_rcp_f32_e32 v12, v12
	v_exp_f32_e32 v13, v13
	v_mul_f32_e32 v12, v4, v12
	v_add_f32_e32 v13, 1.0, v13
	v_rcp_f32_e32 v13, v13
	v_mul_f32_e32 v14, 0xbfb8aa3b, v6
	v_mul_f32_e32 v13, v5, v13
	v_exp_f32_e32 v14, v14
	v_mul_f32_e32 v15, 0xbfb8aa3b, v7
	v_add_f32_e32 v14, 1.0, v14
	v_rcp_f32_e32 v14, v14
	v_exp_f32_e32 v15, v15
	v_mul_f32_e32 v14, v6, v14
	v_add_f32_e32 v15, 1.0, v15
	v_rcp_f32_e32 v15, v15
	v_mul_f32_e32 v16, 0xbfb8aa3b, v8
	v_mul_f32_e32 v15, v7, v15
	v_exp_f32_e32 v16, v16
	v_mul_f32_e32 v17, 0xbfb8aa3b, v9
	v_add_f32_e32 v16, 1.0, v16
	v_rcp_f32_e32 v16, v16
	v_exp_f32_e32 v17, v17
	v_mul_f32_e32 v16, v8, v16
	v_add_f32_e32 v17, 1.0, v17
	v_rcp_f32_e32 v17, v17
	s_mov_b64 s[44:45], 0
	v_mul_f32_e32 v17, v9, v17
	v_add_u32_e32 v2, 0xb0, v197
	v_mad_i64_i32 v[92:93], s[36:37], s36, v2, 0
	v_cvt_pk_bf16_f32 v2, v10, v11
	v_cvt_pk_bf16_f32 v3, v12, v13
	v_cvt_pk_bf16_f32 v4, v14, v15
	v_cvt_pk_bf16_f32 v5, v16, v17
	v_lshl_add_u64 v[10:11], v[92:93], 1, v[180:181]
	global_store_dwordx4 v[10:11], v[2:5], off
	ds_read_b128 v[6:9], v195 offset:1536
	ds_read_b128 v[2:5], v195 offset:1552
	ds_read_b128 v[86:89], v195 offset:2560
	ds_read_b128 v[82:85], v195 offset:2576
	v_mov_b32_e32 v104, v168
	v_mov_b32_e32 v105, v168
	s_waitcnt lgkmcnt(0)
; DI unsigned pk2(float lo, float hi) { f32x2 v = {lo, hi}; bf16x2_t b = __builtin_convertvector(v, bf16x2_t); return __builtin_bit_cast(unsigned, b); }
; DI float sigmoidf_(float x) { return __builtin_amdgcn_rcpf(1.0f + __expf(-x)); }
;     DI void operator()(const f32x4 (&acc)[2][2][4][2], const Unit& u, int wr, int wc, int fr, int fq, const LAS unsigned char* slot) const {
;     ...
; #pragma unroll
;             for (int ai = 0; ai < 2; ++ai)
; #pragma unroll
;                 for (int m = 0; m < 4; ++m) { const int rr = row0 + ai * HALF + m * 16; const size_t ro = (size_t)rr * pitch; float v[8]; const float rs = rsv[ai][m];
; #pragma unroll
;                     for (int j = 0; j < 8; ++j) v[j] = (float)__builtin_bit_cast(i32x4, acc[ai][bj][m][j >> 2])[j & 3] * (rs * csv[j]);
;                     if (cls != 0) {
; #pragma unroll
;                         for (int j = 0; j < 8; ++j) { if (cls == 1) v[j] *= sigmoidf_(v[j]); else v[j] = __builtin_amdgcn_rcpf(1.0f + __builtin_amdgcn_exp2f(v[j])); }
;                         if (cls == 2) {
; #pragma unroll
;                             for (int j = 0; j < 8; ++j) { const float l = lbv[j]; v[j] = __builtin_amdgcn_logf(l + (1.0f - l) * v[j]); } }
;                     }
;                     u32x4 w; w.x = pk2(v[0], v[1]); w.y = pk2(v[2], v[3]); w.z = pk2(v[4], v[5]); w.w = pk2(v[6], v[7]);
;                     *(u32x4*)(colp + ro) = w; }
	v_pk_mul_f32 v[14:15], v[2:3], s[26:27] op_sel_hi:[1,0]
	v_pk_mul_f32 v[16:17], v[4:5], s[26:27] op_sel_hi:[1,0]
	v_cndmask_b32_e64 v97, v3, v15, s[38:39]
	v_cndmask_b32_e64 v96, v2, v14, s[38:39]
	v_cvt_f32_i32_e32 v3, v79
	v_cvt_f32_i32_e32 v2, v78
	v_pk_mul_f32 v[10:11], v[6:7], s[26:27] op_sel_hi:[1,0]
	v_cndmask_b32_e64 v95, v5, v17, s[38:39]
	v_cndmask_b32_e64 v94, v4, v16, s[38:39]
	v_cvt_f32_i32_e32 v5, v81
	v_cvt_f32_i32_e32 v4, v80
	v_pk_mul_f32 v[12:13], v[8:9], s[26:27] op_sel_hi:[1,0]
	v_cndmask_b32_e64 v101, v7, v11, s[38:39]
	v_cndmask_b32_e64 v100, v6, v10, s[38:39]
	v_cndmask_b32_e64 v99, v9, v13, s[38:39]
	v_cndmask_b32_e64 v98, v8, v12, s[38:39]
	v_pk_mul_f32 v[6:7], v[104:105], v[100:101]
	v_cvt_f32_i32_e32 v9, v77
	v_pk_mul_f32 v[2:3], v[6:7], v[2:3]
	v_pk_mul_f32 v[6:7], v[104:105], v[98:99]
	v_cvt_f32_i32_e32 v8, v76
	v_pk_mul_f32 v[4:5], v[6:7], v[4:5]
	v_cvt_f32_i32_e32 v7, v75
	v_cvt_f32_i32_e32 v6, v74
	v_pk_mul_f32 v[10:11], v[104:105], v[96:97]
	v_pk_mul_f32 v[6:7], v[10:11], v[6:7]
	v_pk_mul_f32 v[10:11], v[104:105], v[94:95]
	v_pk_mul_f32 v[8:9], v[10:11], v[8:9]
	v_mul_f32_e32 v10, 0xbfb8aa3b, v2
	v_exp_f32_e32 v10, v10
	v_mul_f32_e32 v11, 0xbfb8aa3b, v3
	v_add_f32_e32 v10, 1.0, v10
	v_rcp_f32_e32 v10, v10
	v_exp_f32_e32 v11, v11
	v_mul_f32_e32 v10, v2, v10
	v_add_f32_e32 v11, 1.0, v11
	v_rcp_f32_e32 v11, v11
	v_mul_f32_e32 v12, 0xbfb8aa3b, v4
	v_mul_f32_e32 v11, v3, v11
	v_exp_f32_e32 v12, v12
	v_mul_f32_e32 v13, 0xbfb8aa3b, v5
	v_add_f32_e32 v12, 1.0, v12
	v_rcp_f32_e32 v12, v12
	v_exp_f32_e32 v13, v13
	v_mul_f32_e32 v12, v4, v12
	v_add_f32_e32 v13, 1.0, v13
	v_rcp_f32_e32 v13, v13
	v_mul_f32_e32 v14, 0xbfb8aa3b, v6
	v_mul_f32_e32 v13, v5, v13
	v_exp_f32_e32 v14, v14
	v_mul_f32_e32 v15, 0xbfb8aa3b, v7
	v_add_f32_e32 v14, 1.0, v14
	v_rcp_f32_e32 v14, v14
	v_exp_f32_e32 v15, v15
	v_mul_f32_e32 v14, v6, v14
	v_add_f32_e32 v15, 1.0, v15
	v_rcp_f32_e32 v15, v15
	v_mul_f32_e32 v16, 0xbfb8aa3b, v8
	v_mul_f32_e32 v15, v7, v15
	v_exp_f32_e32 v16, v16
	v_mul_f32_e32 v17, 0xbfb8aa3b, v9
	v_add_f32_e32 v16, 1.0, v16
	v_rcp_f32_e32 v16, v16
	v_exp_f32_e32 v17, v17
	v_mul_f32_e32 v16, v8, v16
	v_add_f32_e32 v17, 1.0, v17
	v_rcp_f32_e32 v17, v17
	v_or_b32_e32 v2, 0x80, v196
	v_mul_f32_e32 v17, v9, v17
	s_not_b32 s3, s95
	v_ashrrev_i32_e32 v2, s93, v2
	v_mad_i64_i32 v[2:3], s[36:37], s94, v2, 0
	v_bitop3_b32 v4, v196, s3, v190 bitop3:0xc8
	v_lshl_add_u64 v[2:3], v[2:3], 1, s[42:43]
	v_lshlrev_b32_e32 v150, 1, v4
	v_lshl_add_u64 v[74:75], v[2:3], 0, v[150:151]
	v_cvt_pk_bf16_f32 v2, v10, v11
	v_cvt_pk_bf16_f32 v3, v12, v13
	v_cvt_pk_bf16_f32 v4, v14, v15
	v_cvt_pk_bf16_f32 v5, v16, v17
	v_lshl_add_u64 v[6:7], v[170:171], 1, v[74:75]
	global_store_dwordx4 v[6:7], v[2:5], off
	v_mov_b32_e32 v168, v169
	v_pk_mul_f32 v[6:7], v[168:169], v[100:101]
	v_cvt_f32_i32_e32 v3, v71
	v_cvt_f32_i32_e32 v2, v70
	v_cvt_f32_i32_e32 v5, v73
	v_cvt_f32_i32_e32 v4, v72
	v_cvt_f32_i32_e32 v9, v69
	v_pk_mul_f32 v[2:3], v[6:7], v[2:3]
	v_pk_mul_f32 v[6:7], v[168:169], v[98:99]
	v_cvt_f32_i32_e32 v8, v68
	v_pk_mul_f32 v[4:5], v[6:7], v[4:5]
	v_cvt_f32_i32_e32 v7, v67
	v_cvt_f32_i32_e32 v6, v66
	v_pk_mul_f32 v[10:11], v[168:169], v[96:97]
	v_pk_mul_f32 v[6:7], v[10:11], v[6:7]
	v_pk_mul_f32 v[10:11], v[168:169], v[94:95]
	v_pk_mul_f32 v[8:9], v[10:11], v[8:9]
	v_mul_f32_e32 v10, 0xbfb8aa3b, v2
	v_exp_f32_e32 v10, v10
	v_mul_f32_e32 v11, 0xbfb8aa3b, v3
	v_add_f32_e32 v10, 1.0, v10
	v_rcp_f32_e32 v10, v10
	v_exp_f32_e32 v11, v11
	v_mul_f32_e32 v10, v2, v10
	v_add_f32_e32 v11, 1.0, v11
	v_rcp_f32_e32 v11, v11
	v_mul_f32_e32 v12, 0xbfb8aa3b, v4
	v_mul_f32_e32 v11, v3, v11
	v_exp_f32_e32 v12, v12
	v_mul_f32_e32 v13, 0xbfb8aa3b, v5
	v_add_f32_e32 v12, 1.0, v12
	v_rcp_f32_e32 v12, v12
	v_exp_f32_e32 v13, v13
	v_mul_f32_e32 v12, v4, v12
	v_add_f32_e32 v13, 1.0, v13
	v_rcp_f32_e32 v13, v13
	v_mul_f32_e32 v14, 0xbfb8aa3b, v6
	v_mul_f32_e32 v13, v5, v13
	v_exp_f32_e32 v14, v14
	v_mul_f32_e32 v15, 0xbfb8aa3b, v7
	v_add_f32_e32 v14, 1.0, v14
	v_rcp_f32_e32 v14, v14
	v_exp_f32_e32 v15, v15
	v_mul_f32_e32 v14, v6, v14
	v_add_f32_e32 v15, 1.0, v15
	v_rcp_f32_e32 v15, v15
	v_mul_f32_e32 v16, 0xbfb8aa3b, v8
	v_mul_f32_e32 v15, v7, v15
	v_exp_f32_e32 v16, v16
	v_mul_f32_e32 v17, 0xbfb8aa3b, v9
	v_add_f32_e32 v16, 1.0, v16
	v_rcp_f32_e32 v16, v16
	v_exp_f32_e32 v17, v17
	v_mul_f32_e32 v16, v8, v16
	v_add_f32_e32 v17, 1.0, v17
	v_rcp_f32_e32 v17, v17
	v_cvt_pk_bf16_f32 v2, v10, v11
	v_mul_f32_e32 v17, v9, v17
	v_cvt_pk_bf16_f32 v3, v12, v13
	v_cvt_pk_bf16_f32 v4, v14, v15
	v_cvt_pk_bf16_f32 v5, v16, v17
	v_lshl_add_u64 v[6:7], v[138:139], 1, v[74:75]
	global_store_dwordx4 v[6:7], v[2:5], off
	v_mov_b32_e32 v8, v160
	v_mov_b32_e32 v9, v160
	v_cvt_f32_i32_e32 v3, v63
	v_cvt_f32_i32_e32 v2, v62
	v_cvt_f32_i32_e32 v5, v65
	v_cvt_f32_i32_e32 v4, v64
	v_pk_mul_f32 v[6:7], v[8:9], v[100:101]
	v_cvt_f32_i32_e32 v11, v61
	v_pk_mul_f32 v[2:3], v[6:7], v[2:3]
	v_pk_mul_f32 v[6:7], v[8:9], v[98:99]
	v_cvt_f32_i32_e32 v10, v60
	v_pk_mul_f32 v[4:5], v[6:7], v[4:5]
	v_cvt_f32_i32_e32 v7, v59
	v_cvt_f32_i32_e32 v6, v58
	v_pk_mul_f32 v[12:13], v[8:9], v[96:97]
	v_pk_mul_f32 v[8:9], v[8:9], v[94:95]
	v_pk_mul_f32 v[6:7], v[12:13], v[6:7]
	v_pk_mul_f32 v[8:9], v[8:9], v[10:11]
	v_mul_f32_e32 v10, 0xbfb8aa3b, v2
	v_exp_f32_e32 v10, v10
	v_mul_f32_e32 v11, 0xbfb8aa3b, v3
	v_add_f32_e32 v10, 1.0, v10
	v_rcp_f32_e32 v10, v10
	v_exp_f32_e32 v11, v11
	v_mul_f32_e32 v10, v2, v10
	v_add_f32_e32 v11, 1.0, v11
	v_rcp_f32_e32 v11, v11
	v_mul_f32_e32 v12, 0xbfb8aa3b, v4
	v_mul_f32_e32 v11, v3, v11
	v_exp_f32_e32 v12, v12
	v_mul_f32_e32 v13, 0xbfb8aa3b, v5
	v_add_f32_e32 v12, 1.0, v12
; DI unsigned pk2(float lo, float hi) { f32x2 v = {lo, hi}; bf16x2_t b = __builtin_convertvector(v, bf16x2_t); return __builtin_bit_cast(unsigned, b); }
; DI float sigmoidf_(float x) { return __builtin_amdgcn_rcpf(1.0f + __expf(-x)); }
;     DI void operator()(const f32x4 (&acc)[2][2][4][2], const Unit& u, int wr, int wc, int fr, int fq, const LAS unsigned char* slot) const {
;     ...
;             for (int ai = 0; ai < 2; ++ai)
; #pragma unroll
;                 for (int m = 0; m < 4; ++m) { const int rr = row0 + ai * HALF + m * 16; const size_t ro = (size_t)rr * pitch; float v[8]; const float rs = rsv[ai][m];
; #pragma unroll
;                     for (int j = 0; j < 8; ++j) v[j] = (float)__builtin_bit_cast(i32x4, acc[ai][bj][m][j >> 2])[j & 3] * (rs * csv[j]);
;                     if (cls != 0) {
; #pragma unroll
;                         for (int j = 0; j < 8; ++j) { if (cls == 1) v[j] *= sigmoidf_(v[j]); else v[j] = __builtin_amdgcn_rcpf(1.0f + __builtin_amdgcn_exp2f(v[j])); }
;                         if (cls == 2) {
; #pragma unroll
;                             for (int j = 0; j < 8; ++j) { const float l = lbv[j]; v[j] = __builtin_amdgcn_logf(l + (1.0f - l) * v[j]); } }
;                     }
;                     u32x4 w; w.x = pk2(v[0], v[1]); w.y = pk2(v[2], v[3]); w.z = pk2(v[4], v[5]); w.w = pk2(v[6], v[7]);
;                     *(u32x4*)(colp + ro) = w; }
	v_rcp_f32_e32 v12, v12
	v_exp_f32_e32 v13, v13
	v_mul_f32_e32 v12, v4, v12
	v_add_f32_e32 v13, 1.0, v13
	v_rcp_f32_e32 v13, v13
	v_mul_f32_e32 v14, 0xbfb8aa3b, v6
	v_mul_f32_e32 v13, v5, v13
	v_exp_f32_e32 v14, v14
	v_mul_f32_e32 v15, 0xbfb8aa3b, v7
	v_add_f32_e32 v14, 1.0, v14
	v_rcp_f32_e32 v14, v14
	v_exp_f32_e32 v15, v15
	v_mul_f32_e32 v14, v6, v14
	v_add_f32_e32 v15, 1.0, v15
	v_rcp_f32_e32 v15, v15
	v_mul_f32_e32 v16, 0xbfb8aa3b, v8
	v_mul_f32_e32 v15, v7, v15
	v_exp_f32_e32 v16, v16
	v_mul_f32_e32 v17, 0xbfb8aa3b, v9
	v_add_f32_e32 v16, 1.0, v16
	v_rcp_f32_e32 v16, v16
	v_exp_f32_e32 v17, v17
	v_mul_f32_e32 v16, v8, v16
	v_add_f32_e32 v17, 1.0, v17
	v_rcp_f32_e32 v17, v17
	v_cvt_pk_bf16_f32 v2, v10, v11
	v_mul_f32_e32 v17, v9, v17
	v_cvt_pk_bf16_f32 v3, v12, v13
	v_cvt_pk_bf16_f32 v4, v14, v15
	v_cvt_pk_bf16_f32 v5, v16, v17
	v_lshl_add_u64 v[6:7], v[130:131], 1, v[74:75]
	global_store_dwordx4 v[6:7], v[2:5], off
	v_mov_b32_e32 v160, v161
	v_pk_mul_f32 v[6:7], v[160:161], v[100:101]
	v_cvt_f32_i32_e32 v3, v55
	v_cvt_f32_i32_e32 v2, v54
	v_cvt_f32_i32_e32 v5, v57
	v_cvt_f32_i32_e32 v4, v56
	v_cvt_f32_i32_e32 v9, v53
	v_pk_mul_f32 v[2:3], v[6:7], v[2:3]
	v_pk_mul_f32 v[6:7], v[160:161], v[98:99]
	v_cvt_f32_i32_e32 v8, v52
	v_pk_mul_f32 v[4:5], v[6:7], v[4:5]
	v_cvt_f32_i32_e32 v7, v51
	v_cvt_f32_i32_e32 v6, v50
	v_pk_mul_f32 v[10:11], v[160:161], v[96:97]
	v_pk_mul_f32 v[6:7], v[10:11], v[6:7]
	v_pk_mul_f32 v[10:11], v[160:161], v[94:95]
	v_pk_mul_f32 v[8:9], v[10:11], v[8:9]
	v_mul_f32_e32 v10, 0xbfb8aa3b, v2
	v_exp_f32_e32 v10, v10
	v_mul_f32_e32 v11, 0xbfb8aa3b, v3
	v_add_f32_e32 v10, 1.0, v10
	v_rcp_f32_e32 v10, v10
	v_exp_f32_e32 v11, v11
	v_mul_f32_e32 v10, v2, v10
	v_add_f32_e32 v11, 1.0, v11
	v_rcp_f32_e32 v11, v11
	v_mul_f32_e32 v12, 0xbfb8aa3b, v4
	v_mul_f32_e32 v11, v3, v11
	v_exp_f32_e32 v12, v12
	v_mul_f32_e32 v13, 0xbfb8aa3b, v5
	v_add_f32_e32 v12, 1.0, v12
	v_rcp_f32_e32 v12, v12
	v_exp_f32_e32 v13, v13
	v_mul_f32_e32 v12, v4, v12
	v_add_f32_e32 v13, 1.0, v13
	v_rcp_f32_e32 v13, v13
	v_mul_f32_e32 v14, 0xbfb8aa3b, v6
	v_mul_f32_e32 v13, v5, v13
	v_exp_f32_e32 v14, v14
	v_mul_f32_e32 v15, 0xbfb8aa3b, v7
	v_add_f32_e32 v14, 1.0, v14
	v_rcp_f32_e32 v14, v14
	v_exp_f32_e32 v15, v15
	v_mul_f32_e32 v14, v6, v14
	v_add_f32_e32 v15, 1.0, v15
	v_rcp_f32_e32 v15, v15
	v_mul_f32_e32 v16, 0xbfb8aa3b, v8
	v_mul_f32_e32 v15, v7, v15
	v_exp_f32_e32 v16, v16
	v_mul_f32_e32 v17, 0xbfb8aa3b, v9
	v_add_f32_e32 v16, 1.0, v16
	v_rcp_f32_e32 v16, v16
	v_exp_f32_e32 v17, v17
	v_mul_f32_e32 v16, v8, v16
	v_add_f32_e32 v17, 1.0, v17
	v_rcp_f32_e32 v17, v17
	v_cvt_pk_bf16_f32 v2, v10, v11
	v_mul_f32_e32 v17, v9, v17
	v_cvt_pk_bf16_f32 v3, v12, v13
	v_cvt_pk_bf16_f32 v4, v14, v15
	v_cvt_pk_bf16_f32 v5, v16, v17
	v_lshl_add_u64 v[6:7], v[122:123], 1, v[74:75]
	global_store_dwordx4 v[6:7], v[2:5], off
	v_mov_b32_e32 v8, v158
	v_mov_b32_e32 v9, v158
	v_cvt_f32_i32_e32 v3, v47
	v_cvt_f32_i32_e32 v2, v46
	v_cvt_f32_i32_e32 v5, v49
	v_cvt_f32_i32_e32 v4, v48
	v_pk_mul_f32 v[6:7], v[8:9], v[100:101]
	v_cvt_f32_i32_e32 v11, v45
	v_pk_mul_f32 v[2:3], v[6:7], v[2:3]
	v_pk_mul_f32 v[6:7], v[8:9], v[98:99]
	v_cvt_f32_i32_e32 v10, v44
	v_pk_mul_f32 v[4:5], v[6:7], v[4:5]
	v_cvt_f32_i32_e32 v7, v43
	v_cvt_f32_i32_e32 v6, v42
	v_pk_mul_f32 v[12:13], v[8:9], v[96:97]
	v_pk_mul_f32 v[8:9], v[8:9], v[94:95]
	v_pk_mul_f32 v[6:7], v[12:13], v[6:7]
	v_pk_mul_f32 v[8:9], v[8:9], v[10:11]
	v_mul_f32_e32 v10, 0xbfb8aa3b, v2
	v_exp_f32_e32 v10, v10
	v_mul_f32_e32 v11, 0xbfb8aa3b, v3
	v_add_f32_e32 v10, 1.0, v10
	v_rcp_f32_e32 v10, v10
	v_exp_f32_e32 v11, v11
	v_mul_f32_e32 v10, v2, v10
	v_add_f32_e32 v11, 1.0, v11
	v_rcp_f32_e32 v11, v11
	v_mul_f32_e32 v12, 0xbfb8aa3b, v4
	v_mul_f32_e32 v11, v3, v11
	v_exp_f32_e32 v12, v12
	v_mul_f32_e32 v13, 0xbfb8aa3b, v5
	v_add_f32_e32 v12, 1.0, v12
	v_rcp_f32_e32 v12, v12
	v_exp_f32_e32 v13, v13
	v_mul_f32_e32 v12, v4, v12
	v_add_f32_e32 v13, 1.0, v13
	v_rcp_f32_e32 v13, v13
	v_mul_f32_e32 v14, 0xbfb8aa3b, v6
	v_mul_f32_e32 v13, v5, v13
	v_exp_f32_e32 v14, v14
	v_mul_f32_e32 v15, 0xbfb8aa3b, v7
	v_add_f32_e32 v14, 1.0, v14
	v_rcp_f32_e32 v14, v14
	v_exp_f32_e32 v15, v15
	v_mul_f32_e32 v14, v6, v14
	v_add_f32_e32 v15, 1.0, v15
	v_rcp_f32_e32 v15, v15
	v_mul_f32_e32 v16, 0xbfb8aa3b, v8
	v_mul_f32_e32 v15, v7, v15
	v_exp_f32_e32 v16, v16
	v_mul_f32_e32 v17, 0xbfb8aa3b, v9
	v_add_f32_e32 v16, 1.0, v16
	v_rcp_f32_e32 v16, v16
	v_exp_f32_e32 v17, v17
	v_mul_f32_e32 v16, v8, v16
	v_add_f32_e32 v17, 1.0, v17
	v_rcp_f32_e32 v17, v17
	v_cvt_pk_bf16_f32 v2, v10, v11
	v_mul_f32_e32 v17, v9, v17
	v_cvt_pk_bf16_f32 v3, v12, v13
	v_cvt_pk_bf16_f32 v4, v14, v15
	v_cvt_pk_bf16_f32 v5, v16, v17
	v_lshl_add_u64 v[6:7], v[114:115], 1, v[74:75]
	global_store_dwordx4 v[6:7], v[2:5], off
	v_mov_b32_e32 v158, v159
	v_pk_mul_f32 v[6:7], v[158:159], v[100:101]
	v_cvt_f32_i32_e32 v3, v39
	v_cvt_f32_i32_e32 v2, v38
	v_cvt_f32_i32_e32 v5, v41
	v_cvt_f32_i32_e32 v4, v40
	v_cvt_f32_i32_e32 v9, v37
	v_pk_mul_f32 v[2:3], v[6:7], v[2:3]
	v_pk_mul_f32 v[6:7], v[158:159], v[98:99]
	v_cvt_f32_i32_e32 v8, v36
	v_pk_mul_f32 v[4:5], v[6:7], v[4:5]
	v_cvt_f32_i32_e32 v7, v35
	v_cvt_f32_i32_e32 v6, v34
	v_pk_mul_f32 v[10:11], v[158:159], v[96:97]
	v_pk_mul_f32 v[6:7], v[10:11], v[6:7]
	v_pk_mul_f32 v[10:11], v[158:159], v[94:95]
	v_pk_mul_f32 v[8:9], v[10:11], v[8:9]
	v_mul_f32_e32 v10, 0xbfb8aa3b, v2
	v_exp_f32_e32 v10, v10
	v_mul_f32_e32 v11, 0xbfb8aa3b, v3
	v_add_f32_e32 v10, 1.0, v10
	v_rcp_f32_e32 v10, v10
	v_exp_f32_e32 v11, v11
	v_mul_f32_e32 v10, v2, v10
	v_add_f32_e32 v11, 1.0, v11
	v_rcp_f32_e32 v11, v11
	v_mul_f32_e32 v12, 0xbfb8aa3b, v4
	v_mul_f32_e32 v11, v3, v11
; DI unsigned pk2(float lo, float hi) { f32x2 v = {lo, hi}; bf16x2_t b = __builtin_convertvector(v, bf16x2_t); return __builtin_bit_cast(unsigned, b); }
; DI float sigmoidf_(float x) { return __builtin_amdgcn_rcpf(1.0f + __expf(-x)); }
;     DI void operator()(const f32x4 (&acc)[2][2][4][2], const Unit& u, int wr, int wc, int fr, int fq, const LAS unsigned char* slot) const {
;     ...
;             for (int ai = 0; ai < 2; ++ai)
; #pragma unroll
;                 for (int m = 0; m < 4; ++m) { const int rr = row0 + ai * HALF + m * 16; const size_t ro = (size_t)rr * pitch; float v[8]; const float rs = rsv[ai][m];
; #pragma unroll
;                     for (int j = 0; j < 8; ++j) v[j] = (float)__builtin_bit_cast(i32x4, acc[ai][bj][m][j >> 2])[j & 3] * (rs * csv[j]);
;                     if (cls != 0) {
; #pragma unroll
;                         for (int j = 0; j < 8; ++j) { if (cls == 1) v[j] *= sigmoidf_(v[j]); else v[j] = __builtin_amdgcn_rcpf(1.0f + __builtin_amdgcn_exp2f(v[j])); }
;                         if (cls == 2) {
; #pragma unroll
;                             for (int j = 0; j < 8; ++j) { const float l = lbv[j]; v[j] = __builtin_amdgcn_logf(l + (1.0f - l) * v[j]); } }
;                     }
;                     u32x4 w; w.x = pk2(v[0], v[1]); w.y = pk2(v[2], v[3]); w.z = pk2(v[4], v[5]); w.w = pk2(v[6], v[7]);
;                     *(u32x4*)(colp + ro) = w; }
	v_exp_f32_e32 v12, v12
	v_mul_f32_e32 v13, 0xbfb8aa3b, v5
	v_add_f32_e32 v12, 1.0, v12
	v_rcp_f32_e32 v12, v12
	v_exp_f32_e32 v13, v13
	v_mul_f32_e32 v12, v4, v12
	v_add_f32_e32 v13, 1.0, v13
	v_rcp_f32_e32 v13, v13
	v_mul_f32_e32 v14, 0xbfb8aa3b, v6
	v_mul_f32_e32 v13, v5, v13
	v_exp_f32_e32 v14, v14
	v_mul_f32_e32 v15, 0xbfb8aa3b, v7
	v_add_f32_e32 v14, 1.0, v14
	v_rcp_f32_e32 v14, v14
	v_exp_f32_e32 v15, v15
	v_mul_f32_e32 v14, v6, v14
	v_add_f32_e32 v15, 1.0, v15
	v_rcp_f32_e32 v15, v15
	v_mul_f32_e32 v16, 0xbfb8aa3b, v8
	v_mul_f32_e32 v15, v7, v15
	v_exp_f32_e32 v16, v16
	v_mul_f32_e32 v17, 0xbfb8aa3b, v9
	v_add_f32_e32 v16, 1.0, v16
	v_rcp_f32_e32 v16, v16
	v_exp_f32_e32 v17, v17
	v_mul_f32_e32 v16, v8, v16
	v_add_f32_e32 v17, 1.0, v17
	v_rcp_f32_e32 v17, v17
	v_cvt_pk_bf16_f32 v2, v10, v11
	v_mul_f32_e32 v17, v9, v17
	v_cvt_pk_bf16_f32 v3, v12, v13
	v_cvt_pk_bf16_f32 v4, v14, v15
	v_cvt_pk_bf16_f32 v5, v16, v17
	v_lshl_add_u64 v[6:7], v[102:103], 1, v[74:75]
	global_store_dwordx4 v[6:7], v[2:5], off
	v_mov_b32_e32 v8, v156
	v_mov_b32_e32 v9, v156
	v_cvt_f32_i32_e32 v3, v31
	v_cvt_f32_i32_e32 v2, v30
	v_cvt_f32_i32_e32 v5, v33
	v_cvt_f32_i32_e32 v4, v32
	v_pk_mul_f32 v[6:7], v[8:9], v[100:101]
	v_cvt_f32_i32_e32 v11, v29
	v_pk_mul_f32 v[2:3], v[6:7], v[2:3]
	v_pk_mul_f32 v[6:7], v[8:9], v[98:99]
	v_cvt_f32_i32_e32 v10, v28
	v_pk_mul_f32 v[4:5], v[6:7], v[4:5]
	v_cvt_f32_i32_e32 v7, v27
	v_cvt_f32_i32_e32 v6, v26
	v_pk_mul_f32 v[12:13], v[8:9], v[96:97]
	v_pk_mul_f32 v[8:9], v[8:9], v[94:95]
	v_pk_mul_f32 v[6:7], v[12:13], v[6:7]
	v_pk_mul_f32 v[8:9], v[8:9], v[10:11]
	v_mul_f32_e32 v10, 0xbfb8aa3b, v2
	v_exp_f32_e32 v10, v10
	v_mul_f32_e32 v11, 0xbfb8aa3b, v3
	v_add_f32_e32 v10, 1.0, v10
	v_rcp_f32_e32 v10, v10
	v_exp_f32_e32 v11, v11
	v_mul_f32_e32 v10, v2, v10
	v_add_f32_e32 v11, 1.0, v11
	v_rcp_f32_e32 v11, v11
	v_mul_f32_e32 v12, 0xbfb8aa3b, v4
	v_mul_f32_e32 v11, v3, v11
	v_exp_f32_e32 v12, v12
	v_mul_f32_e32 v13, 0xbfb8aa3b, v5
	v_add_f32_e32 v12, 1.0, v12
	v_rcp_f32_e32 v12, v12
	v_exp_f32_e32 v13, v13
	v_mul_f32_e32 v12, v4, v12
	v_add_f32_e32 v13, 1.0, v13
	v_rcp_f32_e32 v13, v13
	v_mul_f32_e32 v14, 0xbfb8aa3b, v6
	v_mul_f32_e32 v13, v5, v13
	v_exp_f32_e32 v14, v14
	v_mul_f32_e32 v15, 0xbfb8aa3b, v7
	v_add_f32_e32 v14, 1.0, v14
	v_rcp_f32_e32 v14, v14
	v_exp_f32_e32 v15, v15
	v_mul_f32_e32 v14, v6, v14
	v_add_f32_e32 v15, 1.0, v15
	v_rcp_f32_e32 v15, v15
	v_mul_f32_e32 v16, 0xbfb8aa3b, v8
	v_mul_f32_e32 v15, v7, v15
	v_exp_f32_e32 v16, v16
	v_mul_f32_e32 v17, 0xbfb8aa3b, v9
	v_add_f32_e32 v16, 1.0, v16
	v_rcp_f32_e32 v16, v16
	v_exp_f32_e32 v17, v17
	v_mul_f32_e32 v16, v8, v16
	v_add_f32_e32 v17, 1.0, v17
	v_rcp_f32_e32 v17, v17
	v_cvt_pk_bf16_f32 v2, v10, v11
	v_mul_f32_e32 v17, v9, v17
	v_cvt_pk_bf16_f32 v3, v12, v13
	v_cvt_pk_bf16_f32 v4, v14, v15
	v_cvt_pk_bf16_f32 v5, v16, v17
	v_lshl_add_u64 v[6:7], v[90:91], 1, v[74:75]
	global_store_dwordx4 v[6:7], v[2:5], off
	v_mov_b32_e32 v156, v157
	v_pk_mul_f32 v[6:7], v[156:157], v[100:101]
	v_cvt_f32_i32_e32 v3, v23
	v_cvt_f32_i32_e32 v2, v22
	v_cvt_f32_i32_e32 v5, v25
	v_cvt_f32_i32_e32 v4, v24
	v_cvt_f32_i32_e32 v9, v21
	v_pk_mul_f32 v[2:3], v[6:7], v[2:3]
	v_pk_mul_f32 v[6:7], v[156:157], v[98:99]
	v_cvt_f32_i32_e32 v8, v20
	v_pk_mul_f32 v[4:5], v[6:7], v[4:5]
	v_cvt_f32_i32_e32 v7, v19
	v_cvt_f32_i32_e32 v6, v18
	v_pk_mul_f32 v[10:11], v[156:157], v[96:97]
	v_pk_mul_f32 v[6:7], v[10:11], v[6:7]
	v_pk_mul_f32 v[10:11], v[156:157], v[94:95]
	v_pk_mul_f32 v[8:9], v[10:11], v[8:9]
	v_mul_f32_e32 v10, 0xbfb8aa3b, v2
	v_exp_f32_e32 v10, v10
	v_mul_f32_e32 v11, 0xbfb8aa3b, v3
	v_add_f32_e32 v10, 1.0, v10
	v_rcp_f32_e32 v10, v10
	v_exp_f32_e32 v11, v11
	v_mul_f32_e32 v10, v2, v10
	v_add_f32_e32 v11, 1.0, v11
	v_rcp_f32_e32 v11, v11
	v_mul_f32_e32 v12, 0xbfb8aa3b, v4
	v_mul_f32_e32 v11, v3, v11
	v_exp_f32_e32 v12, v12
	v_mul_f32_e32 v13, 0xbfb8aa3b, v5
	v_add_f32_e32 v12, 1.0, v12
	v_rcp_f32_e32 v12, v12
	v_exp_f32_e32 v13, v13
	v_mul_f32_e32 v12, v4, v12
	v_add_f32_e32 v13, 1.0, v13
	v_rcp_f32_e32 v13, v13
	v_mul_f32_e32 v14, 0xbfb8aa3b, v6
	v_mul_f32_e32 v13, v5, v13
	v_exp_f32_e32 v14, v14
	v_mul_f32_e32 v15, 0xbfb8aa3b, v7
	v_add_f32_e32 v14, 1.0, v14
	v_rcp_f32_e32 v14, v14
	v_exp_f32_e32 v15, v15
	v_mul_f32_e32 v14, v6, v14
	v_add_f32_e32 v15, 1.0, v15
	v_rcp_f32_e32 v15, v15
	s_mov_b64 s[34:35], -1
	v_mul_f32_e32 v15, v7, v15
	v_mul_f32_e32 v16, 0xbfb8aa3b, v8
	v_exp_f32_e32 v16, v16
	s_mov_b64 s[6:7], -1
	v_add_f32_e32 v16, 1.0, v16
	v_rcp_f32_e32 v16, v16
	v_mul_f32_e32 v17, 0xbfb8aa3b, v9
	v_mul_f32_e32 v16, v8, v16
	v_exp_f32_e32 v17, v17
	s_mov_b64 s[36:37], 0
	v_add_f32_e32 v17, 1.0, v17
	v_rcp_f32_e32 v17, v17
	v_cvt_pk_bf16_f32 v2, v10, v11
	v_mul_f32_e32 v17, v9, v17
	v_cvt_pk_bf16_f32 v3, v12, v13
	v_cvt_pk_bf16_f32 v4, v14, v15
	v_cvt_pk_bf16_f32 v5, v16, v17
	v_lshl_add_u64 v[6:7], v[92:93], 1, v[74:75]
	s_and_b64 vcc, exec, s[4:5]
	s_mov_b64 s[4:5], -1
	global_store_dwordx4 v[6:7], v[2:5], off
	s_branch .Lepj_join
;     DI void operator()(const f32x4 (&acc)[2][2][4][2], const Unit& u, int wr, int wc, int fr, int fq, const LAS unsigned char* slot) const {
;     ...
;         float rsv[2][4];
; #pragma unroll
;         for (int ai = 0; ai < 2; ++ai)
; #pragma unroll
;             for (int m = 0; m < 4; ++m) rsv[ai][m] = *(const LAS float*)(slot + 4 * (ai * HALF + wr * 64 + m * 16 + fr));
; #pragma unroll
;         for (int bj = 0; bj < 2; ++bj) {
;             float lbv[8];
;             const int cin = cin0 + bj * HALF;
;             { const int lc = bj * HALF + wc * 32 + 8 * fq; const f32x4 a = *(const LAS f32x4*)(slot + 2048 + 4 * lc), b = *(const LAS f32x4*)(slot + 2048 + 4 * lc + 16);
; #pragma unroll
;               for (int j = 0; j < 4; ++j) { lbv[j] = (cls == 2) ? a[j] : 0.f; lbv[4 + j] = (cls == 2) ? b[j] : 0.f; } }
;             bf16* colp = base + (size_t)(cin >> hs) * MROWS * pitch + (cin & ((1 << hs) - 1));
;             float csv[8];
;             { const int lc = bj * HALF + wc * 32 + 8 * fq; const f32x4 a = *(const LAS f32x4*)(slot + 1024 + 4 * lc), b = *(const LAS f32x4*)(slot + 1024 + 4 * lc + 16);
; #pragma unroll
;               for (int j = 0; j < 4; ++j) { csv[j] = a[j]; csv[4 + j] = b[j]; }
;               if (cls >= 2) {
; #pragma unroll
;                   for (int j = 0; j < 8; ++j) csv[j] *= -1.4426950408889634f; } }
; #pragma unroll
;             for (int ai = 0; ai < 2; ++ai)
; #pragma unroll
;                 for (int m = 0; m < 4; ++m) { const int rr = row0 + ai * HALF + m * 16; const size_t ro = (size_t)rr * pitch; float v[8]; const float rs = rsv[ai][m];
; #pragma unroll
;                     for (int j = 0; j < 8; ++j) v[j] = (float)__builtin_bit_cast(i32x4, acc[ai][bj][m][j >> 2])[j & 3] * (rs * csv[j]);
;                     if (cls != 0) {
; #pragma unroll
;                         for (int j = 0; j < 8; ++j) { if (cls == 1) v[j] *= sigmoidf_(v[j]); else v[j] = __builtin_amdgcn_rcpf(1.0f + __builtin_amdgcn_exp2f(v[j])); }
;                         if (cls == 2) {
; #pragma unroll
;                             for (int j = 0; j < 8; ++j) { const float l = lbv[j]; v[j] = __builtin_amdgcn_logf(l + (1.0f - l) * v[j]); } }
;                     }
;                     u32x4 w; w.x = pk2(v[0], v[1]); w.y = pk2(v[2], v[3]); w.z = pk2(v[4], v[5]); w.w = pk2(v[6], v[7]);
;                     *(u32x4*)(colp + ro) = w; }
.Lepj_C:
	s_lshl_b32 s37, s90, 12
	s_and_b32 s37, s37, 0x1000
	s_add_i32 s37, s37, 0
	s_add_i32 s37, s37, 0x21000
	v_mov_b32_e32 v150, v151
	v_add_u32_e32 v14, s37, v182
	v_add_u32_e32 v195, s37, v185
	ds_read2_b32 v[168:169], v14 offset1:16
	ds_read2_b32 v[160:161], v14 offset0:32 offset1:48
	ds_read2_b32 v[158:159], v14 offset0:128 offset1:144
	ds_read_b128 v[10:13], v195 offset:1024
	ds_read2_b32 v[156:157], v14 offset0:160 offset1:176
	ds_read_b128 v[14:17], v195 offset:1040
	ds_read_b128 v[106:109], v195 offset:2048
	ds_read_b128 v[98:101], v195 offset:2064
	v_cvt_f32_i32_e32 v3, v3
	v_cvt_f32_i32_e32 v2, v2
	s_waitcnt lgkmcnt(0)
	v_pk_mul_f32 v[170:171], v[10:11], s[26:27] op_sel_hi:[1,0]
	v_cvt_f32_i32_e32 v5, v5
	v_cvt_f32_i32_e32 v4, v4
	v_pk_mul_f32 v[176:177], v[12:13], s[26:27] op_sel_hi:[1,0]
	v_cndmask_b32_e64 v179, v11, v171, s[38:39]
	v_cndmask_b32_e64 v178, v10, v170, s[38:39]
	v_cvt_f32_i32_e32 v7, v7
	v_cvt_f32_i32_e32 v6, v6
	v_pk_mul_f32 v[174:175], v[14:15], s[26:27] op_sel_hi:[1,0]
	v_cndmask_b32_e64 v177, v13, v177, s[38:39]
	v_cndmask_b32_e64 v176, v12, v176, s[38:39]
	v_pk_mul_f32 v[10:11], v[168:169], v[178:179] op_sel_hi:[0,1]
	v_cvt_f32_i32_e32 v9, v9
	v_cvt_f32_i32_e32 v8, v8
	v_pk_mul_f32 v[172:173], v[16:17], s[26:27] op_sel_hi:[1,0]
	v_cndmask_b32_e64 v175, v15, v175, s[38:39]
	v_cndmask_b32_e64 v174, v14, v174, s[38:39]
	v_pk_mul_f32 v[2:3], v[10:11], v[2:3]
	v_pk_mul_f32 v[10:11], v[168:169], v[176:177] op_sel_hi:[0,1]
	v_cndmask_b32_e64 v173, v17, v173, s[38:39]
	v_cndmask_b32_e64 v172, v16, v172, s[38:39]
	v_pk_mul_f32 v[4:5], v[10:11], v[4:5]
	v_pk_mul_f32 v[10:11], v[168:169], v[174:175] op_sel_hi:[0,1]
	v_pk_mul_f32 v[6:7], v[10:11], v[6:7]
	v_pk_mul_f32 v[10:11], v[168:169], v[172:173] op_sel_hi:[0,1]
	v_pk_mul_f32 v[8:9], v[10:11], v[8:9]
	v_exp_f32_e32 v10, v2
	v_exp_f32_e32 v11, v3
	v_add_f32_e32 v10, 1.0, v10
	v_rcp_f32_e32 v10, v10
	v_add_f32_e32 v11, 1.0, v11
	v_rcp_f32_e32 v11, v11
	v_exp_f32_e32 v12, v4
	v_exp_f32_e32 v13, v5
	v_add_f32_e32 v12, 1.0, v12
	v_rcp_f32_e32 v12, v12
	v_add_f32_e32 v13, 1.0, v13
	v_rcp_f32_e32 v13, v13
	v_exp_f32_e32 v14, v6
	v_exp_f32_e32 v15, v7
	v_add_f32_e32 v14, 1.0, v14
	v_rcp_f32_e32 v14, v14
	v_add_f32_e32 v15, 1.0, v15
	v_rcp_f32_e32 v15, v15
	v_exp_f32_e32 v16, v8
	v_exp_f32_e32 v17, v9
	v_add_f32_e32 v16, 1.0, v16
	v_rcp_f32_e32 v16, v16
	v_add_f32_e32 v17, 1.0, v17
	v_rcp_f32_e32 v17, v17
	v_sub_f32_e32 v170, 1.0, v106
	v_fma_f32 v10, v170, v10, v106
	v_sub_f32_e32 v170, 1.0, v107
	v_fma_f32 v11, v170, v11, v107
	v_sub_f32_e32 v170, 1.0, v108
	v_fma_f32 v12, v170, v12, v108
	v_sub_f32_e32 v170, 1.0, v109
	v_fma_f32 v13, v170, v13, v109
	v_sub_f32_e32 v170, 1.0, v98
	v_fma_f32 v14, v170, v14, v98
	v_sub_f32_e32 v170, 1.0, v99
	v_fma_f32 v15, v170, v15, v99
	v_sub_f32_e32 v170, 1.0, v100
	v_fma_f32 v16, v170, v16, v100
	v_sub_f32_e32 v170, 1.0, v101
	v_fma_f32 v17, v170, v17, v101
	v_log_f32_e32 v10, v10
	v_log_f32_e32 v11, v11
	v_log_f32_e32 v12, v12
	v_log_f32_e32 v13, v13
	v_log_f32_e32 v14, v14
	v_log_f32_e32 v15, v15
	v_log_f32_e32 v16, v16
	v_log_f32_e32 v17, v17
	v_lshl_or_b32 v2, s95, 8, v184
	s_lshl_b32 s6, s94, 8
	v_add_u32_e32 v196, s3, v2
	s_lshl_b32 s3, s42, 1
	s_add_u32 s42, s76, s3
	s_addc_u32 s43, s77, 0
	s_mul_i32 s94, s36, 0x4100
	s_lshl_b32 s95, -1, s93
	v_ashrrev_i32_e32 v2, s93, v196
	v_add3_u32 v197, s6, v167, v150
	v_mad_i64_i32 v[2:3], s[6:7], s94, v2, 0
	v_bitop3_b32 v4, v196, s95, v196 bitop3:0x30
	v_lshl_add_u64 v[2:3], v[2:3], 1, s[42:43]
	v_lshlrev_b32_e32 v150, 1, v4
	v_lshl_add_u64 v[180:181], v[2:3], 0, v[150:151]
	v_mad_i64_i32 v[170:171], s[6:7], s36, v197, 0
	v_cvt_pk_bf16_f32 v2, v10, v11
	v_cvt_pk_bf16_f32 v3, v12, v13
	v_cvt_pk_bf16_f32 v4, v14, v15
	v_cvt_pk_bf16_f32 v5, v16, v17
	v_lshl_add_u64 v[6:7], v[170:171], 1, v[180:181]
	global_store_dwordx4 v[6:7], v[2:5], off
	v_mov_b32_e32 v8, v169
	v_pk_mul_f32 v[6:7], v[8:9], v[178:179] op_sel_hi:[0,1]
	v_cvt_f32_i32_e32 v3, v143
	v_cvt_f32_i32_e32 v2, v142
	v_cvt_f32_i32_e32 v5, v145
	v_cvt_f32_i32_e32 v4, v144
	v_cvt_f32_i32_e32 v11, v141
	v_pk_mul_f32 v[2:3], v[6:7], v[2:3]
	v_pk_mul_f32 v[6:7], v[8:9], v[176:177] op_sel_hi:[0,1]
	v_cvt_f32_i32_e32 v10, v140
	v_pk_mul_f32 v[4:5], v[6:7], v[4:5]
	v_cvt_f32_i32_e32 v7, v139
	v_cvt_f32_i32_e32 v6, v138
	v_pk_mul_f32 v[12:13], v[8:9], v[174:175] op_sel_hi:[0,1]
	v_pk_mul_f32 v[8:9], v[8:9], v[172:173] op_sel_hi:[0,1]
	v_pk_mul_f32 v[8:9], v[8:9], v[10:11]
	v_pk_mul_f32 v[6:7], v[12:13], v[6:7]
	v_exp_f32_e32 v10, v2
	v_exp_f32_e32 v11, v3
	v_add_f32_e32 v10, 1.0, v10
	v_rcp_f32_e32 v10, v10
	v_add_f32_e32 v11, 1.0, v11
	v_rcp_f32_e32 v11, v11
	v_exp_f32_e32 v12, v4
	v_exp_f32_e32 v13, v5
	v_add_f32_e32 v12, 1.0, v12
	v_rcp_f32_e32 v12, v12
	v_add_f32_e32 v13, 1.0, v13
	v_rcp_f32_e32 v13, v13
	v_exp_f32_e32 v14, v6
	v_exp_f32_e32 v15, v7
	v_add_f32_e32 v14, 1.0, v14
	v_rcp_f32_e32 v14, v14
	v_add_f32_e32 v15, 1.0, v15
	v_rcp_f32_e32 v15, v15
	v_exp_f32_e32 v16, v8
	v_exp_f32_e32 v17, v9
	v_add_f32_e32 v16, 1.0, v16
	v_rcp_f32_e32 v16, v16
	v_add_f32_e32 v17, 1.0, v17
	v_rcp_f32_e32 v17, v17
	v_sub_f32_e32 v138, 1.0, v106
	v_fma_f32 v10, v138, v10, v106
	v_sub_f32_e32 v138, 1.0, v107
	v_fma_f32 v11, v138, v11, v107
	v_sub_f32_e32 v138, 1.0, v108
	v_fma_f32 v12, v138, v12, v108
	v_sub_f32_e32 v138, 1.0, v109
	v_fma_f32 v13, v138, v13, v109
	v_sub_f32_e32 v138, 1.0, v98
	v_fma_f32 v14, v138, v14, v98
	v_sub_f32_e32 v138, 1.0, v99
	v_fma_f32 v15, v138, v15, v99
	v_sub_f32_e32 v138, 1.0, v100
	v_fma_f32 v16, v138, v16, v100
	v_sub_f32_e32 v138, 1.0, v101
	v_fma_f32 v17, v138, v17, v101
	v_log_f32_e32 v10, v10
; DI unsigned pk2(float lo, float hi) { f32x2 v = {lo, hi}; bf16x2_t b = __builtin_convertvector(v, bf16x2_t); return __builtin_bit_cast(unsigned, b); }
; DI float sigmoidf_(float x) { return __builtin_amdgcn_rcpf(1.0f + __expf(-x)); }
;     DI void operator()(const f32x4 (&acc)[2][2][4][2], const Unit& u, int wr, int wc, int fr, int fq, const LAS unsigned char* slot) const {
;     ...
;             for (int ai = 0; ai < 2; ++ai)
; #pragma unroll
;                 for (int m = 0; m < 4; ++m) { const int rr = row0 + ai * HALF + m * 16; const size_t ro = (size_t)rr * pitch; float v[8]; const float rs = rsv[ai][m];
; #pragma unroll
;                     for (int j = 0; j < 8; ++j) v[j] = (float)__builtin_bit_cast(i32x4, acc[ai][bj][m][j >> 2])[j & 3] * (rs * csv[j]);
;                     if (cls != 0) {
; #pragma unroll
;                         for (int j = 0; j < 8; ++j) { if (cls == 1) v[j] *= sigmoidf_(v[j]); else v[j] = __builtin_amdgcn_rcpf(1.0f + __builtin_amdgcn_exp2f(v[j])); }
;                         if (cls == 2) {
; #pragma unroll
;                             for (int j = 0; j < 8; ++j) { const float l = lbv[j]; v[j] = __builtin_amdgcn_logf(l + (1.0f - l) * v[j]); } }
;                     }
;                     u32x4 w; w.x = pk2(v[0], v[1]); w.y = pk2(v[2], v[3]); w.z = pk2(v[4], v[5]); w.w = pk2(v[6], v[7]);
;                     *(u32x4*)(colp + ro) = w; }
	v_log_f32_e32 v11, v11
	v_log_f32_e32 v12, v12
	v_log_f32_e32 v13, v13
	v_log_f32_e32 v14, v14
	v_log_f32_e32 v15, v15
	v_log_f32_e32 v16, v16
	v_log_f32_e32 v17, v17
	s_mov_b64 s[62:63], 0
	v_add_u32_e32 v2, 16, v197
	v_mad_i64_i32 v[138:139], s[44:45], s36, v2, 0
	v_cvt_pk_bf16_f32 v2, v10, v11
	v_cvt_pk_bf16_f32 v3, v12, v13
	v_cvt_pk_bf16_f32 v4, v14, v15
	v_cvt_pk_bf16_f32 v5, v16, v17
	v_lshl_add_u64 v[6:7], v[138:139], 1, v[180:181]
	global_store_dwordx4 v[6:7], v[2:5], off
	v_pk_mul_f32 v[6:7], v[160:161], v[178:179] op_sel_hi:[0,1]
	v_cvt_f32_i32_e32 v9, v133
	v_cvt_f32_i32_e32 v3, v135
	v_cvt_f32_i32_e32 v2, v134
	v_cvt_f32_i32_e32 v5, v137
	v_cvt_f32_i32_e32 v4, v136
	v_cvt_f32_i32_e32 v8, v132
	v_pk_mul_f32 v[2:3], v[6:7], v[2:3]
	v_pk_mul_f32 v[6:7], v[160:161], v[176:177] op_sel_hi:[0,1]
	v_pk_mul_f32 v[4:5], v[6:7], v[4:5]
	v_cvt_f32_i32_e32 v7, v131
	v_cvt_f32_i32_e32 v6, v130
	v_pk_mul_f32 v[10:11], v[160:161], v[174:175] op_sel_hi:[0,1]
	v_pk_mul_f32 v[6:7], v[10:11], v[6:7]
	v_pk_mul_f32 v[10:11], v[160:161], v[172:173] op_sel_hi:[0,1]
	v_pk_mul_f32 v[8:9], v[10:11], v[8:9]
	v_exp_f32_e32 v10, v2
	v_exp_f32_e32 v11, v3
	v_add_f32_e32 v10, 1.0, v10
	v_rcp_f32_e32 v10, v10
	v_add_f32_e32 v11, 1.0, v11
	v_rcp_f32_e32 v11, v11
	v_exp_f32_e32 v12, v4
	v_exp_f32_e32 v13, v5
	v_add_f32_e32 v12, 1.0, v12
	v_rcp_f32_e32 v12, v12
	v_add_f32_e32 v13, 1.0, v13
	v_rcp_f32_e32 v13, v13
	v_exp_f32_e32 v14, v6
	v_exp_f32_e32 v15, v7
	v_add_f32_e32 v14, 1.0, v14
	v_rcp_f32_e32 v14, v14
	v_add_f32_e32 v15, 1.0, v15
	v_rcp_f32_e32 v15, v15
	v_exp_f32_e32 v16, v8
	v_exp_f32_e32 v17, v9
	v_add_f32_e32 v16, 1.0, v16
	v_rcp_f32_e32 v16, v16
	v_add_f32_e32 v17, 1.0, v17
	v_rcp_f32_e32 v17, v17
	v_sub_f32_e32 v130, 1.0, v106
	v_fma_f32 v10, v130, v10, v106
	v_sub_f32_e32 v130, 1.0, v107
	v_fma_f32 v11, v130, v11, v107
	v_sub_f32_e32 v130, 1.0, v108
	v_fma_f32 v12, v130, v12, v108
	v_sub_f32_e32 v130, 1.0, v109
	v_fma_f32 v13, v130, v13, v109
	v_sub_f32_e32 v130, 1.0, v98
	v_fma_f32 v14, v130, v14, v98
	v_sub_f32_e32 v130, 1.0, v99
	v_fma_f32 v15, v130, v15, v99
	v_sub_f32_e32 v130, 1.0, v100
	v_fma_f32 v16, v130, v16, v100
	v_sub_f32_e32 v130, 1.0, v101
	v_fma_f32 v17, v130, v17, v101
	v_log_f32_e32 v10, v10
	v_log_f32_e32 v11, v11
	v_log_f32_e32 v12, v12
	v_log_f32_e32 v13, v13
	v_log_f32_e32 v14, v14
	v_log_f32_e32 v15, v15
	v_log_f32_e32 v16, v16
	v_log_f32_e32 v17, v17
	v_add_u32_e32 v2, 32, v197
	v_mad_i64_i32 v[130:131], s[44:45], s36, v2, 0
	v_cvt_pk_bf16_f32 v2, v10, v11
	v_cvt_pk_bf16_f32 v3, v12, v13
	v_cvt_pk_bf16_f32 v4, v14, v15
	v_cvt_pk_bf16_f32 v5, v16, v17
	v_lshl_add_u64 v[6:7], v[130:131], 1, v[180:181]
	global_store_dwordx4 v[6:7], v[2:5], off
	v_mov_b32_e32 v8, v161
	v_pk_mul_f32 v[6:7], v[8:9], v[178:179] op_sel_hi:[0,1]
	v_cvt_f32_i32_e32 v3, v127
	v_cvt_f32_i32_e32 v2, v126
	v_cvt_f32_i32_e32 v5, v129
	v_cvt_f32_i32_e32 v4, v128
	v_cvt_f32_i32_e32 v11, v125
	v_pk_mul_f32 v[2:3], v[6:7], v[2:3]
	v_pk_mul_f32 v[6:7], v[8:9], v[176:177] op_sel_hi:[0,1]
	v_pk_mul_f32 v[4:5], v[6:7], v[4:5]
	v_cvt_f32_i32_e32 v7, v123
	v_cvt_f32_i32_e32 v6, v122
	v_cvt_f32_i32_e32 v10, v124
	v_pk_mul_f32 v[12:13], v[8:9], v[174:175] op_sel_hi:[0,1]
	v_pk_mul_f32 v[8:9], v[8:9], v[172:173] op_sel_hi:[0,1]
	v_pk_mul_f32 v[6:7], v[12:13], v[6:7]
	v_pk_mul_f32 v[8:9], v[8:9], v[10:11]
	v_exp_f32_e32 v10, v2
	v_exp_f32_e32 v11, v3
	v_add_f32_e32 v10, 1.0, v10
	v_rcp_f32_e32 v10, v10
	v_add_f32_e32 v11, 1.0, v11
	v_rcp_f32_e32 v11, v11
	v_exp_f32_e32 v12, v4
	v_exp_f32_e32 v13, v5
	v_add_f32_e32 v12, 1.0, v12
	v_rcp_f32_e32 v12, v12
	v_add_f32_e32 v13, 1.0, v13
	v_rcp_f32_e32 v13, v13
	v_exp_f32_e32 v14, v6
	v_exp_f32_e32 v15, v7
	v_add_f32_e32 v14, 1.0, v14
	v_rcp_f32_e32 v14, v14
	v_add_f32_e32 v15, 1.0, v15
	v_rcp_f32_e32 v15, v15
	v_exp_f32_e32 v16, v8
	v_exp_f32_e32 v17, v9
	v_add_f32_e32 v16, 1.0, v16
	v_rcp_f32_e32 v16, v16
	v_add_f32_e32 v17, 1.0, v17
	v_rcp_f32_e32 v17, v17
	v_sub_f32_e32 v122, 1.0, v106
	v_fma_f32 v10, v122, v10, v106
	v_sub_f32_e32 v122, 1.0, v107
	v_fma_f32 v11, v122, v11, v107
	v_sub_f32_e32 v122, 1.0, v108
	v_fma_f32 v12, v122, v12, v108
	v_sub_f32_e32 v122, 1.0, v109
	v_fma_f32 v13, v122, v13, v109
	v_sub_f32_e32 v122, 1.0, v98
	v_fma_f32 v14, v122, v14, v98
	v_sub_f32_e32 v122, 1.0, v99
	v_fma_f32 v15, v122, v15, v99
	v_sub_f32_e32 v122, 1.0, v100
	v_fma_f32 v16, v122, v16, v100
	v_sub_f32_e32 v122, 1.0, v101
	v_fma_f32 v17, v122, v17, v101
	v_log_f32_e32 v10, v10
	v_log_f32_e32 v11, v11
	v_log_f32_e32 v12, v12
	v_log_f32_e32 v13, v13
	v_log_f32_e32 v14, v14
	v_log_f32_e32 v15, v15
	v_log_f32_e32 v16, v16
	v_log_f32_e32 v17, v17
	v_add_u32_e32 v2, 48, v197
	v_mad_i64_i32 v[122:123], s[44:45], s36, v2, 0
	v_cvt_pk_bf16_f32 v2, v10, v11
	v_cvt_pk_bf16_f32 v3, v12, v13
	v_cvt_pk_bf16_f32 v4, v14, v15
	v_cvt_pk_bf16_f32 v5, v16, v17
	v_lshl_add_u64 v[6:7], v[122:123], 1, v[180:181]
	global_store_dwordx4 v[6:7], v[2:5], off
	v_pk_mul_f32 v[6:7], v[158:159], v[178:179] op_sel_hi:[0,1]
	v_cvt_f32_i32_e32 v9, v117
	v_cvt_f32_i32_e32 v3, v119
	v_cvt_f32_i32_e32 v2, v118
	v_cvt_f32_i32_e32 v5, v121
	v_cvt_f32_i32_e32 v4, v120
	v_cvt_f32_i32_e32 v8, v116
	v_pk_mul_f32 v[2:3], v[6:7], v[2:3]
	v_pk_mul_f32 v[6:7], v[158:159], v[176:177] op_sel_hi:[0,1]
	v_pk_mul_f32 v[4:5], v[6:7], v[4:5]
	v_cvt_f32_i32_e32 v7, v115
	v_cvt_f32_i32_e32 v6, v114
	v_pk_mul_f32 v[10:11], v[158:159], v[174:175] op_sel_hi:[0,1]
	v_pk_mul_f32 v[6:7], v[10:11], v[6:7]
	v_pk_mul_f32 v[10:11], v[158:159], v[172:173] op_sel_hi:[0,1]
	v_pk_mul_f32 v[8:9], v[10:11], v[8:9]
	v_exp_f32_e32 v10, v2
	v_exp_f32_e32 v11, v3
	v_add_f32_e32 v10, 1.0, v10
; DI unsigned pk2(float lo, float hi) { f32x2 v = {lo, hi}; bf16x2_t b = __builtin_convertvector(v, bf16x2_t); return __builtin_bit_cast(unsigned, b); }
; DI float sigmoidf_(float x) { return __builtin_amdgcn_rcpf(1.0f + __expf(-x)); }
;     DI void operator()(const f32x4 (&acc)[2][2][4][2], const Unit& u, int wr, int wc, int fr, int fq, const LAS unsigned char* slot) const {
;     ...
;             for (int ai = 0; ai < 2; ++ai)
; #pragma unroll
;                 for (int m = 0; m < 4; ++m) { const int rr = row0 + ai * HALF + m * 16; const size_t ro = (size_t)rr * pitch; float v[8]; const float rs = rsv[ai][m];
; #pragma unroll
;                     for (int j = 0; j < 8; ++j) v[j] = (float)__builtin_bit_cast(i32x4, acc[ai][bj][m][j >> 2])[j & 3] * (rs * csv[j]);
;                     if (cls != 0) {
; #pragma unroll
;                         for (int j = 0; j < 8; ++j) { if (cls == 1) v[j] *= sigmoidf_(v[j]); else v[j] = __builtin_amdgcn_rcpf(1.0f + __builtin_amdgcn_exp2f(v[j])); }
;                         if (cls == 2) {
; #pragma unroll
;                             for (int j = 0; j < 8; ++j) { const float l = lbv[j]; v[j] = __builtin_amdgcn_logf(l + (1.0f - l) * v[j]); } }
;                     }
;                     u32x4 w; w.x = pk2(v[0], v[1]); w.y = pk2(v[2], v[3]); w.z = pk2(v[4], v[5]); w.w = pk2(v[6], v[7]);
;                     *(u32x4*)(colp + ro) = w; }
	v_rcp_f32_e32 v10, v10
	v_add_f32_e32 v11, 1.0, v11
	v_rcp_f32_e32 v11, v11
	v_exp_f32_e32 v12, v4
	v_exp_f32_e32 v13, v5
	v_add_f32_e32 v12, 1.0, v12
	v_rcp_f32_e32 v12, v12
	v_add_f32_e32 v13, 1.0, v13
	v_rcp_f32_e32 v13, v13
	v_exp_f32_e32 v14, v6
	v_exp_f32_e32 v15, v7
	v_add_f32_e32 v14, 1.0, v14
	v_rcp_f32_e32 v14, v14
	v_add_f32_e32 v15, 1.0, v15
	v_rcp_f32_e32 v15, v15
	v_exp_f32_e32 v16, v8
	v_exp_f32_e32 v17, v9
	v_add_f32_e32 v16, 1.0, v16
	v_rcp_f32_e32 v16, v16
	v_add_f32_e32 v17, 1.0, v17
	v_rcp_f32_e32 v17, v17
	v_sub_f32_e32 v114, 1.0, v106
	v_fma_f32 v10, v114, v10, v106
	v_sub_f32_e32 v114, 1.0, v107
	v_fma_f32 v11, v114, v11, v107
	v_sub_f32_e32 v114, 1.0, v108
	v_fma_f32 v12, v114, v12, v108
	v_sub_f32_e32 v114, 1.0, v109
	v_fma_f32 v13, v114, v13, v109
	v_sub_f32_e32 v114, 1.0, v98
	v_fma_f32 v14, v114, v14, v98
	v_sub_f32_e32 v114, 1.0, v99
	v_fma_f32 v15, v114, v15, v99
	v_sub_f32_e32 v114, 1.0, v100
	v_fma_f32 v16, v114, v16, v100
	v_sub_f32_e32 v114, 1.0, v101
	v_fma_f32 v17, v114, v17, v101
	v_log_f32_e32 v10, v10
	v_log_f32_e32 v11, v11
	v_log_f32_e32 v12, v12
	v_log_f32_e32 v13, v13
	v_log_f32_e32 v14, v14
	v_log_f32_e32 v15, v15
	v_log_f32_e32 v16, v16
	v_log_f32_e32 v17, v17
	v_add_u32_e32 v2, 0x80, v197
	v_mad_i64_i32 v[114:115], s[44:45], s36, v2, 0
	v_cvt_pk_bf16_f32 v2, v10, v11
	v_cvt_pk_bf16_f32 v3, v12, v13
	v_cvt_pk_bf16_f32 v4, v14, v15
	v_cvt_pk_bf16_f32 v5, v16, v17
	v_lshl_add_u64 v[6:7], v[114:115], 1, v[180:181]
	global_store_dwordx4 v[6:7], v[2:5], off
	v_mov_b32_e32 v8, v159
	v_pk_mul_f32 v[6:7], v[8:9], v[178:179] op_sel_hi:[0,1]
	v_cvt_f32_i32_e32 v3, v111
	v_cvt_f32_i32_e32 v2, v110
	v_cvt_f32_i32_e32 v5, v113
	v_cvt_f32_i32_e32 v4, v112
	v_cvt_f32_i32_e32 v11, v105
	v_pk_mul_f32 v[2:3], v[6:7], v[2:3]
	v_pk_mul_f32 v[6:7], v[8:9], v[176:177] op_sel_hi:[0,1]
	v_pk_mul_f32 v[4:5], v[6:7], v[4:5]
	v_cvt_f32_i32_e32 v7, v103
	v_cvt_f32_i32_e32 v6, v102
	v_cvt_f32_i32_e32 v10, v104
	v_pk_mul_f32 v[12:13], v[8:9], v[174:175] op_sel_hi:[0,1]
	v_pk_mul_f32 v[8:9], v[8:9], v[172:173] op_sel_hi:[0,1]
	v_pk_mul_f32 v[6:7], v[12:13], v[6:7]
	v_pk_mul_f32 v[8:9], v[8:9], v[10:11]
	v_exp_f32_e32 v10, v2
	v_exp_f32_e32 v11, v3
	v_add_f32_e32 v10, 1.0, v10
	v_rcp_f32_e32 v10, v10
	v_add_f32_e32 v11, 1.0, v11
	v_rcp_f32_e32 v11, v11
	v_exp_f32_e32 v12, v4
	v_exp_f32_e32 v13, v5
	v_add_f32_e32 v12, 1.0, v12
	v_rcp_f32_e32 v12, v12
	v_add_f32_e32 v13, 1.0, v13
	v_rcp_f32_e32 v13, v13
	v_exp_f32_e32 v14, v6
	v_exp_f32_e32 v15, v7
	v_add_f32_e32 v14, 1.0, v14
	v_rcp_f32_e32 v14, v14
	v_add_f32_e32 v15, 1.0, v15
	v_rcp_f32_e32 v15, v15
	v_exp_f32_e32 v16, v8
	v_exp_f32_e32 v17, v9
	v_add_f32_e32 v16, 1.0, v16
	v_rcp_f32_e32 v16, v16
	v_add_f32_e32 v17, 1.0, v17
	v_rcp_f32_e32 v17, v17
	v_sub_f32_e32 v102, 1.0, v106
	v_fma_f32 v10, v102, v10, v106
	v_sub_f32_e32 v102, 1.0, v107
	v_fma_f32 v11, v102, v11, v107
	v_sub_f32_e32 v102, 1.0, v108
	v_fma_f32 v12, v102, v12, v108
	v_sub_f32_e32 v102, 1.0, v109
	v_fma_f32 v13, v102, v13, v109
	v_sub_f32_e32 v102, 1.0, v98
	v_fma_f32 v14, v102, v14, v98
	v_sub_f32_e32 v102, 1.0, v99
	v_fma_f32 v15, v102, v15, v99
	v_sub_f32_e32 v102, 1.0, v100
	v_fma_f32 v16, v102, v16, v100
	v_sub_f32_e32 v102, 1.0, v101
	v_fma_f32 v17, v102, v17, v101
	v_log_f32_e32 v10, v10
	v_log_f32_e32 v11, v11
	v_log_f32_e32 v12, v12
	v_log_f32_e32 v13, v13
	v_log_f32_e32 v14, v14
	v_log_f32_e32 v15, v15
	v_log_f32_e32 v16, v16
	v_log_f32_e32 v17, v17
	v_add_u32_e32 v2, 0x90, v197
	v_mad_i64_i32 v[102:103], s[44:45], s36, v2, 0
	v_cvt_pk_bf16_f32 v2, v10, v11
	v_cvt_pk_bf16_f32 v3, v12, v13
	v_cvt_pk_bf16_f32 v4, v14, v15
	v_cvt_pk_bf16_f32 v5, v16, v17
	v_lshl_add_u64 v[6:7], v[102:103], 1, v[180:181]
	global_store_dwordx4 v[6:7], v[2:5], off
	v_pk_mul_f32 v[6:7], v[156:157], v[178:179] op_sel_hi:[0,1]
	v_cvt_f32_i32_e32 v9, v93
	v_cvt_f32_i32_e32 v3, v95
	v_cvt_f32_i32_e32 v2, v94
	v_cvt_f32_i32_e32 v5, v97
	v_cvt_f32_i32_e32 v4, v96
	v_cvt_f32_i32_e32 v8, v92
	v_pk_mul_f32 v[2:3], v[6:7], v[2:3]
	v_pk_mul_f32 v[6:7], v[156:157], v[176:177] op_sel_hi:[0,1]
	v_pk_mul_f32 v[4:5], v[6:7], v[4:5]
	v_cvt_f32_i32_e32 v7, v91
	v_cvt_f32_i32_e32 v6, v90
	v_pk_mul_f32 v[10:11], v[156:157], v[174:175] op_sel_hi:[0,1]
	v_pk_mul_f32 v[6:7], v[10:11], v[6:7]
	v_pk_mul_f32 v[10:11], v[156:157], v[172:173] op_sel_hi:[0,1]
	v_pk_mul_f32 v[8:9], v[10:11], v[8:9]
	v_exp_f32_e32 v10, v2
	v_exp_f32_e32 v11, v3
	v_add_f32_e32 v10, 1.0, v10
	v_rcp_f32_e32 v10, v10
	v_add_f32_e32 v11, 1.0, v11
	v_rcp_f32_e32 v11, v11
	v_exp_f32_e32 v12, v4
	v_exp_f32_e32 v13, v5
	v_add_f32_e32 v12, 1.0, v12
	v_rcp_f32_e32 v12, v12
	v_add_f32_e32 v13, 1.0, v13
	v_rcp_f32_e32 v13, v13
	v_exp_f32_e32 v14, v6
	v_exp_f32_e32 v15, v7
	v_add_f32_e32 v14, 1.0, v14
	v_rcp_f32_e32 v14, v14
	v_add_f32_e32 v15, 1.0, v15
	v_rcp_f32_e32 v15, v15
	v_exp_f32_e32 v16, v8
	v_exp_f32_e32 v17, v9
	v_add_f32_e32 v16, 1.0, v16
	v_rcp_f32_e32 v16, v16
	v_add_f32_e32 v17, 1.0, v17
	v_rcp_f32_e32 v17, v17
	v_sub_f32_e32 v90, 1.0, v106
	v_fma_f32 v10, v90, v10, v106
	v_sub_f32_e32 v90, 1.0, v107
	v_fma_f32 v11, v90, v11, v107
	v_sub_f32_e32 v90, 1.0, v108
	v_fma_f32 v12, v90, v12, v108
	v_sub_f32_e32 v90, 1.0, v109
	v_fma_f32 v13, v90, v13, v109
	v_sub_f32_e32 v90, 1.0, v98
	v_fma_f32 v14, v90, v14, v98
	v_sub_f32_e32 v90, 1.0, v99
	v_fma_f32 v15, v90, v15, v99
	v_sub_f32_e32 v90, 1.0, v100
	v_fma_f32 v16, v90, v16, v100
	v_sub_f32_e32 v90, 1.0, v101
	v_fma_f32 v17, v90, v17, v101
	v_log_f32_e32 v10, v10
	v_log_f32_e32 v11, v11
	v_log_f32_e32 v12, v12
	v_log_f32_e32 v13, v13
	v_log_f32_e32 v14, v14
	v_log_f32_e32 v15, v15
	v_log_f32_e32 v16, v16
; #define LAS __attribute__((address_space(3)))
; DI unsigned pk2(float lo, float hi) { f32x2 v = {lo, hi}; bf16x2_t b = __builtin_convertvector(v, bf16x2_t); return __builtin_bit_cast(unsigned, b); }
; DI float sigmoidf_(float x) { return __builtin_amdgcn_rcpf(1.0f + __expf(-x)); }
;     DI void operator()(const f32x4 (&acc)[2][2][4][2], const Unit& u, int wr, int wc, int fr, int fq, const LAS unsigned char* slot) const {
;     ...
;         for (int bj = 0; bj < 2; ++bj) {
;             float lbv[8];
;             const int cin = cin0 + bj * HALF;
;             { const int lc = bj * HALF + wc * 32 + 8 * fq; const f32x4 a = *(const LAS f32x4*)(slot + 2048 + 4 * lc), b = *(const LAS f32x4*)(slot + 2048 + 4 * lc + 16);
; #pragma unroll
;               for (int j = 0; j < 4; ++j) { lbv[j] = (cls == 2) ? a[j] : 0.f; lbv[4 + j] = (cls == 2) ? b[j] : 0.f; } }
;             bf16* colp = base + (size_t)(cin >> hs) * MROWS * pitch + (cin & ((1 << hs) - 1));
;             float csv[8];
;             { const int lc = bj * HALF + wc * 32 + 8 * fq; const f32x4 a = *(const LAS f32x4*)(slot + 1024 + 4 * lc), b = *(const LAS f32x4*)(slot + 1024 + 4 * lc + 16);
;     ...
;             for (int ai = 0; ai < 2; ++ai)
; #pragma unroll
;                 for (int m = 0; m < 4; ++m) { const int rr = row0 + ai * HALF + m * 16; const size_t ro = (size_t)rr * pitch; float v[8]; const float rs = rsv[ai][m];
; #pragma unroll
;                     for (int j = 0; j < 8; ++j) v[j] = (float)__builtin_bit_cast(i32x4, acc[ai][bj][m][j >> 2])[j & 3] * (rs * csv[j]);
;                     if (cls != 0) {
; #pragma unroll
;                         for (int j = 0; j < 8; ++j) { if (cls == 1) v[j] *= sigmoidf_(v[j]); else v[j] = __builtin_amdgcn_rcpf(1.0f + __builtin_amdgcn_exp2f(v[j])); }
;                         if (cls == 2) {
; #pragma unroll
;                             for (int j = 0; j < 8; ++j) { const float l = lbv[j]; v[j] = __builtin_amdgcn_logf(l + (1.0f - l) * v[j]); } }
;                     }
;                     u32x4 w; w.x = pk2(v[0], v[1]); w.y = pk2(v[2], v[3]); w.z = pk2(v[4], v[5]); w.w = pk2(v[6], v[7]);
;                     *(u32x4*)(colp + ro) = w; }
	v_log_f32_e32 v17, v17
	v_add_u32_e32 v2, 0xa0, v197
	v_mad_i64_i32 v[90:91], s[44:45], s36, v2, 0
	v_cvt_pk_bf16_f32 v2, v10, v11
	v_cvt_pk_bf16_f32 v3, v12, v13
	v_cvt_pk_bf16_f32 v4, v14, v15
	v_cvt_pk_bf16_f32 v5, v16, v17
	v_lshl_add_u64 v[6:7], v[90:91], 1, v[180:181]
	global_store_dwordx4 v[6:7], v[2:5], off
	v_mov_b32_e32 v8, v157
	v_pk_mul_f32 v[6:7], v[8:9], v[178:179] op_sel_hi:[0,1]
	v_cvt_f32_i32_e32 v3, v87
	v_cvt_f32_i32_e32 v2, v86
	v_cvt_f32_i32_e32 v5, v89
	v_cvt_f32_i32_e32 v4, v88
	v_cvt_f32_i32_e32 v11, v85
	v_pk_mul_f32 v[2:3], v[6:7], v[2:3]
	v_pk_mul_f32 v[6:7], v[8:9], v[176:177] op_sel_hi:[0,1]
	v_pk_mul_f32 v[4:5], v[6:7], v[4:5]
	v_cvt_f32_i32_e32 v7, v83
	v_cvt_f32_i32_e32 v6, v82
	v_cvt_f32_i32_e32 v10, v84
	v_pk_mul_f32 v[12:13], v[8:9], v[174:175] op_sel_hi:[0,1]
	v_pk_mul_f32 v[8:9], v[8:9], v[172:173] op_sel_hi:[0,1]
	v_pk_mul_f32 v[6:7], v[12:13], v[6:7]
	v_pk_mul_f32 v[8:9], v[8:9], v[10:11]
	v_exp_f32_e32 v10, v2
	v_exp_f32_e32 v11, v3
	v_add_f32_e32 v10, 1.0, v10
	v_rcp_f32_e32 v10, v10
	v_add_f32_e32 v11, 1.0, v11
	v_rcp_f32_e32 v11, v11
	v_exp_f32_e32 v12, v4
	v_exp_f32_e32 v13, v5
	v_add_f32_e32 v12, 1.0, v12
	v_rcp_f32_e32 v12, v12
	v_add_f32_e32 v13, 1.0, v13
	v_rcp_f32_e32 v13, v13
	v_exp_f32_e32 v14, v6
	v_exp_f32_e32 v15, v7
	v_add_f32_e32 v14, 1.0, v14
	v_rcp_f32_e32 v14, v14
	v_add_f32_e32 v15, 1.0, v15
	v_rcp_f32_e32 v15, v15
	v_exp_f32_e32 v16, v8
	v_exp_f32_e32 v17, v9
	v_add_f32_e32 v16, 1.0, v16
	v_rcp_f32_e32 v16, v16
	v_add_f32_e32 v17, 1.0, v17
	v_rcp_f32_e32 v17, v17
	v_sub_f32_e32 v82, 1.0, v106
	v_fma_f32 v10, v82, v10, v106
	v_sub_f32_e32 v82, 1.0, v107
	v_fma_f32 v11, v82, v11, v107
	v_sub_f32_e32 v82, 1.0, v108
	v_fma_f32 v12, v82, v12, v108
	v_sub_f32_e32 v82, 1.0, v109
	v_fmac_f32_e32 v109, v82, v13
	v_sub_f32_e32 v82, 1.0, v98
	v_fma_f32 v14, v82, v14, v98
	v_sub_f32_e32 v82, 1.0, v99
	v_fma_f32 v15, v82, v15, v99
	v_sub_f32_e32 v82, 1.0, v100
	v_fma_f32 v16, v82, v16, v100
	v_sub_f32_e32 v82, 1.0, v101
	v_fmac_f32_e32 v101, v82, v17
	v_log_f32_e32 v10, v10
	v_log_f32_e32 v11, v11
	v_log_f32_e32 v12, v12
	v_log_f32_e32 v13, v109
	v_log_f32_e32 v14, v14
	v_log_f32_e32 v15, v15
	v_log_f32_e32 v16, v16
	v_log_f32_e32 v17, v101
	s_mov_b64 s[44:45], 0
	v_add_u32_e32 v2, 0xb0, v197
	v_mad_i64_i32 v[92:93], s[36:37], s36, v2, 0
	v_cvt_pk_bf16_f32 v2, v10, v11
	v_cvt_pk_bf16_f32 v3, v12, v13
	v_cvt_pk_bf16_f32 v4, v14, v15
	v_cvt_pk_bf16_f32 v5, v16, v17
	v_lshl_add_u64 v[10:11], v[92:93], 1, v[180:181]
	global_store_dwordx4 v[10:11], v[2:5], off
	ds_read_b128 v[6:9], v195 offset:1536
	ds_read_b128 v[2:5], v195 offset:1552
	ds_read_b128 v[86:89], v195 offset:2560
	ds_read_b128 v[82:85], v195 offset:2576
	v_mov_b32_e32 v104, v168
	v_mov_b32_e32 v105, v168
	s_waitcnt lgkmcnt(0)
	v_pk_mul_f32 v[14:15], v[2:3], s[26:27] op_sel_hi:[1,0]
	v_pk_mul_f32 v[16:17], v[4:5], s[26:27] op_sel_hi:[1,0]
	v_cndmask_b32_e64 v97, v3, v15, s[38:39]
	v_cndmask_b32_e64 v96, v2, v14, s[38:39]
	v_cvt_f32_i32_e32 v3, v79
	v_cvt_f32_i32_e32 v2, v78
	v_pk_mul_f32 v[10:11], v[6:7], s[26:27] op_sel_hi:[1,0]
	v_cndmask_b32_e64 v95, v5, v17, s[38:39]
	v_cndmask_b32_e64 v94, v4, v16, s[38:39]
	v_cvt_f32_i32_e32 v5, v81
	v_cvt_f32_i32_e32 v4, v80
	v_pk_mul_f32 v[12:13], v[8:9], s[26:27] op_sel_hi:[1,0]
	v_cndmask_b32_e64 v101, v7, v11, s[38:39]
	v_cndmask_b32_e64 v100, v6, v10, s[38:39]
	v_cndmask_b32_e64 v99, v9, v13, s[38:39]
	v_cndmask_b32_e64 v98, v8, v12, s[38:39]
	v_pk_mul_f32 v[6:7], v[104:105], v[100:101]
	v_cvt_f32_i32_e32 v9, v77
	v_pk_mul_f32 v[2:3], v[6:7], v[2:3]
	v_pk_mul_f32 v[6:7], v[104:105], v[98:99]
	v_cvt_f32_i32_e32 v8, v76
	v_pk_mul_f32 v[4:5], v[6:7], v[4:5]
	v_cvt_f32_i32_e32 v7, v75
	v_cvt_f32_i32_e32 v6, v74
	v_pk_mul_f32 v[10:11], v[104:105], v[96:97]
	v_pk_mul_f32 v[6:7], v[10:11], v[6:7]
	v_pk_mul_f32 v[10:11], v[104:105], v[94:95]
	v_pk_mul_f32 v[8:9], v[10:11], v[8:9]
	v_exp_f32_e32 v10, v2
	v_exp_f32_e32 v11, v3
	v_add_f32_e32 v10, 1.0, v10
	v_rcp_f32_e32 v10, v10
	v_add_f32_e32 v11, 1.0, v11
	v_rcp_f32_e32 v11, v11
	v_exp_f32_e32 v12, v4
	v_exp_f32_e32 v13, v5
	v_add_f32_e32 v12, 1.0, v12
	v_rcp_f32_e32 v12, v12
	v_add_f32_e32 v13, 1.0, v13
	v_rcp_f32_e32 v13, v13
	v_exp_f32_e32 v14, v6
	v_exp_f32_e32 v15, v7
	v_add_f32_e32 v14, 1.0, v14
	v_rcp_f32_e32 v14, v14
	v_add_f32_e32 v15, 1.0, v15
	v_rcp_f32_e32 v15, v15
	v_exp_f32_e32 v16, v8
	v_exp_f32_e32 v17, v9
	v_add_f32_e32 v16, 1.0, v16
	v_rcp_f32_e32 v16, v16
	v_add_f32_e32 v17, 1.0, v17
	v_rcp_f32_e32 v17, v17
	v_sub_f32_e32 v74, 1.0, v86
	v_fma_f32 v10, v74, v10, v86
	v_sub_f32_e32 v74, 1.0, v87
	v_fma_f32 v11, v74, v11, v87
	v_sub_f32_e32 v74, 1.0, v88
	v_fma_f32 v12, v74, v12, v88
	v_sub_f32_e32 v74, 1.0, v89
	v_fma_f32 v13, v74, v13, v89
	v_sub_f32_e32 v74, 1.0, v82
	v_fma_f32 v14, v74, v14, v82
	v_sub_f32_e32 v74, 1.0, v83
	v_fma_f32 v15, v74, v15, v83
	v_sub_f32_e32 v74, 1.0, v84
	v_fma_f32 v16, v74, v16, v84
	v_sub_f32_e32 v74, 1.0, v85
	v_fma_f32 v17, v74, v17, v85
	v_log_f32_e32 v10, v10
	v_log_f32_e32 v11, v11
	v_log_f32_e32 v12, v12
	v_log_f32_e32 v13, v13
	v_log_f32_e32 v14, v14
	v_log_f32_e32 v15, v15
	v_log_f32_e32 v16, v16
	v_log_f32_e32 v17, v17
	v_or_b32_e32 v2, 0x80, v196
	s_not_b32 s3, s95
	v_ashrrev_i32_e32 v2, s93, v2
	v_mad_i64_i32 v[2:3], s[36:37], s94, v2, 0
	v_bitop3_b32 v4, v196, s3, v190 bitop3:0xc8
	v_lshl_add_u64 v[2:3], v[2:3], 1, s[42:43]
	v_lshlrev_b32_e32 v150, 1, v4
	v_lshl_add_u64 v[74:75], v[2:3], 0, v[150:151]
	v_cvt_pk_bf16_f32 v2, v10, v11
	v_cvt_pk_bf16_f32 v3, v12, v13
	v_cvt_pk_bf16_f32 v4, v14, v15
	v_cvt_pk_bf16_f32 v5, v16, v17
	v_lshl_add_u64 v[6:7], v[170:171], 1, v[74:75]
; DI unsigned pk2(float lo, float hi) { f32x2 v = {lo, hi}; bf16x2_t b = __builtin_convertvector(v, bf16x2_t); return __builtin_bit_cast(unsigned, b); }
; DI float sigmoidf_(float x) { return __builtin_amdgcn_rcpf(1.0f + __expf(-x)); }
;     DI void operator()(const f32x4 (&acc)[2][2][4][2], const Unit& u, int wr, int wc, int fr, int fq, const LAS unsigned char* slot) const {
;     ...
;             for (int ai = 0; ai < 2; ++ai)
; #pragma unroll
;                 for (int m = 0; m < 4; ++m) { const int rr = row0 + ai * HALF + m * 16; const size_t ro = (size_t)rr * pitch; float v[8]; const float rs = rsv[ai][m];
; #pragma unroll
;                     for (int j = 0; j < 8; ++j) v[j] = (float)__builtin_bit_cast(i32x4, acc[ai][bj][m][j >> 2])[j & 3] * (rs * csv[j]);
;                     if (cls != 0) {
; #pragma unroll
;                         for (int j = 0; j < 8; ++j) { if (cls == 1) v[j] *= sigmoidf_(v[j]); else v[j] = __builtin_amdgcn_rcpf(1.0f + __builtin_amdgcn_exp2f(v[j])); }
;                         if (cls == 2) {
; #pragma unroll
;                             for (int j = 0; j < 8; ++j) { const float l = lbv[j]; v[j] = __builtin_amdgcn_logf(l + (1.0f - l) * v[j]); } }
;                     }
;                     u32x4 w; w.x = pk2(v[0], v[1]); w.y = pk2(v[2], v[3]); w.z = pk2(v[4], v[5]); w.w = pk2(v[6], v[7]);
;                     *(u32x4*)(colp + ro) = w; }
	global_store_dwordx4 v[6:7], v[2:5], off
	v_mov_b32_e32 v168, v169
	v_pk_mul_f32 v[6:7], v[168:169], v[100:101]
	v_cvt_f32_i32_e32 v3, v71
	v_cvt_f32_i32_e32 v2, v70
	v_cvt_f32_i32_e32 v5, v73
	v_cvt_f32_i32_e32 v4, v72
	v_cvt_f32_i32_e32 v9, v69
	v_pk_mul_f32 v[2:3], v[6:7], v[2:3]
	v_pk_mul_f32 v[6:7], v[168:169], v[98:99]
	v_cvt_f32_i32_e32 v8, v68
	v_pk_mul_f32 v[4:5], v[6:7], v[4:5]
	v_cvt_f32_i32_e32 v7, v67
	v_cvt_f32_i32_e32 v6, v66
	v_pk_mul_f32 v[10:11], v[168:169], v[96:97]
	v_pk_mul_f32 v[6:7], v[10:11], v[6:7]
	v_pk_mul_f32 v[10:11], v[168:169], v[94:95]
	v_pk_mul_f32 v[8:9], v[10:11], v[8:9]
	v_exp_f32_e32 v10, v2
	v_exp_f32_e32 v11, v3
	v_add_f32_e32 v10, 1.0, v10
	v_rcp_f32_e32 v10, v10
	v_add_f32_e32 v11, 1.0, v11
	v_rcp_f32_e32 v11, v11
	v_exp_f32_e32 v12, v4
	v_exp_f32_e32 v13, v5
	v_add_f32_e32 v12, 1.0, v12
	v_rcp_f32_e32 v12, v12
	v_add_f32_e32 v13, 1.0, v13
	v_rcp_f32_e32 v13, v13
	v_exp_f32_e32 v14, v6
	v_exp_f32_e32 v15, v7
	v_add_f32_e32 v14, 1.0, v14
	v_rcp_f32_e32 v14, v14
	v_add_f32_e32 v15, 1.0, v15
	v_rcp_f32_e32 v15, v15
	v_exp_f32_e32 v16, v8
	v_exp_f32_e32 v17, v9
	v_add_f32_e32 v16, 1.0, v16
	v_rcp_f32_e32 v16, v16
	v_add_f32_e32 v17, 1.0, v17
	v_rcp_f32_e32 v17, v17
	v_sub_f32_e32 v66, 1.0, v86
	v_fma_f32 v10, v66, v10, v86
	v_sub_f32_e32 v66, 1.0, v87
	v_fma_f32 v11, v66, v11, v87
	v_sub_f32_e32 v66, 1.0, v88
	v_fma_f32 v12, v66, v12, v88
	v_sub_f32_e32 v66, 1.0, v89
	v_fma_f32 v13, v66, v13, v89
	v_sub_f32_e32 v66, 1.0, v82
	v_fma_f32 v14, v66, v14, v82
	v_sub_f32_e32 v66, 1.0, v83
	v_fma_f32 v15, v66, v15, v83
	v_sub_f32_e32 v66, 1.0, v84
	v_fma_f32 v16, v66, v16, v84
	v_sub_f32_e32 v66, 1.0, v85
	v_fma_f32 v17, v66, v17, v85
	v_log_f32_e32 v10, v10
	v_log_f32_e32 v11, v11
	v_log_f32_e32 v12, v12
	v_log_f32_e32 v13, v13
	v_log_f32_e32 v14, v14
	v_log_f32_e32 v15, v15
	v_log_f32_e32 v16, v16
	v_log_f32_e32 v17, v17
	v_cvt_pk_bf16_f32 v2, v10, v11
	v_cvt_pk_bf16_f32 v3, v12, v13
	v_cvt_pk_bf16_f32 v4, v14, v15
	v_cvt_pk_bf16_f32 v5, v16, v17
	v_lshl_add_u64 v[6:7], v[138:139], 1, v[74:75]
	global_store_dwordx4 v[6:7], v[2:5], off
	v_mov_b32_e32 v8, v160
	v_mov_b32_e32 v9, v160
	v_cvt_f32_i32_e32 v3, v63
	v_cvt_f32_i32_e32 v2, v62
	v_cvt_f32_i32_e32 v5, v65
	v_cvt_f32_i32_e32 v4, v64
	v_pk_mul_f32 v[6:7], v[8:9], v[100:101]
	v_cvt_f32_i32_e32 v11, v61
	v_pk_mul_f32 v[2:3], v[6:7], v[2:3]
	v_pk_mul_f32 v[6:7], v[8:9], v[98:99]
	v_cvt_f32_i32_e32 v10, v60
	v_pk_mul_f32 v[4:5], v[6:7], v[4:5]
	v_cvt_f32_i32_e32 v7, v59
	v_cvt_f32_i32_e32 v6, v58
	v_pk_mul_f32 v[12:13], v[8:9], v[96:97]
	v_pk_mul_f32 v[8:9], v[8:9], v[94:95]
	v_pk_mul_f32 v[6:7], v[12:13], v[6:7]
	v_pk_mul_f32 v[8:9], v[8:9], v[10:11]
	v_exp_f32_e32 v10, v2
	v_exp_f32_e32 v11, v3
	v_add_f32_e32 v10, 1.0, v10
	v_rcp_f32_e32 v10, v10
	v_add_f32_e32 v11, 1.0, v11
	v_rcp_f32_e32 v11, v11
	v_exp_f32_e32 v12, v4
	v_exp_f32_e32 v13, v5
	v_add_f32_e32 v12, 1.0, v12
	v_rcp_f32_e32 v12, v12
	v_add_f32_e32 v13, 1.0, v13
	v_rcp_f32_e32 v13, v13
	v_exp_f32_e32 v14, v6
	v_exp_f32_e32 v15, v7
	v_add_f32_e32 v14, 1.0, v14
	v_rcp_f32_e32 v14, v14
	v_add_f32_e32 v15, 1.0, v15
	v_rcp_f32_e32 v15, v15
	v_exp_f32_e32 v16, v8
	v_exp_f32_e32 v17, v9
	v_add_f32_e32 v16, 1.0, v16
	v_rcp_f32_e32 v16, v16
	v_add_f32_e32 v17, 1.0, v17
	v_rcp_f32_e32 v17, v17
	v_sub_f32_e32 v58, 1.0, v86
	v_fma_f32 v10, v58, v10, v86
	v_sub_f32_e32 v58, 1.0, v87
	v_fma_f32 v11, v58, v11, v87
	v_sub_f32_e32 v58, 1.0, v88
	v_fma_f32 v12, v58, v12, v88
	v_sub_f32_e32 v58, 1.0, v89
	v_fma_f32 v13, v58, v13, v89
	v_sub_f32_e32 v58, 1.0, v82
	v_fma_f32 v14, v58, v14, v82
	v_sub_f32_e32 v58, 1.0, v83
	v_fma_f32 v15, v58, v15, v83
	v_sub_f32_e32 v58, 1.0, v84
	v_fma_f32 v16, v58, v16, v84
	v_sub_f32_e32 v58, 1.0, v85
	v_fma_f32 v17, v58, v17, v85
	v_log_f32_e32 v10, v10
	v_log_f32_e32 v11, v11
	v_log_f32_e32 v12, v12
	v_log_f32_e32 v13, v13
	v_log_f32_e32 v14, v14
	v_log_f32_e32 v15, v15
	v_log_f32_e32 v16, v16
	v_log_f32_e32 v17, v17
	v_cvt_pk_bf16_f32 v2, v10, v11
	v_cvt_pk_bf16_f32 v3, v12, v13
	v_cvt_pk_bf16_f32 v4, v14, v15
	v_cvt_pk_bf16_f32 v5, v16, v17
	v_lshl_add_u64 v[6:7], v[130:131], 1, v[74:75]
	global_store_dwordx4 v[6:7], v[2:5], off
	v_mov_b32_e32 v160, v161
	v_pk_mul_f32 v[6:7], v[160:161], v[100:101]
	v_cvt_f32_i32_e32 v3, v55
	v_cvt_f32_i32_e32 v2, v54
	v_cvt_f32_i32_e32 v5, v57
	v_cvt_f32_i32_e32 v4, v56
	v_cvt_f32_i32_e32 v9, v53
	v_pk_mul_f32 v[2:3], v[6:7], v[2:3]
	v_pk_mul_f32 v[6:7], v[160:161], v[98:99]
	v_cvt_f32_i32_e32 v8, v52
	v_pk_mul_f32 v[4:5], v[6:7], v[4:5]
	v_cvt_f32_i32_e32 v7, v51
	v_cvt_f32_i32_e32 v6, v50
	v_pk_mul_f32 v[10:11], v[160:161], v[96:97]
	v_pk_mul_f32 v[6:7], v[10:11], v[6:7]
	v_pk_mul_f32 v[10:11], v[160:161], v[94:95]
	v_pk_mul_f32 v[8:9], v[10:11], v[8:9]
	v_exp_f32_e32 v10, v2
	v_exp_f32_e32 v11, v3
	v_add_f32_e32 v10, 1.0, v10
	v_rcp_f32_e32 v10, v10
	v_add_f32_e32 v11, 1.0, v11
	v_rcp_f32_e32 v11, v11
	v_exp_f32_e32 v12, v4
	v_exp_f32_e32 v13, v5
	v_add_f32_e32 v12, 1.0, v12
	v_rcp_f32_e32 v12, v12
	v_add_f32_e32 v13, 1.0, v13
	v_rcp_f32_e32 v13, v13
	v_exp_f32_e32 v14, v6
	v_exp_f32_e32 v15, v7
	v_add_f32_e32 v14, 1.0, v14
	v_rcp_f32_e32 v14, v14
	v_add_f32_e32 v15, 1.0, v15
	v_rcp_f32_e32 v15, v15
	v_exp_f32_e32 v16, v8
	v_exp_f32_e32 v17, v9
	v_add_f32_e32 v16, 1.0, v16
	v_rcp_f32_e32 v16, v16
	v_add_f32_e32 v17, 1.0, v17
	v_rcp_f32_e32 v17, v17
	v_sub_f32_e32 v50, 1.0, v86
	v_fma_f32 v10, v50, v10, v86
	v_sub_f32_e32 v50, 1.0, v87
	v_fma_f32 v11, v50, v11, v87
	v_sub_f32_e32 v50, 1.0, v88
	v_fma_f32 v12, v50, v12, v88
	v_sub_f32_e32 v50, 1.0, v89
	v_fma_f32 v13, v50, v13, v89
	v_sub_f32_e32 v50, 1.0, v82
	v_fma_f32 v14, v50, v14, v82
; DI unsigned pk2(float lo, float hi) { f32x2 v = {lo, hi}; bf16x2_t b = __builtin_convertvector(v, bf16x2_t); return __builtin_bit_cast(unsigned, b); }
; DI float sigmoidf_(float x) { return __builtin_amdgcn_rcpf(1.0f + __expf(-x)); }
;     DI void operator()(const f32x4 (&acc)[2][2][4][2], const Unit& u, int wr, int wc, int fr, int fq, const LAS unsigned char* slot) const {
;     ...
;             for (int ai = 0; ai < 2; ++ai)
; #pragma unroll
;                 for (int m = 0; m < 4; ++m) { const int rr = row0 + ai * HALF + m * 16; const size_t ro = (size_t)rr * pitch; float v[8]; const float rs = rsv[ai][m];
; #pragma unroll
;                     for (int j = 0; j < 8; ++j) v[j] = (float)__builtin_bit_cast(i32x4, acc[ai][bj][m][j >> 2])[j & 3] * (rs * csv[j]);
;                     if (cls != 0) {
; #pragma unroll
;                         for (int j = 0; j < 8; ++j) { if (cls == 1) v[j] *= sigmoidf_(v[j]); else v[j] = __builtin_amdgcn_rcpf(1.0f + __builtin_amdgcn_exp2f(v[j])); }
;                         if (cls == 2) {
; #pragma unroll
;                             for (int j = 0; j < 8; ++j) { const float l = lbv[j]; v[j] = __builtin_amdgcn_logf(l + (1.0f - l) * v[j]); } }
;                     }
;                     u32x4 w; w.x = pk2(v[0], v[1]); w.y = pk2(v[2], v[3]); w.z = pk2(v[4], v[5]); w.w = pk2(v[6], v[7]);
;                     *(u32x4*)(colp + ro) = w; }
	v_sub_f32_e32 v50, 1.0, v83
	v_fma_f32 v15, v50, v15, v83
	v_sub_f32_e32 v50, 1.0, v84
	v_fma_f32 v16, v50, v16, v84
	v_sub_f32_e32 v50, 1.0, v85
	v_fma_f32 v17, v50, v17, v85
	v_log_f32_e32 v10, v10
	v_log_f32_e32 v11, v11
	v_log_f32_e32 v12, v12
	v_log_f32_e32 v13, v13
	v_log_f32_e32 v14, v14
	v_log_f32_e32 v15, v15
	v_log_f32_e32 v16, v16
	v_log_f32_e32 v17, v17
	v_cvt_pk_bf16_f32 v2, v10, v11
	v_cvt_pk_bf16_f32 v3, v12, v13
	v_cvt_pk_bf16_f32 v4, v14, v15
	v_cvt_pk_bf16_f32 v5, v16, v17
	v_lshl_add_u64 v[6:7], v[122:123], 1, v[74:75]
	global_store_dwordx4 v[6:7], v[2:5], off
	v_mov_b32_e32 v8, v158
	v_mov_b32_e32 v9, v158
	v_cvt_f32_i32_e32 v3, v47
	v_cvt_f32_i32_e32 v2, v46
	v_cvt_f32_i32_e32 v5, v49
	v_cvt_f32_i32_e32 v4, v48
	v_pk_mul_f32 v[6:7], v[8:9], v[100:101]
	v_cvt_f32_i32_e32 v11, v45
	v_pk_mul_f32 v[2:3], v[6:7], v[2:3]
	v_pk_mul_f32 v[6:7], v[8:9], v[98:99]
	v_cvt_f32_i32_e32 v10, v44
	v_pk_mul_f32 v[4:5], v[6:7], v[4:5]
	v_cvt_f32_i32_e32 v7, v43
	v_cvt_f32_i32_e32 v6, v42
	v_pk_mul_f32 v[12:13], v[8:9], v[96:97]
	v_pk_mul_f32 v[8:9], v[8:9], v[94:95]
	v_pk_mul_f32 v[6:7], v[12:13], v[6:7]
	v_pk_mul_f32 v[8:9], v[8:9], v[10:11]
	v_exp_f32_e32 v10, v2
	v_exp_f32_e32 v11, v3
	v_add_f32_e32 v10, 1.0, v10
	v_rcp_f32_e32 v10, v10
	v_add_f32_e32 v11, 1.0, v11
	v_rcp_f32_e32 v11, v11
	v_exp_f32_e32 v12, v4
	v_exp_f32_e32 v13, v5
	v_add_f32_e32 v12, 1.0, v12
	v_rcp_f32_e32 v12, v12
	v_add_f32_e32 v13, 1.0, v13
	v_rcp_f32_e32 v13, v13
	v_exp_f32_e32 v14, v6
	v_exp_f32_e32 v15, v7
	v_add_f32_e32 v14, 1.0, v14
	v_rcp_f32_e32 v14, v14
	v_add_f32_e32 v15, 1.0, v15
	v_rcp_f32_e32 v15, v15
	v_exp_f32_e32 v16, v8
	v_exp_f32_e32 v17, v9
	v_add_f32_e32 v16, 1.0, v16
	v_rcp_f32_e32 v16, v16
	v_add_f32_e32 v17, 1.0, v17
	v_rcp_f32_e32 v17, v17
	v_sub_f32_e32 v42, 1.0, v86
	v_fma_f32 v10, v42, v10, v86
	v_sub_f32_e32 v42, 1.0, v87
	v_fma_f32 v11, v42, v11, v87
	v_sub_f32_e32 v42, 1.0, v88
	v_fma_f32 v12, v42, v12, v88
	v_sub_f32_e32 v42, 1.0, v89
	v_fma_f32 v13, v42, v13, v89
	v_sub_f32_e32 v42, 1.0, v82
	v_fma_f32 v14, v42, v14, v82
	v_sub_f32_e32 v42, 1.0, v83
	v_fma_f32 v15, v42, v15, v83
	v_sub_f32_e32 v42, 1.0, v84
	v_fma_f32 v16, v42, v16, v84
	v_sub_f32_e32 v42, 1.0, v85
	v_fma_f32 v17, v42, v17, v85
	v_log_f32_e32 v10, v10
	v_log_f32_e32 v11, v11
	v_log_f32_e32 v12, v12
	v_log_f32_e32 v13, v13
	v_log_f32_e32 v14, v14
	v_log_f32_e32 v15, v15
	v_log_f32_e32 v16, v16
	v_log_f32_e32 v17, v17
	v_cvt_pk_bf16_f32 v2, v10, v11
	v_cvt_pk_bf16_f32 v3, v12, v13
	v_cvt_pk_bf16_f32 v4, v14, v15
	v_cvt_pk_bf16_f32 v5, v16, v17
	v_lshl_add_u64 v[6:7], v[114:115], 1, v[74:75]
	global_store_dwordx4 v[6:7], v[2:5], off
	v_mov_b32_e32 v158, v159
	v_pk_mul_f32 v[6:7], v[158:159], v[100:101]
	v_cvt_f32_i32_e32 v3, v39
	v_cvt_f32_i32_e32 v2, v38
	v_cvt_f32_i32_e32 v5, v41
	v_cvt_f32_i32_e32 v4, v40
	v_cvt_f32_i32_e32 v9, v37
	v_pk_mul_f32 v[2:3], v[6:7], v[2:3]
	v_pk_mul_f32 v[6:7], v[158:159], v[98:99]
	v_cvt_f32_i32_e32 v8, v36
	v_pk_mul_f32 v[4:5], v[6:7], v[4:5]
	v_cvt_f32_i32_e32 v7, v35
	v_cvt_f32_i32_e32 v6, v34
	v_pk_mul_f32 v[10:11], v[158:159], v[96:97]
	v_pk_mul_f32 v[6:7], v[10:11], v[6:7]
	v_pk_mul_f32 v[10:11], v[158:159], v[94:95]
	v_pk_mul_f32 v[8:9], v[10:11], v[8:9]
	v_exp_f32_e32 v10, v2
	v_exp_f32_e32 v11, v3
	v_add_f32_e32 v10, 1.0, v10
	v_rcp_f32_e32 v10, v10
	v_add_f32_e32 v11, 1.0, v11
	v_rcp_f32_e32 v11, v11
	v_exp_f32_e32 v12, v4
	v_exp_f32_e32 v13, v5
	v_add_f32_e32 v12, 1.0, v12
	v_rcp_f32_e32 v12, v12
	v_add_f32_e32 v13, 1.0, v13
	v_rcp_f32_e32 v13, v13
	v_exp_f32_e32 v14, v6
	v_exp_f32_e32 v15, v7
	v_add_f32_e32 v14, 1.0, v14
	v_rcp_f32_e32 v14, v14
	v_add_f32_e32 v15, 1.0, v15
	v_rcp_f32_e32 v15, v15
	v_exp_f32_e32 v16, v8
	v_exp_f32_e32 v17, v9
	v_add_f32_e32 v16, 1.0, v16
	v_rcp_f32_e32 v16, v16
	v_add_f32_e32 v17, 1.0, v17
	v_rcp_f32_e32 v17, v17
	v_sub_f32_e32 v34, 1.0, v86
	v_fma_f32 v10, v34, v10, v86
	v_sub_f32_e32 v34, 1.0, v87
	v_fma_f32 v11, v34, v11, v87
	v_sub_f32_e32 v34, 1.0, v88
	v_fma_f32 v12, v34, v12, v88
	v_sub_f32_e32 v34, 1.0, v89
	v_fma_f32 v13, v34, v13, v89
	v_sub_f32_e32 v34, 1.0, v82
	v_fma_f32 v14, v34, v14, v82
	v_sub_f32_e32 v34, 1.0, v83
	v_fma_f32 v15, v34, v15, v83
	v_sub_f32_e32 v34, 1.0, v84
	v_fma_f32 v16, v34, v16, v84
	v_sub_f32_e32 v34, 1.0, v85
	v_fma_f32 v17, v34, v17, v85
	v_log_f32_e32 v10, v10
	v_log_f32_e32 v11, v11
	v_log_f32_e32 v12, v12
	v_log_f32_e32 v13, v13
	v_log_f32_e32 v14, v14
	v_log_f32_e32 v15, v15
	v_log_f32_e32 v16, v16
	v_log_f32_e32 v17, v17
	v_cvt_pk_bf16_f32 v2, v10, v11
	v_cvt_pk_bf16_f32 v3, v12, v13
	v_cvt_pk_bf16_f32 v4, v14, v15
	v_cvt_pk_bf16_f32 v5, v16, v17
	v_lshl_add_u64 v[6:7], v[102:103], 1, v[74:75]
	global_store_dwordx4 v[6:7], v[2:5], off
	v_mov_b32_e32 v8, v156
	v_mov_b32_e32 v9, v156
	v_cvt_f32_i32_e32 v3, v31
	v_cvt_f32_i32_e32 v2, v30
	v_cvt_f32_i32_e32 v5, v33
	v_cvt_f32_i32_e32 v4, v32
	v_pk_mul_f32 v[6:7], v[8:9], v[100:101]
	v_cvt_f32_i32_e32 v11, v29
	v_pk_mul_f32 v[2:3], v[6:7], v[2:3]
	v_pk_mul_f32 v[6:7], v[8:9], v[98:99]
	v_cvt_f32_i32_e32 v10, v28
	v_pk_mul_f32 v[4:5], v[6:7], v[4:5]
; #define LAS __attribute__((address_space(3)))
; DI unsigned pk2(float lo, float hi) { f32x2 v = {lo, hi}; bf16x2_t b = __builtin_convertvector(v, bf16x2_t); return __builtin_bit_cast(unsigned, b); }
; DI float sigmoidf_(float x) { return __builtin_amdgcn_rcpf(1.0f + __expf(-x)); }
;     DI void prefetch(const Unit& u, LAS unsigned char* slot, int wid, int lane) const {
;         if (wid != 0) return;
;         __builtin_amdgcn_global_load_lds((const unsigned*)(hrs + u.pm * BM + 4 * lane), (LAS unsigned*)slot, 16, 0, 0);
;         __builtin_amdgcn_global_load_lds((const unsigned*)(wcs + u.pn * BM + 4 * lane), (LAS unsigned*)(slot + 1024), 16, 0, 0);
;         if (u.pn >= 9 && u.pn < 17) __builtin_amdgcn_global_load_lds((const unsigned*)((u.pn < 13 ? lbf + (u.pn - 9) * BM : lbb + (u.pn - 13) * BM) + 4 * lane), (LAS unsigned*)(slot + 2048), 16, 0, 0);
;     }
;     DI void operator()(const f32x4 (&acc)[2][2][4][2], const Unit& u, int wr, int wc, int fr, int fq, const LAS unsigned char* slot) const {
;     ...
;             for (int ai = 0; ai < 2; ++ai)
; #pragma unroll
;                 for (int m = 0; m < 4; ++m) { const int rr = row0 + ai * HALF + m * 16; const size_t ro = (size_t)rr * pitch; float v[8]; const float rs = rsv[ai][m];
; #pragma unroll
;                     for (int j = 0; j < 8; ++j) v[j] = (float)__builtin_bit_cast(i32x4, acc[ai][bj][m][j >> 2])[j & 3] * (rs * csv[j]);
;                     if (cls != 0) {
; #pragma unroll
;                         for (int j = 0; j < 8; ++j) { if (cls == 1) v[j] *= sigmoidf_(v[j]); else v[j] = __builtin_amdgcn_rcpf(1.0f + __builtin_amdgcn_exp2f(v[j])); }
;                         if (cls == 2) {
; #pragma unroll
;                             for (int j = 0; j < 8; ++j) { const float l = lbv[j]; v[j] = __builtin_amdgcn_logf(l + (1.0f - l) * v[j]); } }
;                     }
;                     u32x4 w; w.x = pk2(v[0], v[1]); w.y = pk2(v[2], v[3]); w.z = pk2(v[4], v[5]); w.w = pk2(v[6], v[7]);
;                     *(u32x4*)(colp + ro) = w; }
	v_cvt_f32_i32_e32 v7, v27
	v_cvt_f32_i32_e32 v6, v26
	v_pk_mul_f32 v[12:13], v[8:9], v[96:97]
	v_pk_mul_f32 v[8:9], v[8:9], v[94:95]
	v_pk_mul_f32 v[6:7], v[12:13], v[6:7]
	v_pk_mul_f32 v[8:9], v[8:9], v[10:11]
	v_exp_f32_e32 v10, v2
	v_exp_f32_e32 v11, v3
	v_add_f32_e32 v10, 1.0, v10
	v_rcp_f32_e32 v10, v10
	v_add_f32_e32 v11, 1.0, v11
	v_rcp_f32_e32 v11, v11
	v_exp_f32_e32 v12, v4
	v_exp_f32_e32 v13, v5
	v_add_f32_e32 v12, 1.0, v12
	v_rcp_f32_e32 v12, v12
	v_add_f32_e32 v13, 1.0, v13
	v_rcp_f32_e32 v13, v13
	v_exp_f32_e32 v14, v6
	v_exp_f32_e32 v15, v7
	v_add_f32_e32 v14, 1.0, v14
	v_rcp_f32_e32 v14, v14
	v_add_f32_e32 v15, 1.0, v15
	v_rcp_f32_e32 v15, v15
	v_exp_f32_e32 v16, v8
	v_exp_f32_e32 v17, v9
	v_add_f32_e32 v16, 1.0, v16
	v_rcp_f32_e32 v16, v16
	v_add_f32_e32 v17, 1.0, v17
	v_rcp_f32_e32 v17, v17
	v_sub_f32_e32 v26, 1.0, v86
	v_fma_f32 v10, v26, v10, v86
	v_sub_f32_e32 v26, 1.0, v87
	v_fma_f32 v11, v26, v11, v87
	v_sub_f32_e32 v26, 1.0, v88
	v_fma_f32 v12, v26, v12, v88
	v_sub_f32_e32 v26, 1.0, v89
	v_fma_f32 v13, v26, v13, v89
	v_sub_f32_e32 v26, 1.0, v82
	v_fma_f32 v14, v26, v14, v82
	v_sub_f32_e32 v26, 1.0, v83
	v_fma_f32 v15, v26, v15, v83
	v_sub_f32_e32 v26, 1.0, v84
	v_fma_f32 v16, v26, v16, v84
	v_sub_f32_e32 v26, 1.0, v85
	v_fma_f32 v17, v26, v17, v85
	v_log_f32_e32 v10, v10
	v_log_f32_e32 v11, v11
	v_log_f32_e32 v12, v12
	v_log_f32_e32 v13, v13
	v_log_f32_e32 v14, v14
	v_log_f32_e32 v15, v15
	v_log_f32_e32 v16, v16
	v_log_f32_e32 v17, v17
	v_cvt_pk_bf16_f32 v2, v10, v11
	v_cvt_pk_bf16_f32 v3, v12, v13
	v_cvt_pk_bf16_f32 v4, v14, v15
	v_cvt_pk_bf16_f32 v5, v16, v17
	v_lshl_add_u64 v[6:7], v[90:91], 1, v[74:75]
	global_store_dwordx4 v[6:7], v[2:5], off
	v_mov_b32_e32 v156, v157
	v_pk_mul_f32 v[6:7], v[156:157], v[100:101]
	v_cvt_f32_i32_e32 v3, v23
	v_cvt_f32_i32_e32 v2, v22
	v_cvt_f32_i32_e32 v5, v25
	v_cvt_f32_i32_e32 v4, v24
	v_cvt_f32_i32_e32 v9, v21
	v_pk_mul_f32 v[2:3], v[6:7], v[2:3]
	v_pk_mul_f32 v[6:7], v[156:157], v[98:99]
	v_cvt_f32_i32_e32 v8, v20
	v_pk_mul_f32 v[4:5], v[6:7], v[4:5]
	v_cvt_f32_i32_e32 v7, v19
	v_cvt_f32_i32_e32 v6, v18
	v_pk_mul_f32 v[10:11], v[156:157], v[96:97]
	v_pk_mul_f32 v[6:7], v[10:11], v[6:7]
	v_pk_mul_f32 v[10:11], v[156:157], v[94:95]
	v_pk_mul_f32 v[8:9], v[10:11], v[8:9]
	v_exp_f32_e32 v10, v2
	v_exp_f32_e32 v11, v3
	v_add_f32_e32 v10, 1.0, v10
	v_rcp_f32_e32 v10, v10
	v_add_f32_e32 v11, 1.0, v11
	v_rcp_f32_e32 v11, v11
	v_exp_f32_e32 v12, v4
	v_exp_f32_e32 v13, v5
	v_add_f32_e32 v12, 1.0, v12
	v_rcp_f32_e32 v12, v12
	v_add_f32_e32 v13, 1.0, v13
	v_rcp_f32_e32 v13, v13
	v_exp_f32_e32 v14, v6
	v_exp_f32_e32 v15, v7
	v_add_f32_e32 v14, 1.0, v14
	v_rcp_f32_e32 v14, v14
	v_add_f32_e32 v15, 1.0, v15
	v_rcp_f32_e32 v15, v15
	s_mov_b64 s[34:35], -1
	v_exp_f32_e32 v16, v8
	s_mov_b64 s[6:7], -1
	v_add_f32_e32 v16, 1.0, v16
	v_rcp_f32_e32 v16, v16
	v_exp_f32_e32 v17, v9
	v_sub_f32_e32 v18, 1.0, v86
	v_add_f32_e32 v17, 1.0, v17
	v_rcp_f32_e32 v17, v17
	v_fma_f32 v10, v18, v10, v86
	v_sub_f32_e32 v18, 1.0, v87
	v_fma_f32 v11, v18, v11, v87
	v_sub_f32_e32 v18, 1.0, v88
	v_fma_f32 v12, v18, v12, v88
	v_sub_f32_e32 v18, 1.0, v89
	v_fmac_f32_e32 v89, v18, v13
	v_sub_f32_e32 v18, 1.0, v82
	v_fma_f32 v14, v18, v14, v82
	v_sub_f32_e32 v18, 1.0, v83
	v_fma_f32 v15, v18, v15, v83
	v_sub_f32_e32 v18, 1.0, v84
	v_fma_f32 v16, v18, v16, v84
	v_sub_f32_e32 v18, 1.0, v85
	v_fmac_f32_e32 v85, v18, v17
	v_log_f32_e32 v10, v10
	v_log_f32_e32 v11, v11
	v_log_f32_e32 v12, v12
	v_log_f32_e32 v13, v89
	v_log_f32_e32 v14, v14
	v_log_f32_e32 v15, v15
	v_log_f32_e32 v16, v16
	v_log_f32_e32 v17, v85
	s_mov_b64 s[36:37], 0
	v_cvt_pk_bf16_f32 v2, v10, v11
	v_cvt_pk_bf16_f32 v3, v12, v13
	v_cvt_pk_bf16_f32 v4, v14, v15
	v_cvt_pk_bf16_f32 v5, v16, v17
	v_lshl_add_u64 v[6:7], v[92:93], 1, v[74:75]
	s_and_b64 vcc, exec, s[4:5]
	s_mov_b64 s[4:5], -1
	global_store_dwordx4 v[6:7], v[2:5], off
.Lepj_join:
	s_cbranch_vccnz .LBB0_468
	s_andn2_b64 vcc, exec, s[8:9]
	s_add_i32 s90, s90, 1
	s_cbranch_vccnz .LBB0_864
	s_lshl_b32 s3, s90, 12
	s_lshl_b32 s4, s92, 8
	s_and_b32 s3, s3, 0x1000
	s_ashr_i32 s5, s4, 31
	s_add_i32 s3, s3, 0
	v_lshl_add_u64 v[2:3], s[4:5], 2, v[152:153]
	s_lshl_b32 s4, s91, 8
	s_add_i32 m0, s3, 0x21000
	s_ashr_i32 s5, s4, 31
	global_load_lds_dwordx4 v[2:3], off
	v_lshl_add_u64 v[2:3], s[4:5], 2, v[154:155]
	s_add_i32 m0, s3, 0x21400
	s_add_i32 s5, s91, -9
	global_load_lds_dwordx4 v[2:3], off
	s_cmp_gt_u32 s5, 7
	s_cbranch_scc1 .LBB0_864
	s_mov_b32 s5, s75
	s_lshl_b64 s[4:5], s[4:5], 2
	s_cmp_lt_u32 s91, 13
	s_cselect_b32 s7, s27, s61
	s_cselect_b32 s6, s59, s64
	s_cselect_b32 s30, s88, 0xffffcc00
	s_add_u32 s4, s7, s4
	s_addc_u32 s5, s6, s5
	s_add_u32 s4, s4, s30
	s_addc_u32 s5, s5, -1
	s_add_i32 m0, s3, 0x21800
	s_nop 0
	global_load_lds_dwordx4 v189, s[4:5]
.LBB0_864:
	s_andn2_b64 vcc, exec, s[12:13]
	s_cbranch_vccnz .LBB0_467
	s_barrier
	s_branch .LBB0_467
.LBB0_1120:
	s_mov_b64 s[42:43], 0x4510000
	s_mov_b64 s[36:37], 0x80
	s_mov_b32 s93, 7
	s_movk_i32 s3, 0xef00
	s_mov_b64 s[34:35], -1
	s_mov_b64 s[44:45], 0
	s_mov_b64 s[38:39], 0
	s_branch .LBB0_506
